# P0 transposes: streaming (nt) cache policy also on the converted-weight stores
# speedup vs baseline: 1.0126x; 1.0037x over previous
.LBB0_80:
	v_add_u32_e32 v132, 0x420, v154
	ds_write2_b32 v132, v128, v129 offset1:1
	v_add_u32_e32 v128, 0x428, v154
	s_mul_i32 s38, s38, s4
	ds_write2_b32 v128, v130, v131 offset1:1
	s_sub_i32 s0, s58, s38
	s_waitcnt lgkmcnt(0)
	s_lshl_b32 s2, s0, 6
	s_lshl_b64 s[0:1], s[36:37], 1
	s_add_u32 s0, s18, s0
	ds_read2_b32 v[132:133], v155 offset0:33 offset1:41
	ds_read2_b32 v[134:135], v155 offset1:8
	ds_read2_b32 v[168:169], v155 offset0:66 offset1:74
	ds_read2_b32 v[170:171], v155 offset0:99 offset1:107
	ds_read2_b32 v[172:173], v155 offset0:132 offset1:140
	ds_read2_b32 v[174:175], v155 offset0:165 offset1:173
	ds_read2_b32 v[176:177], v155 offset0:198 offset1:206
	ds_read2_b32 v[178:179], v155 offset0:231 offset1:239
	s_addc_u32 s1, s19, s1
	v_lshlrev_b32_e32 v138, 1, v140
	s_waitcnt lgkmcnt(6)
	s_nop 1
	v_cvt_pk_bf16_f32 v128, v134, v132
	v_or_b32_e32 v132, s2, v160
	v_lshl_add_u64 v[180:181], s[0:1], 0, v[138:139]
	v_mad_u64_u32 v[182:183], s[0:1], s20, v132, 0
	s_ashr_i32 s0, s2, 31
	v_mul_lo_u32 v134, s21, v132
	s_mul_i32 s3, s20, s0
	v_add3_u32 v183, v183, s3, v134
	v_lshl_add_u64 v[182:183], v[182:183], 1, v[180:181]
	v_or_b32_e32 v132, s2, v161
	s_waitcnt lgkmcnt(4)
	s_nop 1
	v_cvt_pk_bf16_f32 v129, v168, v170
	s_waitcnt lgkmcnt(2)
	s_nop 1
	v_cvt_pk_bf16_f32 v130, v172, v174
	s_waitcnt lgkmcnt(0)
	s_nop 1
	v_cvt_pk_bf16_f32 v131, v176, v178
	global_store_dwordx4 v[182:183], v[128:131], off nt
	v_mul_lo_u32 v134, s21, v132
	s_nop 0
	s_nop 1
	v_cvt_pk_bf16_f32 v128, v135, v133
	v_mad_u64_u32 v[132:133], s[0:1], s20, v132, 0
	v_add3_u32 v133, v133, s3, v134
	s_nop 1
	v_cvt_pk_bf16_f32 v129, v169, v171
	s_nop 1
	v_cvt_pk_bf16_f32 v130, v173, v175
	s_nop 1
	v_cvt_pk_bf16_f32 v131, v177, v179
	v_lshl_add_u64 v[132:133], v[132:133], 1, v[180:181]
	ds_read2_b32 v[134:135], v155 offset0:16 offset1:24
	ds_read2_b32 v[168:169], v155 offset0:49 offset1:57
	ds_read2_b32 v[170:171], v155 offset0:82 offset1:90
	ds_read2_b32 v[172:173], v155 offset0:115 offset1:123
	ds_read2_b32 v[174:175], v155 offset0:148 offset1:156
	ds_read2_b32 v[176:177], v155 offset0:181 offset1:189
	ds_read2_b32 v[178:179], v155 offset0:214 offset1:222
	ds_read2_b32 v[182:183], v155 offset0:247 offset1:255
	global_store_dwordx4 v[132:133], v[128:131], off nt
	v_or_b32_e32 v132, s2, v162
	s_waitcnt lgkmcnt(6)
	s_nop 1
	v_cvt_pk_bf16_f32 v128, v134, v168
	v_mul_lo_u32 v134, s21, v132
	v_mad_u64_u32 v[132:133], s[0:1], s20, v132, 0
	v_add3_u32 v133, v133, s3, v134
	v_lshl_add_u64 v[132:133], v[132:133], 1, v[180:181]
	s_waitcnt lgkmcnt(4)
	s_nop 1
	v_cvt_pk_bf16_f32 v129, v170, v172
	s_waitcnt lgkmcnt(2)
	s_nop 1
	v_cvt_pk_bf16_f32 v130, v174, v176
	s_waitcnt lgkmcnt(0)
	s_nop 1
	v_cvt_pk_bf16_f32 v131, v178, v182
	global_store_dwordx4 v[132:133], v[128:131], off nt
	v_or_b32_e32 v132, s2, v163
	v_mul_lo_u32 v134, s21, v132
	v_mad_u64_u32 v[132:133], s[0:1], s20, v132, 0
	v_add3_u32 v133, v133, s3, v134
	v_lshl_add_u64 v[132:133], v[132:133], 1, v[180:181]
	s_nop 1
	v_cvt_pk_bf16_f32 v128, v135, v169
	s_nop 1
	v_cvt_pk_bf16_f32 v129, v171, v173
	s_nop 1
	v_cvt_pk_bf16_f32 v130, v175, v177
	s_nop 1
	v_cvt_pk_bf16_f32 v131, v179, v183
	global_store_dwordx4 v[132:133], v[128:131], off nt
	s_waitcnt lgkmcnt(0)
	s_mov_b64 s[0:1], 0

.LBB0_94:
	s_cmp_ge_u32 s60, s4
	s_cselect_b32 s0, s61, s60
	s_sub_i32 s1, s0, s4
	s_cmp_ge_u32 s0, s4
	v_add_u32_e32 v132, 0x420, v154
	s_cselect_b32 s0, s1, s0
	ds_write2_b32 v132, v128, v129 offset1:1
	v_add_u32_e32 v128, 0x428, v154
	s_xor_b32 s0, s0, s59
	ds_write2_b32 v128, v130, v131 offset1:1
	s_sub_i32 s0, s0, s59
	s_waitcnt lgkmcnt(0)
	s_lshl_b32 s2, s0, 6
	s_lshl_b64 s[0:1], s[36:37], 1
	s_add_u32 s0, s18, s0
	ds_read2_b32 v[132:133], v155 offset0:33 offset1:41
	ds_read2_b32 v[134:135], v155 offset1:8
	ds_read2_b32 v[168:169], v155 offset0:66 offset1:74
	ds_read2_b32 v[170:171], v155 offset0:99 offset1:107
	ds_read2_b32 v[172:173], v155 offset0:132 offset1:140
	ds_read2_b32 v[174:175], v155 offset0:165 offset1:173
	ds_read2_b32 v[176:177], v155 offset0:198 offset1:206
	ds_read2_b32 v[178:179], v155 offset0:231 offset1:239
	s_addc_u32 s1, s19, s1
	v_lshlrev_b32_e32 v138, 1, v140
	s_waitcnt lgkmcnt(6)
	s_nop 1
	v_cvt_pk_bf16_f32 v128, v134, v132
	v_or_b32_e32 v132, s2, v156
	v_lshl_add_u64 v[180:181], s[0:1], 0, v[138:139]
	v_mad_u64_u32 v[182:183], s[0:1], s20, v132, 0
	s_ashr_i32 s0, s2, 31
	v_mul_lo_u32 v134, s21, v132
	s_mul_i32 s3, s20, s0
	v_add3_u32 v183, v183, s3, v134
	v_lshl_add_u64 v[182:183], v[182:183], 1, v[180:181]
	v_or_b32_e32 v132, s2, v157
	s_waitcnt lgkmcnt(4)
	s_nop 1
	v_cvt_pk_bf16_f32 v129, v168, v170
	s_waitcnt lgkmcnt(2)
	s_nop 1
	v_cvt_pk_bf16_f32 v130, v172, v174
	s_waitcnt lgkmcnt(0)
	s_nop 1
	v_cvt_pk_bf16_f32 v131, v176, v178
	global_store_dwordx4 v[182:183], v[128:131], off nt
	v_mul_lo_u32 v134, s21, v132
	s_nop 0
	s_nop 1
	v_cvt_pk_bf16_f32 v128, v135, v133
	v_mad_u64_u32 v[132:133], s[0:1], s20, v132, 0
	v_add3_u32 v133, v133, s3, v134
	s_nop 1
	v_cvt_pk_bf16_f32 v129, v169, v171
	s_nop 1
	v_cvt_pk_bf16_f32 v130, v173, v175
	s_nop 1
	v_cvt_pk_bf16_f32 v131, v177, v179
	v_lshl_add_u64 v[132:133], v[132:133], 1, v[180:181]
	ds_read2_b32 v[134:135], v155 offset0:16 offset1:24
	ds_read2_b32 v[168:169], v155 offset0:49 offset1:57
	ds_read2_b32 v[170:171], v155 offset0:82 offset1:90
	ds_read2_b32 v[172:173], v155 offset0:115 offset1:123
	ds_read2_b32 v[174:175], v155 offset0:148 offset1:156
	ds_read2_b32 v[176:177], v155 offset0:181 offset1:189
	ds_read2_b32 v[178:179], v155 offset0:214 offset1:222
	ds_read2_b32 v[182:183], v155 offset0:247 offset1:255
	global_store_dwordx4 v[132:133], v[128:131], off nt
	v_or_b32_e32 v132, s2, v158
	s_waitcnt lgkmcnt(6)
	s_nop 1
	v_cvt_pk_bf16_f32 v128, v134, v168
	v_mul_lo_u32 v134, s21, v132
	v_mad_u64_u32 v[132:133], s[0:1], s20, v132, 0
	v_add3_u32 v133, v133, s3, v134
	v_lshl_add_u64 v[132:133], v[132:133], 1, v[180:181]
	s_waitcnt lgkmcnt(4)
	s_nop 1
	v_cvt_pk_bf16_f32 v129, v170, v172
	s_waitcnt lgkmcnt(2)
	s_nop 1
	v_cvt_pk_bf16_f32 v130, v174, v176
	s_waitcnt lgkmcnt(0)
	s_nop 1
	v_cvt_pk_bf16_f32 v131, v178, v182
	global_store_dwordx4 v[132:133], v[128:131], off nt
	v_or_b32_e32 v132, s2, v159
	v_mul_lo_u32 v134, s21, v132
	v_mad_u64_u32 v[132:133], s[0:1], s20, v132, 0
	v_add3_u32 v133, v133, s3, v134
	v_lshl_add_u64 v[132:133], v[132:133], 1, v[180:181]
	s_nop 1
	v_cvt_pk_bf16_f32 v128, v135, v169
	s_nop 1
	v_cvt_pk_bf16_f32 v129, v171, v173
	s_nop 1
	v_cvt_pk_bf16_f32 v130, v175, v177
	s_nop 1
	v_cvt_pk_bf16_f32 v131, v179, v183
	global_store_dwordx4 v[132:133], v[128:131], off nt
	s_waitcnt lgkmcnt(0)
	s_mov_b64 s[0:1], 0

.LBB0_108:
	s_cmp_ge_u32 s60, s4
	s_cselect_b32 s0, s61, s60
	s_sub_i32 s1, s0, s4
	s_cmp_ge_u32 s0, s4
	s_cselect_b32 s0, s1, s0
	s_xor_b32 s0, s0, s59
	s_sub_i32 s0, s0, s59
	s_lshl_b32 s38, s0, 5
	v_add_u32_e32 v132, 0x420, v154
	s_cmpk_lt_u32 s38, 0xa00
	ds_write2_b32 v132, v128, v129 offset1:1
	v_add_u32_e32 v128, 0x428, v154
	s_cselect_b64 s[0:1], -1, 0
	s_cmpk_lt_u32 s38, 0xe00
	ds_write2_b32 v128, v130, v131 offset1:1
	s_cselect_b64 s[2:3], -1, 0
	s_waitcnt lgkmcnt(0)
	s_and_b64 s[2:3], s[2:3], exec
	ds_read2_b32 v[132:133], v155 offset0:33 offset1:41
	ds_read2_b32 v[134:135], v155 offset1:8
	ds_read2_b32 v[168:169], v155 offset0:66 offset1:74
	ds_read2_b32 v[170:171], v155 offset0:99 offset1:107
	ds_read2_b32 v[172:173], v155 offset0:132 offset1:140
	ds_read2_b32 v[174:175], v155 offset0:165 offset1:173
	ds_read2_b32 v[176:177], v155 offset0:198 offset1:206
	ds_read2_b32 v[178:179], v155 offset0:231 offset1:239
	s_cselect_b32 s2, s54, 0xfffffa00
	s_cselect_b32 s3, s31, s19
	s_cselect_b32 s39, s30, s18
	s_and_b64 s[0:1], s[0:1], exec
	s_waitcnt lgkmcnt(6)
	s_nop 1
	v_cvt_pk_bf16_f32 v128, v134, v132
	v_or_b32_e32 v132, s38, v136
	s_cselect_b32 s0, 0xfffffe00, s2
	v_mov_b32_e32 v184, s0
	v_cmp_gt_i32_e32 vcc, s52, v132
	s_cselect_b32 s1, s18, s39
	s_cselect_b32 s2, s19, s3
	v_cndmask_b32_e32 v134, v184, v165, vcc
	v_add_u32_e32 v132, v134, v132
	v_ashrrev_i32_e32 v134, 31, v132
	v_mov_b32_e32 v185, s2
	v_mov_b32_e32 v186, s31
	v_mov_b32_e32 v187, s1
	v_mov_b32_e32 v188, s30
	v_mul_lo_u32 v134, s20, v134
	v_mul_lo_u32 v138, s21, v132
	v_mad_u64_u32 v[182:183], s[0:1], s20, v132, 0
	v_cndmask_b32_e32 v181, v185, v186, vcc
	v_cndmask_b32_e32 v180, v187, v188, vcc
	v_add3_u32 v183, v183, v134, v138
	v_lshl_add_u64 v[180:181], v[182:183], 1, v[180:181]
	s_lshl_b64 s[0:1], s[36:37], 1
	v_lshl_add_u64 v[180:181], v[180:181], 0, s[0:1]
	v_lshlrev_b32_e32 v138, 1, v140
	v_or_b32_e32 v134, s38, v146
	v_lshl_add_u64 v[180:181], v[180:181], 0, v[138:139]
	v_cmp_gt_i32_e32 vcc, s52, v134
	s_waitcnt lgkmcnt(4)
	s_nop 1
	v_cvt_pk_bf16_f32 v129, v168, v170
	s_waitcnt lgkmcnt(2)
	s_nop 1
	v_cvt_pk_bf16_f32 v130, v172, v174
	s_waitcnt lgkmcnt(0)
	s_nop 1
	v_cvt_pk_bf16_f32 v131, v176, v178
	global_store_dwordx4 v[180:181], v[128:131], off nt
	v_cndmask_b32_e32 v132, v187, v188, vcc
	s_nop 0
	s_nop 1
	v_cvt_pk_bf16_f32 v128, v135, v133
	v_cndmask_b32_e32 v135, v184, v165, vcc
	v_add_u32_e32 v134, v135, v134
	v_ashrrev_i32_e32 v135, 31, v134
	s_nop 1
	v_cvt_pk_bf16_f32 v129, v169, v171
	v_mul_lo_u32 v168, s20, v135
	v_mul_lo_u32 v169, s21, v134
	v_mad_u64_u32 v[134:135], s[2:3], s20, v134, 0
	v_cndmask_b32_e32 v133, v185, v186, vcc
	v_add3_u32 v135, v135, v168, v169
	v_lshl_add_u64 v[132:133], v[134:135], 1, v[132:133]
	v_lshl_add_u64 v[132:133], v[132:133], 0, s[0:1]
	s_nop 1
	v_cvt_pk_bf16_f32 v130, v173, v175
	s_nop 1
	v_cvt_pk_bf16_f32 v131, v177, v179
	v_lshl_add_u64 v[132:133], v[132:133], 0, v[138:139]
	ds_read2_b32 v[134:135], v155 offset0:16 offset1:24
	ds_read2_b32 v[168:169], v155 offset0:49 offset1:57
	ds_read2_b32 v[170:171], v155 offset0:82 offset1:90
	ds_read2_b32 v[172:173], v155 offset0:115 offset1:123
	ds_read2_b32 v[174:175], v155 offset0:148 offset1:156
	ds_read2_b32 v[176:177], v155 offset0:181 offset1:189
	ds_read2_b32 v[178:179], v155 offset0:214 offset1:222
	ds_read2_b32 v[180:181], v155 offset0:247 offset1:255
	global_store_dwordx4 v[132:133], v[128:131], off nt
	s_waitcnt lgkmcnt(6)
	s_nop 0
	s_nop 1
	v_cvt_pk_bf16_f32 v128, v134, v168
	v_or_b32_e32 v134, s38, v148
	v_cmp_gt_i32_e32 vcc, s52, v134
	s_waitcnt lgkmcnt(4)
	s_nop 1
	v_cvt_pk_bf16_f32 v129, v170, v172
	s_waitcnt lgkmcnt(2)
	s_nop 1
	v_cvt_pk_bf16_f32 v130, v174, v176
	s_waitcnt lgkmcnt(0)
	s_nop 1
	v_cvt_pk_bf16_f32 v131, v178, v180
	v_cndmask_b32_e32 v168, v184, v165, vcc
	v_add_u32_e32 v134, v168, v134
	v_ashrrev_i32_e32 v168, 31, v134
	v_mul_lo_u32 v168, s20, v168
	v_mul_lo_u32 v170, s21, v134
	v_mad_u64_u32 v[182:183], s[2:3], s20, v134, 0
	v_cndmask_b32_e32 v133, v185, v186, vcc
	v_cndmask_b32_e32 v132, v187, v188, vcc
	v_add3_u32 v183, v183, v168, v170
	v_lshl_add_u64 v[132:133], v[182:183], 1, v[132:133]
	v_lshl_add_u64 v[132:133], v[132:133], 0, s[0:1]
	v_or_b32_e32 v134, s38, v150
	v_lshl_add_u64 v[132:133], v[132:133], 0, v[138:139]
	v_cmp_gt_i32_e32 vcc, s52, v134
	global_store_dwordx4 v[132:133], v[128:131], off nt
	s_nop 0
	v_cndmask_b32_e32 v133, v185, v186, vcc
	s_nop 1
	v_cvt_pk_bf16_f32 v128, v135, v169
	v_cndmask_b32_e32 v135, v184, v165, vcc
	v_add_u32_e32 v134, v135, v134
	v_ashrrev_i32_e32 v135, 31, v134
	v_mul_lo_u32 v168, s20, v135
	v_mul_lo_u32 v169, s21, v134
	v_mad_u64_u32 v[134:135], s[2:3], s20, v134, 0
	v_cndmask_b32_e32 v132, v187, v188, vcc
	v_add3_u32 v135, v135, v168, v169
	v_lshl_add_u64 v[132:133], v[134:135], 1, v[132:133]
	v_lshl_add_u64 v[132:133], v[132:133], 0, s[0:1]
	v_lshl_add_u64 v[132:133], v[132:133], 0, v[138:139]
	s_nop 1
	v_cvt_pk_bf16_f32 v129, v171, v173
	s_nop 1
	v_cvt_pk_bf16_f32 v130, v175, v177
	s_nop 1
	v_cvt_pk_bf16_f32 v131, v179, v181
	global_store_dwordx4 v[132:133], v[128:131], off nt
	s_waitcnt lgkmcnt(0)

.LBB0_123:
	s_cmp_ge_u32 s60, s4
	s_cselect_b32 s0, s61, s60
	s_sub_i32 s1, s0, s4
	s_cmp_ge_u32 s0, s4
	s_cselect_b32 s0, s1, s0
	s_xor_b32 s0, s0, s59
	v_add_u32_e32 v132, 0x420, v154
	s_sub_i32 s0, s0, s59
	ds_write2_b32 v132, v128, v129 offset1:1
	v_add_u32_e32 v128, 0x428, v154
	s_lshl_b32 s2, s0, 5
	s_lshl_b64 s[0:1], s[28:29], 1
	ds_write2_b32 v128, v130, v131 offset1:1
	s_add_u32 s3, s18, s0
	s_waitcnt lgkmcnt(0)
	s_addc_u32 s38, s19, s1
	s_lshl_b64 s[0:1], s[36:37], 1
	s_add_u32 s0, s3, s0
	ds_read2_b32 v[132:133], v155 offset0:33 offset1:41
	ds_read2_b32 v[134:135], v155 offset1:8
	ds_read2_b32 v[168:169], v155 offset0:66 offset1:74
	ds_read2_b32 v[170:171], v155 offset0:99 offset1:107
	ds_read2_b32 v[172:173], v155 offset0:132 offset1:140
	ds_read2_b32 v[174:175], v155 offset0:165 offset1:173
	ds_read2_b32 v[176:177], v155 offset0:198 offset1:206
	ds_read2_b32 v[178:179], v155 offset0:231 offset1:239
	s_addc_u32 s1, s38, s1
	v_lshlrev_b32_e32 v138, 1, v140
	s_waitcnt lgkmcnt(6)
	s_nop 1
	v_cvt_pk_bf16_f32 v128, v134, v132
	v_or_b32_e32 v132, s2, v136
	v_lshl_add_u64 v[180:181], s[0:1], 0, v[138:139]
	v_mad_u64_u32 v[182:183], s[0:1], s26, v132, 0
	s_ashr_i32 s0, s2, 31
	v_mul_lo_u32 v134, s27, v132
	s_mul_i32 s3, s26, s0
	v_add3_u32 v183, v183, s3, v134
	v_lshl_add_u64 v[182:183], v[182:183], 1, v[180:181]
	v_or_b32_e32 v132, s2, v146
	s_waitcnt lgkmcnt(4)
	s_nop 1
	v_cvt_pk_bf16_f32 v129, v168, v170
	s_waitcnt lgkmcnt(2)
	s_nop 1
	v_cvt_pk_bf16_f32 v130, v172, v174
	s_waitcnt lgkmcnt(0)
	s_nop 1
	v_cvt_pk_bf16_f32 v131, v176, v178
	global_store_dwordx4 v[182:183], v[128:131], off nt
	v_mul_lo_u32 v134, s27, v132
	s_nop 0
	s_nop 1
	v_cvt_pk_bf16_f32 v128, v135, v133
	v_mad_u64_u32 v[132:133], s[0:1], s26, v132, 0
	v_add3_u32 v133, v133, s3, v134
	s_nop 1
	v_cvt_pk_bf16_f32 v129, v169, v171
	s_nop 1
	v_cvt_pk_bf16_f32 v130, v173, v175
	s_nop 1
	v_cvt_pk_bf16_f32 v131, v177, v179
	v_lshl_add_u64 v[132:133], v[132:133], 1, v[180:181]
	ds_read2_b32 v[134:135], v155 offset0:16 offset1:24
	ds_read2_b32 v[168:169], v155 offset0:49 offset1:57
	ds_read2_b32 v[170:171], v155 offset0:82 offset1:90
	ds_read2_b32 v[172:173], v155 offset0:115 offset1:123
	ds_read2_b32 v[174:175], v155 offset0:148 offset1:156
	ds_read2_b32 v[176:177], v155 offset0:181 offset1:189
	ds_read2_b32 v[178:179], v155 offset0:214 offset1:222
	ds_read2_b32 v[182:183], v155 offset0:247 offset1:255
	global_store_dwordx4 v[132:133], v[128:131], off nt
	v_or_b32_e32 v132, s2, v148
	s_waitcnt lgkmcnt(6)
	s_nop 1
	v_cvt_pk_bf16_f32 v128, v134, v168
	v_mul_lo_u32 v134, s27, v132
	v_mad_u64_u32 v[132:133], s[0:1], s26, v132, 0
	v_add3_u32 v133, v133, s3, v134
	v_lshl_add_u64 v[132:133], v[132:133], 1, v[180:181]
	s_waitcnt lgkmcnt(4)
	s_nop 1
	v_cvt_pk_bf16_f32 v129, v170, v172
	s_waitcnt lgkmcnt(2)
	s_nop 1
	v_cvt_pk_bf16_f32 v130, v174, v176
	s_waitcnt lgkmcnt(0)
	s_nop 1
	v_cvt_pk_bf16_f32 v131, v178, v182
	global_store_dwordx4 v[132:133], v[128:131], off nt
	v_or_b32_e32 v132, s2, v150
	v_mul_lo_u32 v134, s27, v132
	v_mad_u64_u32 v[132:133], s[0:1], s26, v132, 0
	v_add3_u32 v133, v133, s3, v134
	v_lshl_add_u64 v[132:133], v[132:133], 1, v[180:181]
	s_nop 1
	v_cvt_pk_bf16_f32 v128, v135, v169
	s_nop 1
	v_cvt_pk_bf16_f32 v129, v171, v173
	s_nop 1
	v_cvt_pk_bf16_f32 v130, v175, v177
	s_nop 1
	v_cvt_pk_bf16_f32 v131, v179, v183
	global_store_dwordx4 v[132:133], v[128:131], off nt
	s_waitcnt lgkmcnt(0)

.LBB0_146:
	v_add_u32_e32 v128, 0x420, v154
	ds_write2_b32 v128, v132, v133 offset1:1
	v_add_u32_e32 v128, 0x428, v154
	s_cmp_ge_u32 s60, s4
	ds_write2_b32 v128, v134, v135 offset1:1
	s_cselect_b32 s0, s61, s60
	s_sub_i32 s1, s0, s4
	s_waitcnt lgkmcnt(0)
	s_cmp_ge_u32 s0, s4
	ds_read2_b32 v[128:129], v155 offset0:33 offset1:41
	ds_read2_b32 v[130:131], v155 offset1:8
	s_cselect_b32 s0, s1, s0
	s_xor_b32 s0, s0, s59
	s_sub_i32 s0, s0, s59
	ds_read2_b32 v[134:135], v155 offset0:66 offset1:74
	ds_read2_b32 v[168:169], v155 offset0:132 offset1:140
	ds_read2_b32 v[170:171], v155 offset0:165 offset1:173
	ds_read2_b32 v[172:173], v155 offset0:99 offset1:107
	s_lshl_b32 s2, s0, 5
	v_mov_b32_e32 v132, 0
	s_waitcnt lgkmcnt(4)
	v_cvt_pk_fp8_f32 v132, v130, v128
	v_or_b32_e32 v128, s2, v136
	v_mov_b32_e32 v133, 0
	ds_read2_b32 v[174:175], v155 offset0:198 offset1:206
	ds_read2_b32 v[176:177], v155 offset0:231 offset1:239
	v_cmp_gt_i32_e32 vcc, s53, v128
	s_add_u32 s0, s18, s36
	s_waitcnt lgkmcnt(3)
	v_cvt_pk_fp8_f32 v133, v168, v170
	v_cndmask_b32_e32 v130, v166, v167, vcc
	s_addc_u32 s1, s19, s37
	v_add_u32_e32 v128, v130, v128
	v_lshl_add_u64 v[178:179], s[0:1], 0, v[140:141]
	v_ashrrev_i32_e32 v130, 31, v128
	s_waitcnt lgkmcnt(2)
	v_cvt_pk_fp8_f32 v132, v134, v172 op_sel:[0,0,1]
	v_mul_lo_u32 v130, s20, v130
	v_mul_lo_u32 v134, s21, v128
	v_mad_u64_u32 v[180:181], s[0:1], s20, v128, v[178:179]
	s_waitcnt lgkmcnt(0)
	v_cvt_pk_fp8_f32 v133, v174, v176 op_sel:[0,0,1]
	v_mov_b32_e32 v128, 0
	v_add3_u32 v181, v134, v181, v130
	v_or_b32_e32 v130, s2, v146
	v_cvt_pk_fp8_f32 v128, v131, v129
	v_mov_b32_e32 v129, 0
	v_cmp_gt_i32_e32 vcc, s53, v130
	v_cvt_pk_fp8_f32 v129, v169, v171
	global_store_dwordx2 v[180:181], v[132:133], off nt
	v_cndmask_b32_e32 v131, v166, v167, vcc
	v_add_u32_e32 v134, v131, v130
	v_ashrrev_i32_e32 v130, 31, v134
	v_mul_lo_u32 v138, s20, v130
	ds_read2_b32 v[130:131], v155 offset0:16 offset1:24
	ds_read2_b32 v[132:133], v155 offset0:49 offset1:57
	v_cvt_pk_fp8_f32 v128, v135, v173 op_sel:[0,0,1]
	v_cvt_pk_fp8_f32 v129, v175, v177 op_sel:[0,0,1]
	ds_read2_b32 v[170:171], v155 offset0:82 offset1:90
	ds_read2_b32 v[172:173], v155 offset0:148 offset1:156
	ds_read2_b32 v[174:175], v155 offset0:181 offset1:189
	ds_read2_b32 v[176:177], v155 offset0:115 offset1:123
	v_mul_lo_u32 v184, s21, v134
	v_mad_u64_u32 v[134:135], s[0:1], s20, v134, v[178:179]
	v_mov_b32_e32 v168, 0
	v_mov_b32_e32 v169, 0
	ds_read2_b32 v[180:181], v155 offset0:214 offset1:222
	ds_read2_b32 v[182:183], v155 offset0:247 offset1:255
	s_waitcnt lgkmcnt(6)
	v_cvt_pk_fp8_f32 v168, v130, v132
	s_waitcnt lgkmcnt(3)
	v_cvt_pk_fp8_f32 v169, v172, v174
	v_add3_u32 v135, v184, v135, v138
	global_store_dwordx2 v[134:135], v[128:129], off nt
	v_or_b32_e32 v128, s2, v148
	v_cmp_gt_i32_e32 vcc, s53, v128
	s_waitcnt lgkmcnt(2)
	v_cvt_pk_fp8_f32 v168, v170, v176 op_sel:[0,0,1]
	s_waitcnt lgkmcnt(0)
	v_cvt_pk_fp8_f32 v169, v180, v182 op_sel:[0,0,1]
	v_cndmask_b32_e32 v129, v166, v167, vcc
	v_add_u32_e32 v128, v129, v128
	v_ashrrev_i32_e32 v129, 31, v128
	v_mov_b32_e32 v130, 0
	v_mul_lo_u32 v132, s20, v129
	v_mul_lo_u32 v134, s21, v128
	v_mad_u64_u32 v[128:129], s[0:1], s20, v128, v[178:179]
	v_cvt_pk_fp8_f32 v130, v131, v133
	v_mov_b32_e32 v131, 0
	v_cvt_pk_fp8_f32 v131, v173, v175
	v_add3_u32 v129, v134, v129, v132
	global_store_dwordx2 v[128:129], v[168:169], off nt
	v_or_b32_e32 v128, s2, v150
	v_cmp_gt_i32_e32 vcc, s53, v128
	v_cvt_pk_fp8_f32 v130, v171, v177 op_sel:[0,0,1]
	v_cvt_pk_fp8_f32 v131, v181, v183 op_sel:[0,0,1]
	v_cndmask_b32_e32 v129, v166, v167, vcc
	v_add_u32_e32 v128, v129, v128
	v_ashrrev_i32_e32 v129, 31, v128
	v_mul_lo_u32 v132, s20, v129
	v_mul_lo_u32 v133, s21, v128
	v_mad_u64_u32 v[128:129], s[0:1], s20, v128, v[178:179]
	v_add3_u32 v129, v133, v129, v132
	global_store_dwordx2 v[128:129], v[130:131], off nt
	s_waitcnt lgkmcnt(0)
	s_mov_b64 s[0:1], 0

.LBB0_165:
	v_add_u32_e32 v128, 0x420, v154
	ds_write2_b32 v128, v132, v133 offset1:1
	v_add_u32_e32 v128, 0x428, v154
	s_cmp_ge_u32 s60, s4
	ds_write2_b32 v128, v134, v135 offset1:1
	s_cselect_b32 s0, s61, s60
	s_sub_i32 s1, s0, s4
	s_waitcnt lgkmcnt(0)
	s_cmp_ge_u32 s0, s4
	ds_read2_b32 v[128:129], v155 offset0:33 offset1:41
	ds_read2_b32 v[130:131], v155 offset1:8
	s_cselect_b32 s0, s1, s0
	ds_read2_b32 v[134:135], v155 offset0:66 offset1:74
	ds_read2_b32 v[168:169], v155 offset0:132 offset1:140
	ds_read2_b32 v[170:171], v155 offset0:165 offset1:173
	ds_read2_b32 v[172:173], v155 offset0:99 offset1:107
	s_xor_b32 s0, s0, s59
	s_sub_i32 s0, s0, s59
	s_lshl_b32 s0, s0, 5
	v_mov_b32_e32 v132, 0
	v_mov_b32_e32 v133, 0
	ds_read2_b32 v[174:175], v155 offset0:198 offset1:206
	ds_read2_b32 v[176:177], v155 offset0:231 offset1:239
	s_add_i32 s2, s0, 0xfffff600
	s_waitcnt lgkmcnt(6)
	v_cvt_pk_fp8_f32 v132, v130, v128
	s_waitcnt lgkmcnt(3)
	v_cvt_pk_fp8_f32 v133, v168, v170
	s_add_u32 s0, s18, s36
	s_addc_u32 s1, s19, s37
	v_lshl_add_u64 v[178:179], s[0:1], 0, v[140:141]
	v_or_b32_e32 v128, s2, v136
	s_waitcnt lgkmcnt(2)
	v_cvt_pk_fp8_f32 v132, v134, v172 op_sel:[0,0,1]
	s_waitcnt lgkmcnt(0)
	v_cvt_pk_fp8_f32 v133, v174, v176 op_sel:[0,0,1]
	v_mul_lo_u32 v130, s21, v128
	v_mad_u64_u32 v[180:181], s[0:1], s20, v128, v[178:179]
	v_mov_b32_e32 v128, 0
	s_ashr_i32 s0, s2, 31
	v_cvt_pk_fp8_f32 v128, v131, v129
	v_mov_b32_e32 v129, 0
	s_mul_i32 s3, s20, s0
	v_cvt_pk_fp8_f32 v129, v169, v171
	v_add3_u32 v181, v130, v181, s3
	global_store_dwordx2 v[180:181], v[132:133], off nt
	ds_read2_b32 v[130:131], v155 offset0:16 offset1:24
	ds_read2_b32 v[132:133], v155 offset0:49 offset1:57
	v_cvt_pk_fp8_f32 v128, v135, v173 op_sel:[0,0,1]
	v_cvt_pk_fp8_f32 v129, v175, v177 op_sel:[0,0,1]
	ds_read2_b32 v[170:171], v155 offset0:82 offset1:90
	ds_read2_b32 v[172:173], v155 offset0:148 offset1:156
	ds_read2_b32 v[174:175], v155 offset0:181 offset1:189
	ds_read2_b32 v[176:177], v155 offset0:115 offset1:123
	v_mov_b32_e32 v168, 0
	v_mov_b32_e32 v169, 0
	ds_read2_b32 v[180:181], v155 offset0:214 offset1:222
	ds_read2_b32 v[182:183], v155 offset0:247 offset1:255
	s_waitcnt lgkmcnt(6)
	v_cvt_pk_fp8_f32 v168, v130, v132
	s_waitcnt lgkmcnt(3)
	v_cvt_pk_fp8_f32 v169, v172, v174
	v_mov_b32_e32 v130, 0
	v_or_b32_e32 v134, s2, v146
	v_cvt_pk_fp8_f32 v130, v131, v133
	v_mov_b32_e32 v131, 0
	v_mul_lo_u32 v138, s21, v134
	v_mad_u64_u32 v[134:135], s[0:1], s20, v134, v[178:179]
	v_cvt_pk_fp8_f32 v131, v173, v175
	v_add3_u32 v135, v138, v135, s3
	s_waitcnt lgkmcnt(2)
	v_cvt_pk_fp8_f32 v168, v170, v176 op_sel:[0,0,1]
	s_waitcnt lgkmcnt(0)
	v_cvt_pk_fp8_f32 v169, v180, v182 op_sel:[0,0,1]
	global_store_dwordx2 v[134:135], v[128:129], off nt
	v_or_b32_e32 v128, s2, v148
	v_mul_lo_u32 v132, s21, v128
	v_mad_u64_u32 v[128:129], s[0:1], s20, v128, v[178:179]
	v_add3_u32 v129, v132, v129, s3
	v_cvt_pk_fp8_f32 v130, v171, v177 op_sel:[0,0,1]
	v_cvt_pk_fp8_f32 v131, v181, v183 op_sel:[0,0,1]
	global_store_dwordx2 v[128:129], v[168:169], off nt
	v_or_b32_e32 v128, s2, v150
	v_mul_lo_u32 v132, s21, v128
	v_mad_u64_u32 v[128:129], s[0:1], s20, v128, v[178:179]
	v_add3_u32 v129, v132, v129, s3
	global_store_dwordx2 v[128:129], v[130:131], off nt
	s_waitcnt lgkmcnt(0)

.LBB0_185:
	v_add_u32_e32 v128, 0x420, v154
	ds_write2_b32 v128, v132, v133 offset1:1
	v_add_u32_e32 v128, 0x428, v154
	s_cmp_ge_u32 s60, s4
	ds_write2_b32 v128, v134, v135 offset1:1
	s_cselect_b32 s0, s61, s60
	s_sub_i32 s1, s0, s4
	s_waitcnt lgkmcnt(0)
	s_cmp_ge_u32 s0, s4
	ds_read2_b32 v[128:129], v155 offset0:33 offset1:41
	ds_read2_b32 v[130:131], v155 offset1:8
	s_cselect_b32 s0, s1, s0
	ds_read2_b32 v[134:135], v155 offset0:66 offset1:74
	ds_read2_b32 v[168:169], v155 offset0:132 offset1:140
	ds_read2_b32 v[170:171], v155 offset0:165 offset1:173
	ds_read2_b32 v[172:173], v155 offset0:99 offset1:107
	s_xor_b32 s0, s0, s59
	s_sub_i32 s0, s0, s59
	s_lshl_b32 s0, s0, 5
	v_mov_b32_e32 v132, 0
	v_mov_b32_e32 v133, 0
	ds_read2_b32 v[174:175], v155 offset0:198 offset1:206
	ds_read2_b32 v[176:177], v155 offset0:231 offset1:239
	s_add_i32 s2, s0, 0xfffff000
	s_waitcnt lgkmcnt(6)
	v_cvt_pk_fp8_f32 v132, v130, v128
	s_waitcnt lgkmcnt(3)
	v_cvt_pk_fp8_f32 v133, v168, v170
	s_add_u32 s0, s18, s36
	s_addc_u32 s1, s19, s37
	v_lshl_add_u64 v[178:179], s[0:1], 0, v[140:141]
	v_or_b32_e32 v128, s2, v136
	s_waitcnt lgkmcnt(2)
	v_cvt_pk_fp8_f32 v132, v134, v172 op_sel:[0,0,1]
	s_waitcnt lgkmcnt(0)
	v_cvt_pk_fp8_f32 v133, v174, v176 op_sel:[0,0,1]
	v_mul_lo_u32 v130, s21, v128
	v_mad_u64_u32 v[180:181], s[0:1], s20, v128, v[178:179]
	v_mov_b32_e32 v128, 0
	s_ashr_i32 s0, s2, 31
	v_cvt_pk_fp8_f32 v128, v131, v129
	v_mov_b32_e32 v129, 0
	s_mul_i32 s3, s20, s0
	v_cvt_pk_fp8_f32 v129, v169, v171
	v_add3_u32 v181, v130, v181, s3
	global_store_dwordx2 v[180:181], v[132:133], off nt
	ds_read2_b32 v[130:131], v155 offset0:16 offset1:24
	ds_read2_b32 v[132:133], v155 offset0:49 offset1:57
	v_cvt_pk_fp8_f32 v128, v135, v173 op_sel:[0,0,1]
	v_cvt_pk_fp8_f32 v129, v175, v177 op_sel:[0,0,1]
	ds_read2_b32 v[170:171], v155 offset0:82 offset1:90
	ds_read2_b32 v[172:173], v155 offset0:148 offset1:156
	ds_read2_b32 v[174:175], v155 offset0:181 offset1:189
	ds_read2_b32 v[176:177], v155 offset0:115 offset1:123
	v_mov_b32_e32 v168, 0
	v_mov_b32_e32 v169, 0
	ds_read2_b32 v[180:181], v155 offset0:214 offset1:222
	ds_read2_b32 v[182:183], v155 offset0:247 offset1:255
	s_waitcnt lgkmcnt(6)
	v_cvt_pk_fp8_f32 v168, v130, v132
	s_waitcnt lgkmcnt(3)
	v_cvt_pk_fp8_f32 v169, v172, v174
	v_mov_b32_e32 v130, 0
	v_or_b32_e32 v134, s2, v146
	v_cvt_pk_fp8_f32 v130, v131, v133
	v_mov_b32_e32 v131, 0
	v_mul_lo_u32 v138, s21, v134
	v_mad_u64_u32 v[134:135], s[0:1], s20, v134, v[178:179]
	v_cvt_pk_fp8_f32 v131, v173, v175
	v_add3_u32 v135, v138, v135, s3
	s_waitcnt lgkmcnt(2)
	v_cvt_pk_fp8_f32 v168, v170, v176 op_sel:[0,0,1]
	s_waitcnt lgkmcnt(0)
	v_cvt_pk_fp8_f32 v169, v180, v182 op_sel:[0,0,1]
	global_store_dwordx2 v[134:135], v[128:129], off nt
	v_or_b32_e32 v128, s2, v148
	v_mul_lo_u32 v132, s21, v128
	v_mad_u64_u32 v[128:129], s[0:1], s20, v128, v[178:179]
	v_add3_u32 v129, v132, v129, s3
	v_cvt_pk_fp8_f32 v130, v171, v177 op_sel:[0,0,1]
	v_cvt_pk_fp8_f32 v131, v181, v183 op_sel:[0,0,1]
	global_store_dwordx2 v[128:129], v[168:169], off nt
	v_or_b32_e32 v128, s2, v150
	v_mul_lo_u32 v132, s21, v128
	v_mad_u64_u32 v[128:129], s[0:1], s20, v128, v[178:179]
	v_add3_u32 v129, v132, v129, s3
	global_store_dwordx2 v[128:129], v[130:131], off nt
	s_waitcnt lgkmcnt(0)

.LBB0_211:
	v_add_u32_e32 v128, 0x420, v154
	ds_write2_b32 v128, v132, v133 offset1:1
	v_add_u32_e32 v128, 0x428, v154
	ds_write2_b32 v128, v134, v135 offset1:1
	s_cmp_ge_u32 s60, s4
	s_cselect_b32 s2, s61, s60
	s_waitcnt lgkmcnt(0)
	s_sub_i32 s3, s2, s4
	ds_read2_b32 v[128:129], v155 offset0:33 offset1:41
	ds_read2_b32 v[130:131], v155 offset1:8
	s_cmp_ge_u32 s2, s4
	ds_read2_b32 v[134:135], v155 offset0:66 offset1:74
	ds_read2_b32 v[168:169], v155 offset0:132 offset1:140
	ds_read2_b32 v[170:171], v155 offset0:165 offset1:173
	ds_read2_b32 v[172:173], v155 offset0:99 offset1:107
	s_cselect_b32 s2, s3, s2
	s_xor_b32 s2, s2, s59
	s_sub_i32 s2, s2, s59
	v_mov_b32_e32 v132, 0
	v_mov_b32_e32 v133, 0
	ds_read2_b32 v[174:175], v155 offset0:198 offset1:206
	ds_read2_b32 v[176:177], v155 offset0:231 offset1:239
	s_lshl_b32 s38, s2, 6
	s_waitcnt lgkmcnt(6)
	v_cvt_pk_fp8_f32 v132, v130, v128
	s_waitcnt lgkmcnt(3)
	v_cvt_pk_fp8_f32 v133, v168, v170
	s_add_u32 s2, s18, s36
	s_addc_u32 s3, s19, s37
	v_lshl_add_u64 v[178:179], s[2:3], 0, v[140:141]
	v_or_b32_e32 v128, s38, v156
	s_waitcnt lgkmcnt(2)
	v_cvt_pk_fp8_f32 v132, v134, v172 op_sel:[0,0,1]
	s_waitcnt lgkmcnt(0)
	v_cvt_pk_fp8_f32 v133, v174, v176 op_sel:[0,0,1]
	v_mul_lo_u32 v130, s21, v128
	v_mad_u64_u32 v[180:181], s[2:3], s20, v128, v[178:179]
	v_mov_b32_e32 v128, 0
	s_ashr_i32 s2, s38, 31
	v_cvt_pk_fp8_f32 v128, v131, v129
	v_mov_b32_e32 v129, 0
	s_mul_i32 s37, s20, s2
	v_cvt_pk_fp8_f32 v129, v169, v171
	v_add3_u32 v181, v130, v181, s37
	global_store_dwordx2 v[180:181], v[132:133], off nt
	ds_read2_b32 v[130:131], v155 offset0:16 offset1:24
	ds_read2_b32 v[132:133], v155 offset0:49 offset1:57
	v_cvt_pk_fp8_f32 v128, v135, v173 op_sel:[0,0,1]
	v_cvt_pk_fp8_f32 v129, v175, v177 op_sel:[0,0,1]
	ds_read2_b32 v[170:171], v155 offset0:82 offset1:90
	ds_read2_b32 v[172:173], v155 offset0:148 offset1:156
	ds_read2_b32 v[174:175], v155 offset0:181 offset1:189
	ds_read2_b32 v[176:177], v155 offset0:115 offset1:123
	v_mov_b32_e32 v168, 0
	v_mov_b32_e32 v169, 0
	ds_read2_b32 v[180:181], v155 offset0:214 offset1:222
	ds_read2_b32 v[182:183], v155 offset0:247 offset1:255
	s_waitcnt lgkmcnt(6)
	v_cvt_pk_fp8_f32 v168, v130, v132
	s_waitcnt lgkmcnt(3)
	v_cvt_pk_fp8_f32 v169, v172, v174
	v_mov_b32_e32 v130, 0
	v_or_b32_e32 v134, s38, v157
	v_cvt_pk_fp8_f32 v130, v131, v133
	v_mov_b32_e32 v131, 0
	v_mul_lo_u32 v138, s21, v134
	v_mad_u64_u32 v[134:135], s[2:3], s20, v134, v[178:179]
	v_cvt_pk_fp8_f32 v131, v173, v175
	v_add3_u32 v135, v138, v135, s37
	s_waitcnt lgkmcnt(2)
	v_cvt_pk_fp8_f32 v168, v170, v176 op_sel:[0,0,1]
	s_waitcnt lgkmcnt(0)
	v_cvt_pk_fp8_f32 v169, v180, v182 op_sel:[0,0,1]
	global_store_dwordx2 v[134:135], v[128:129], off nt
	v_or_b32_e32 v128, s38, v158
	v_mul_lo_u32 v132, s21, v128
	v_mad_u64_u32 v[128:129], s[2:3], s20, v128, v[178:179]
	v_add3_u32 v129, v132, v129, s37
	v_cvt_pk_fp8_f32 v130, v171, v177 op_sel:[0,0,1]
	v_cvt_pk_fp8_f32 v131, v181, v183 op_sel:[0,0,1]
	global_store_dwordx2 v[128:129], v[168:169], off nt
	v_or_b32_e32 v128, s38, v159
	v_mul_lo_u32 v132, s21, v128
	v_mad_u64_u32 v[128:129], s[2:3], s20, v128, v[178:179]
	v_add3_u32 v129, v132, v129, s37
	global_store_dwordx2 v[128:129], v[130:131], off nt
	s_waitcnt lgkmcnt(0)
	s_mov_b64 s[2:3], 0

.LBB0_231:
	v_add_u32_e32 v128, 0x420, v154
	ds_write2_b32 v128, v132, v133 offset1:1
	v_add_u32_e32 v128, 0x428, v154
	ds_write2_b32 v128, v134, v135 offset1:1
	s_cmp_ge_u32 s60, s4
	s_cselect_b32 s0, s61, s60
	s_waitcnt lgkmcnt(0)
	s_sub_i32 s1, s0, s4
	ds_read2_b32 v[128:129], v155 offset0:33 offset1:41
	ds_read2_b32 v[130:131], v155 offset1:8
	s_cmp_ge_u32 s0, s4
	ds_read2_b32 v[134:135], v155 offset0:66 offset1:74
	ds_read2_b32 v[168:169], v155 offset0:132 offset1:140
	ds_read2_b32 v[170:171], v155 offset0:165 offset1:173
	ds_read2_b32 v[172:173], v155 offset0:99 offset1:107
	s_cselect_b32 s0, s1, s0
	s_xor_b32 s0, s0, s59
	s_sub_i32 s0, s0, s59
	v_mov_b32_e32 v132, 0
	v_mov_b32_e32 v133, 0
	ds_read2_b32 v[174:175], v155 offset0:198 offset1:206
	ds_read2_b32 v[176:177], v155 offset0:231 offset1:239
	s_lshl_b32 s2, s0, 6
	s_waitcnt lgkmcnt(6)
	v_cvt_pk_fp8_f32 v132, v130, v128
	s_waitcnt lgkmcnt(3)
	v_cvt_pk_fp8_f32 v133, v168, v170
	s_add_u32 s0, s18, s36
	s_addc_u32 s1, s19, s37
	v_lshl_add_u64 v[178:179], s[0:1], 0, v[140:141]
	v_or_b32_e32 v128, s2, v160
	s_waitcnt lgkmcnt(2)
	v_cvt_pk_fp8_f32 v132, v134, v172 op_sel:[0,0,1]
	s_waitcnt lgkmcnt(0)
	v_cvt_pk_fp8_f32 v133, v174, v176 op_sel:[0,0,1]
	v_mul_lo_u32 v130, s21, v128
	v_mad_u64_u32 v[180:181], s[0:1], s20, v128, v[178:179]
	v_mov_b32_e32 v128, 0
	s_ashr_i32 s0, s2, 31
	v_cvt_pk_fp8_f32 v128, v131, v129
	v_mov_b32_e32 v129, 0
	s_mul_i32 s3, s20, s0
	v_cvt_pk_fp8_f32 v129, v169, v171
	v_add3_u32 v181, v130, v181, s3
	global_store_dwordx2 v[180:181], v[132:133], off nt
	ds_read2_b32 v[130:131], v155 offset0:16 offset1:24
	ds_read2_b32 v[132:133], v155 offset0:49 offset1:57
	v_cvt_pk_fp8_f32 v128, v135, v173 op_sel:[0,0,1]
	v_cvt_pk_fp8_f32 v129, v175, v177 op_sel:[0,0,1]
	ds_read2_b32 v[170:171], v155 offset0:82 offset1:90
	ds_read2_b32 v[172:173], v155 offset0:148 offset1:156
	ds_read2_b32 v[174:175], v155 offset0:181 offset1:189
	ds_read2_b32 v[176:177], v155 offset0:115 offset1:123
	v_mov_b32_e32 v168, 0
	v_mov_b32_e32 v169, 0
	ds_read2_b32 v[180:181], v155 offset0:214 offset1:222
	ds_read2_b32 v[182:183], v155 offset0:247 offset1:255
	s_waitcnt lgkmcnt(6)
	v_cvt_pk_fp8_f32 v168, v130, v132
	s_waitcnt lgkmcnt(3)
	v_cvt_pk_fp8_f32 v169, v172, v174
	v_mov_b32_e32 v130, 0
	v_or_b32_e32 v134, s2, v161
	v_cvt_pk_fp8_f32 v130, v131, v133
	v_mov_b32_e32 v131, 0
	v_mul_lo_u32 v138, s21, v134
	v_mad_u64_u32 v[134:135], s[0:1], s20, v134, v[178:179]
	v_cvt_pk_fp8_f32 v131, v173, v175
	v_add3_u32 v135, v138, v135, s3
	s_waitcnt lgkmcnt(2)
	v_cvt_pk_fp8_f32 v168, v170, v176 op_sel:[0,0,1]
	s_waitcnt lgkmcnt(0)
	v_cvt_pk_fp8_f32 v169, v180, v182 op_sel:[0,0,1]
	global_store_dwordx2 v[134:135], v[128:129], off nt
	v_or_b32_e32 v128, s2, v162
	v_mul_lo_u32 v132, s21, v128
	v_mad_u64_u32 v[128:129], s[0:1], s20, v128, v[178:179]
	v_add3_u32 v129, v132, v129, s3
	v_cvt_pk_fp8_f32 v130, v171, v177 op_sel:[0,0,1]
	v_cvt_pk_fp8_f32 v131, v181, v183 op_sel:[0,0,1]
	global_store_dwordx2 v[128:129], v[168:169], off nt
	v_or_b32_e32 v128, s2, v163
	v_mul_lo_u32 v132, s21, v128
	v_mad_u64_u32 v[128:129], s[0:1], s20, v128, v[178:179]
	v_add3_u32 v129, v132, v129, s3
	global_store_dwordx2 v[128:129], v[130:131], off nt
	s_waitcnt lgkmcnt(0)
	s_branch .LBB0_250

.LBB0_249:
	v_add_u32_e32 v96, 0x420, v154
	ds_write2_b32 v96, v100, v101 offset1:1
	v_add_u32_e32 v96, 0x428, v154
	ds_write2_b32 v96, v102, v103 offset1:1
	s_cmp_ge_u32 s60, s4
	s_cselect_b32 s0, s61, s60
	s_waitcnt lgkmcnt(0)
	s_sub_i32 s1, s0, s4
	ds_read2_b32 v[96:97], v155 offset0:33 offset1:41
	ds_read2_b32 v[98:99], v155 offset1:8
	s_cmp_ge_u32 s0, s4
	ds_read2_b32 v[102:103], v155 offset0:66 offset1:74
	ds_read2_b32 v[104:105], v155 offset0:132 offset1:140
	ds_read2_b32 v[106:107], v155 offset0:165 offset1:173
	ds_read2_b32 v[108:109], v155 offset0:99 offset1:107
	s_cselect_b32 s0, s1, s0
	s_xor_b32 s0, s0, s59
	s_sub_i32 s0, s0, s59
	v_mov_b32_e32 v100, 0
	v_mov_b32_e32 v101, 0
	ds_read2_b32 v[110:111], v155 offset0:198 offset1:206
	ds_read2_b32 v[112:113], v155 offset0:231 offset1:239
	s_lshl_b32 s2, s0, 5
	s_waitcnt lgkmcnt(6)
	v_cvt_pk_fp8_f32 v100, v98, v96
	s_waitcnt lgkmcnt(3)
	v_cvt_pk_fp8_f32 v101, v104, v106
	s_add_u32 s0, s18, s36
	s_addc_u32 s1, s19, s37
	v_lshl_add_u64 v[114:115], s[0:1], 0, v[140:141]
	v_or_b32_e32 v96, s2, v136
	s_waitcnt lgkmcnt(2)
	v_cvt_pk_fp8_f32 v100, v102, v108 op_sel:[0,0,1]
	s_waitcnt lgkmcnt(0)
	v_cvt_pk_fp8_f32 v101, v110, v112 op_sel:[0,0,1]
	v_mul_lo_u32 v98, s21, v96
	v_mad_u64_u32 v[116:117], s[0:1], s20, v96, v[114:115]
	v_mov_b32_e32 v96, 0
	s_ashr_i32 s0, s2, 31
	v_cvt_pk_fp8_f32 v96, v99, v97
	v_mov_b32_e32 v97, 0
	s_mul_i32 s3, s20, s0
	v_cvt_pk_fp8_f32 v97, v105, v107
	v_add3_u32 v117, v98, v117, s3
	global_store_dwordx2 v[116:117], v[100:101], off nt
	ds_read2_b32 v[98:99], v155 offset0:16 offset1:24
	ds_read2_b32 v[100:101], v155 offset0:49 offset1:57
	v_cvt_pk_fp8_f32 v96, v103, v109 op_sel:[0,0,1]
	v_cvt_pk_fp8_f32 v97, v111, v113 op_sel:[0,0,1]
	ds_read2_b32 v[106:107], v155 offset0:82 offset1:90
	ds_read2_b32 v[108:109], v155 offset0:148 offset1:156
	ds_read2_b32 v[110:111], v155 offset0:181 offset1:189
	ds_read2_b32 v[112:113], v155 offset0:115 offset1:123
	v_mov_b32_e32 v104, 0
	v_mov_b32_e32 v105, 0
	ds_read2_b32 v[116:117], v155 offset0:214 offset1:222
	ds_read2_b32 v[118:119], v155 offset0:247 offset1:255
	s_waitcnt lgkmcnt(6)
	v_cvt_pk_fp8_f32 v104, v98, v100
	s_waitcnt lgkmcnt(3)
	v_cvt_pk_fp8_f32 v105, v108, v110
	v_mov_b32_e32 v98, 0
	v_or_b32_e32 v102, s2, v146
	v_cvt_pk_fp8_f32 v98, v99, v101
	v_mov_b32_e32 v99, 0
	v_mul_lo_u32 v120, s21, v102
	v_mad_u64_u32 v[102:103], s[0:1], s20, v102, v[114:115]
	v_cvt_pk_fp8_f32 v99, v109, v111
	v_add3_u32 v103, v120, v103, s3
	s_waitcnt lgkmcnt(2)
	v_cvt_pk_fp8_f32 v104, v106, v112 op_sel:[0,0,1]
	s_waitcnt lgkmcnt(0)
	v_cvt_pk_fp8_f32 v105, v116, v118 op_sel:[0,0,1]
	global_store_dwordx2 v[102:103], v[96:97], off nt
	v_or_b32_e32 v96, s2, v148
	v_mul_lo_u32 v100, s21, v96
	v_mad_u64_u32 v[96:97], s[0:1], s20, v96, v[114:115]
	v_add3_u32 v97, v100, v97, s3
	v_cvt_pk_fp8_f32 v98, v107, v113 op_sel:[0,0,1]
	v_cvt_pk_fp8_f32 v99, v117, v119 op_sel:[0,0,1]
	global_store_dwordx2 v[96:97], v[104:105], off nt
	v_or_b32_e32 v96, s2, v150
	v_mul_lo_u32 v100, s21, v96
	v_mad_u64_u32 v[96:97], s[0:1], s20, v96, v[114:115]
	v_add3_u32 v97, v100, v97, s3
	global_store_dwordx2 v[96:97], v[98:99], off nt
	s_waitcnt lgkmcnt(0)

.LBB0_266:
	v_add_u32_e32 v100, 0x420, v154
	ds_write2_b32 v100, v96, v97 offset1:1
	v_add_u32_e32 v96, 0x428, v154
	s_mul_i32 s38, s38, s4
	ds_write2_b32 v96, v98, v99 offset1:1
	s_sub_i32 s0, s60, s38
	s_waitcnt lgkmcnt(0)
	s_lshl_b32 s2, s0, 6
	s_lshl_b64 s[0:1], s[36:37], 1
	s_add_u32 s0, s18, s0
	ds_read2_b32 v[100:101], v155 offset0:33 offset1:41
	ds_read2_b32 v[102:103], v155 offset1:8
	ds_read2_b32 v[104:105], v155 offset0:66 offset1:74
	ds_read2_b32 v[106:107], v155 offset0:99 offset1:107
	ds_read2_b32 v[108:109], v155 offset0:132 offset1:140
	ds_read2_b32 v[110:111], v155 offset0:165 offset1:173
	ds_read2_b32 v[112:113], v155 offset0:198 offset1:206
	ds_read2_b32 v[114:115], v155 offset0:231 offset1:239
	s_addc_u32 s1, s19, s1
	v_lshlrev_b32_e32 v138, 1, v140
	s_waitcnt lgkmcnt(6)
	s_nop 1
	v_cvt_pk_bf16_f32 v96, v102, v100
	v_or_b32_e32 v100, s2, v160
	v_lshl_add_u64 v[116:117], s[0:1], 0, v[138:139]
	v_mad_u64_u32 v[118:119], s[0:1], s20, v100, 0
	s_ashr_i32 s0, s2, 31
	v_mul_lo_u32 v102, s21, v100
	s_mul_i32 s3, s20, s0
	v_add3_u32 v119, v119, s3, v102
	v_lshl_add_u64 v[118:119], v[118:119], 1, v[116:117]
	v_or_b32_e32 v100, s2, v161
	s_waitcnt lgkmcnt(4)
	s_nop 1
	v_cvt_pk_bf16_f32 v97, v104, v106
	s_waitcnt lgkmcnt(2)
	s_nop 1
	v_cvt_pk_bf16_f32 v98, v108, v110
	s_waitcnt lgkmcnt(0)
	s_nop 1
	v_cvt_pk_bf16_f32 v99, v112, v114
	global_store_dwordx4 v[118:119], v[96:99], off nt
	v_mul_lo_u32 v102, s21, v100
	s_nop 0
	s_nop 1
	v_cvt_pk_bf16_f32 v96, v103, v101
	v_mad_u64_u32 v[100:101], s[0:1], s20, v100, 0
	v_add3_u32 v101, v101, s3, v102
	s_nop 1
	v_cvt_pk_bf16_f32 v97, v105, v107
	s_nop 1
	v_cvt_pk_bf16_f32 v98, v109, v111
	s_nop 1
	v_cvt_pk_bf16_f32 v99, v113, v115
	v_lshl_add_u64 v[100:101], v[100:101], 1, v[116:117]
	ds_read2_b32 v[102:103], v155 offset0:16 offset1:24
	ds_read2_b32 v[104:105], v155 offset0:49 offset1:57
	ds_read2_b32 v[106:107], v155 offset0:82 offset1:90
	ds_read2_b32 v[108:109], v155 offset0:115 offset1:123
	ds_read2_b32 v[110:111], v155 offset0:148 offset1:156
	ds_read2_b32 v[112:113], v155 offset0:181 offset1:189
	ds_read2_b32 v[114:115], v155 offset0:214 offset1:222
	ds_read2_b32 v[118:119], v155 offset0:247 offset1:255
	global_store_dwordx4 v[100:101], v[96:99], off nt
	v_or_b32_e32 v100, s2, v162
	s_waitcnt lgkmcnt(6)
	s_nop 1
	v_cvt_pk_bf16_f32 v96, v102, v104
	v_mul_lo_u32 v102, s21, v100
	v_mad_u64_u32 v[100:101], s[0:1], s20, v100, 0
	v_add3_u32 v101, v101, s3, v102
	v_lshl_add_u64 v[100:101], v[100:101], 1, v[116:117]
	s_waitcnt lgkmcnt(4)
	s_nop 1
	v_cvt_pk_bf16_f32 v97, v106, v108
	s_waitcnt lgkmcnt(2)
	s_nop 1
	v_cvt_pk_bf16_f32 v98, v110, v112
	s_waitcnt lgkmcnt(0)
	s_nop 1
	v_cvt_pk_bf16_f32 v99, v114, v118
	global_store_dwordx4 v[100:101], v[96:99], off nt
	v_or_b32_e32 v100, s2, v163
	v_mul_lo_u32 v102, s21, v100
	v_mad_u64_u32 v[100:101], s[0:1], s20, v100, 0
	v_add3_u32 v101, v101, s3, v102
	v_lshl_add_u64 v[100:101], v[100:101], 1, v[116:117]
	s_nop 1
	v_cvt_pk_bf16_f32 v96, v103, v105
	s_nop 1
	v_cvt_pk_bf16_f32 v97, v107, v109
	s_nop 1
	v_cvt_pk_bf16_f32 v98, v111, v113
	s_nop 1
	v_cvt_pk_bf16_f32 v99, v115, v119
	global_store_dwordx4 v[100:101], v[96:99], off nt
	s_waitcnt lgkmcnt(0)
	s_mov_b64 s[0:1], 0

.LBB0_280:
	s_abs_i32 s0, s60
	s_mul_hi_u32 s1, s0, s56
	s_mul_i32 s1, s1, s4
	s_sub_i32 s0, s0, s1
	s_sub_i32 s1, s0, s4
	s_cmp_ge_u32 s0, s4
	s_cselect_b32 s0, s1, s0
	s_sub_i32 s1, s0, s4
	s_cmp_ge_u32 s0, s4
	v_add_u32_e32 v100, 0x420, v154
	s_cselect_b32 s0, s1, s0
	ds_write2_b32 v100, v96, v97 offset1:1
	v_add_u32_e32 v96, 0x428, v154
	s_xor_b32 s0, s0, s59
	ds_write2_b32 v96, v98, v99 offset1:1
	s_sub_i32 s0, s0, s59
	s_waitcnt lgkmcnt(0)
	s_lshl_b32 s2, s0, 6
	s_lshl_b64 s[0:1], s[36:37], 1
	s_add_u32 s0, s18, s0
	ds_read2_b32 v[100:101], v155 offset0:33 offset1:41
	ds_read2_b32 v[102:103], v155 offset1:8
	ds_read2_b32 v[104:105], v155 offset0:66 offset1:74
	ds_read2_b32 v[106:107], v155 offset0:99 offset1:107
	ds_read2_b32 v[108:109], v155 offset0:132 offset1:140
	ds_read2_b32 v[110:111], v155 offset0:165 offset1:173
	ds_read2_b32 v[112:113], v155 offset0:198 offset1:206
	ds_read2_b32 v[114:115], v155 offset0:231 offset1:239
	s_addc_u32 s1, s19, s1
	v_lshlrev_b32_e32 v138, 1, v140
	s_waitcnt lgkmcnt(6)
	s_nop 1
	v_cvt_pk_bf16_f32 v96, v102, v100
	v_or_b32_e32 v100, s2, v156
	v_lshl_add_u64 v[116:117], s[0:1], 0, v[138:139]
	v_mad_u64_u32 v[118:119], s[0:1], s20, v100, 0
	s_ashr_i32 s0, s2, 31
	v_mul_lo_u32 v102, s21, v100
	s_mul_i32 s3, s20, s0
	v_add3_u32 v119, v119, s3, v102
	v_lshl_add_u64 v[118:119], v[118:119], 1, v[116:117]
	v_or_b32_e32 v100, s2, v157
	s_waitcnt lgkmcnt(4)
	s_nop 1
	v_cvt_pk_bf16_f32 v97, v104, v106
	s_waitcnt lgkmcnt(2)
	s_nop 1
	v_cvt_pk_bf16_f32 v98, v108, v110
	s_waitcnt lgkmcnt(0)
	s_nop 1
	v_cvt_pk_bf16_f32 v99, v112, v114
	global_store_dwordx4 v[118:119], v[96:99], off nt
	v_mul_lo_u32 v102, s21, v100
	s_nop 0
	s_nop 1
	v_cvt_pk_bf16_f32 v96, v103, v101
	v_mad_u64_u32 v[100:101], s[0:1], s20, v100, 0
	v_add3_u32 v101, v101, s3, v102
	s_nop 1
	v_cvt_pk_bf16_f32 v97, v105, v107
	s_nop 1
	v_cvt_pk_bf16_f32 v98, v109, v111
	s_nop 1
	v_cvt_pk_bf16_f32 v99, v113, v115
	v_lshl_add_u64 v[100:101], v[100:101], 1, v[116:117]
	ds_read2_b32 v[102:103], v155 offset0:16 offset1:24
	ds_read2_b32 v[104:105], v155 offset0:49 offset1:57
	ds_read2_b32 v[106:107], v155 offset0:82 offset1:90
	ds_read2_b32 v[108:109], v155 offset0:115 offset1:123
	ds_read2_b32 v[110:111], v155 offset0:148 offset1:156
	ds_read2_b32 v[112:113], v155 offset0:181 offset1:189
	ds_read2_b32 v[114:115], v155 offset0:214 offset1:222
	ds_read2_b32 v[118:119], v155 offset0:247 offset1:255
	global_store_dwordx4 v[100:101], v[96:99], off nt
	v_or_b32_e32 v100, s2, v158
	s_waitcnt lgkmcnt(6)
	s_nop 1
	v_cvt_pk_bf16_f32 v96, v102, v104
	v_mul_lo_u32 v102, s21, v100
	v_mad_u64_u32 v[100:101], s[0:1], s20, v100, 0
	v_add3_u32 v101, v101, s3, v102
	v_lshl_add_u64 v[100:101], v[100:101], 1, v[116:117]
	s_waitcnt lgkmcnt(4)
	s_nop 1
	v_cvt_pk_bf16_f32 v97, v106, v108
	s_waitcnt lgkmcnt(2)
	s_nop 1
	v_cvt_pk_bf16_f32 v98, v110, v112
	s_waitcnt lgkmcnt(0)
	s_nop 1
	v_cvt_pk_bf16_f32 v99, v114, v118
	global_store_dwordx4 v[100:101], v[96:99], off nt
	v_or_b32_e32 v100, s2, v159
	v_mul_lo_u32 v102, s21, v100
	v_mad_u64_u32 v[100:101], s[0:1], s20, v100, 0
	v_add3_u32 v101, v101, s3, v102
	v_lshl_add_u64 v[100:101], v[100:101], 1, v[116:117]
	s_nop 1
	v_cvt_pk_bf16_f32 v96, v103, v105
	s_nop 1
	v_cvt_pk_bf16_f32 v97, v107, v109
	s_nop 1
	v_cvt_pk_bf16_f32 v98, v111, v113
	s_nop 1
	v_cvt_pk_bf16_f32 v99, v115, v119
	global_store_dwordx4 v[100:101], v[96:99], off nt
	s_waitcnt lgkmcnt(0)
	s_mov_b64 s[0:1], 0

.LBB0_294:
	s_abs_i32 s0, s60
	s_mul_hi_u32 s1, s0, s56
	s_mul_i32 s1, s1, s4
	s_sub_i32 s0, s0, s1
	s_sub_i32 s1, s0, s4
	s_cmp_ge_u32 s0, s4
	s_cselect_b32 s0, s1, s0
	s_sub_i32 s1, s0, s4
	s_cmp_ge_u32 s0, s4
	s_cselect_b32 s0, s1, s0
	s_xor_b32 s0, s0, s59
	s_sub_i32 s0, s0, s59
	s_lshl_b32 s38, s0, 5
	v_add_u32_e32 v100, 0x420, v154
	s_cmpk_lt_u32 s38, 0xa00
	ds_write2_b32 v100, v96, v97 offset1:1
	v_add_u32_e32 v96, 0x428, v154
	s_cselect_b64 s[0:1], -1, 0
	s_cmpk_lt_u32 s38, 0xe00
	ds_write2_b32 v96, v98, v99 offset1:1
	s_cselect_b64 s[2:3], -1, 0
	s_waitcnt lgkmcnt(0)
	s_and_b64 s[2:3], s[2:3], exec
	ds_read2_b32 v[100:101], v155 offset0:33 offset1:41
	ds_read2_b32 v[102:103], v155 offset1:8
	ds_read2_b32 v[104:105], v155 offset0:66 offset1:74
	ds_read2_b32 v[106:107], v155 offset0:99 offset1:107
	ds_read2_b32 v[108:109], v155 offset0:132 offset1:140
	ds_read2_b32 v[110:111], v155 offset0:165 offset1:173
	ds_read2_b32 v[112:113], v155 offset0:198 offset1:206
	ds_read2_b32 v[114:115], v155 offset0:231 offset1:239
	s_cselect_b32 s2, s54, 0xfffffa00
	s_cselect_b32 s3, s31, s19
	s_cselect_b32 s39, s30, s18
	s_and_b64 s[0:1], s[0:1], exec
	s_waitcnt lgkmcnt(6)
	s_nop 1
	v_cvt_pk_bf16_f32 v96, v102, v100
	v_or_b32_e32 v100, s38, v136
	s_cselect_b32 s0, 0xfffffe00, s2
	v_mov_b32_e32 v120, s0
	v_cmp_gt_i32_e32 vcc, s52, v100
	s_cselect_b32 s1, s18, s39
	s_cselect_b32 s2, s19, s3
	v_cndmask_b32_e32 v102, v120, v165, vcc
	v_add_u32_e32 v100, v102, v100
	v_ashrrev_i32_e32 v102, 31, v100
	s_waitcnt lgkmcnt(4)
	s_nop 1
	v_cvt_pk_bf16_f32 v97, v104, v106
	v_mov_b32_e32 v121, s2
	v_mov_b32_e32 v122, s31
	v_mov_b32_e32 v123, s1
	s_waitcnt vmcnt(10)
	v_mov_b32_e32 v124, s30
	v_mul_lo_u32 v102, s20, v102
	v_mul_lo_u32 v104, s21, v100
	v_mad_u64_u32 v[118:119], s[0:1], s20, v100, 0
	v_cndmask_b32_e32 v117, v121, v122, vcc
	v_cndmask_b32_e32 v116, v123, v124, vcc
	v_add3_u32 v119, v119, v102, v104
	v_lshl_add_u64 v[116:117], v[118:119], 1, v[116:117]
	s_lshl_b64 s[0:1], s[36:37], 1
	v_lshl_add_u64 v[116:117], v[116:117], 0, s[0:1]
	v_lshlrev_b32_e32 v138, 1, v140
	v_or_b32_e32 v102, s38, v146
	v_lshl_add_u64 v[116:117], v[116:117], 0, v[138:139]
	v_cmp_gt_i32_e32 vcc, s52, v102
	s_waitcnt lgkmcnt(2)
	s_nop 1
	v_cvt_pk_bf16_f32 v98, v108, v110
	s_waitcnt lgkmcnt(0)
	s_nop 1
	v_cvt_pk_bf16_f32 v99, v112, v114
	global_store_dwordx4 v[116:117], v[96:99], off nt
	v_cndmask_b32_e32 v100, v123, v124, vcc
	s_nop 0
	s_nop 1
	v_cvt_pk_bf16_f32 v96, v103, v101
	v_cndmask_b32_e32 v103, v120, v165, vcc
	v_add_u32_e32 v102, v103, v102
	v_ashrrev_i32_e32 v103, 31, v102
	s_nop 1
	v_cvt_pk_bf16_f32 v97, v105, v107
	v_mul_lo_u32 v104, s20, v103
	v_mul_lo_u32 v105, s21, v102
	v_mad_u64_u32 v[102:103], s[2:3], s20, v102, 0
	v_cndmask_b32_e32 v101, v121, v122, vcc
	v_add3_u32 v103, v103, v104, v105
	v_lshl_add_u64 v[100:101], v[102:103], 1, v[100:101]
	v_lshl_add_u64 v[100:101], v[100:101], 0, s[0:1]
	s_nop 1
	v_cvt_pk_bf16_f32 v98, v109, v111
	s_nop 1
	v_cvt_pk_bf16_f32 v99, v113, v115
	v_lshl_add_u64 v[100:101], v[100:101], 0, v[138:139]
	ds_read2_b32 v[102:103], v155 offset0:16 offset1:24
	ds_read2_b32 v[104:105], v155 offset0:49 offset1:57
	ds_read2_b32 v[106:107], v155 offset0:82 offset1:90
	ds_read2_b32 v[108:109], v155 offset0:115 offset1:123
	ds_read2_b32 v[110:111], v155 offset0:148 offset1:156
	ds_read2_b32 v[112:113], v155 offset0:181 offset1:189
	ds_read2_b32 v[114:115], v155 offset0:214 offset1:222
	ds_read2_b32 v[116:117], v155 offset0:247 offset1:255
	global_store_dwordx4 v[100:101], v[96:99], off nt
	s_waitcnt lgkmcnt(6)
	s_nop 0
	s_nop 1
	v_cvt_pk_bf16_f32 v96, v102, v104
	v_or_b32_e32 v102, s38, v148
	v_cmp_gt_i32_e32 vcc, s52, v102
	s_waitcnt lgkmcnt(4)
	s_nop 1
	v_cvt_pk_bf16_f32 v97, v106, v108
	s_waitcnt lgkmcnt(2)
	s_nop 1
	v_cvt_pk_bf16_f32 v98, v110, v112
	s_waitcnt lgkmcnt(0)
	s_nop 1
	v_cvt_pk_bf16_f32 v99, v114, v116
	v_cndmask_b32_e32 v104, v120, v165, vcc
	v_add_u32_e32 v102, v104, v102
	v_ashrrev_i32_e32 v104, 31, v102
	v_mul_lo_u32 v104, s20, v104
	v_mul_lo_u32 v106, s21, v102
	v_mad_u64_u32 v[118:119], s[2:3], s20, v102, 0
	v_cndmask_b32_e32 v101, v121, v122, vcc
	v_cndmask_b32_e32 v100, v123, v124, vcc
	v_add3_u32 v119, v119, v104, v106
	v_lshl_add_u64 v[100:101], v[118:119], 1, v[100:101]
	v_lshl_add_u64 v[100:101], v[100:101], 0, s[0:1]
	v_or_b32_e32 v102, s38, v150
	v_lshl_add_u64 v[100:101], v[100:101], 0, v[138:139]
	v_cmp_gt_i32_e32 vcc, s52, v102
	global_store_dwordx4 v[100:101], v[96:99], off nt
	s_nop 0
	v_cndmask_b32_e32 v101, v121, v122, vcc
	s_nop 1
	v_cvt_pk_bf16_f32 v96, v103, v105
	v_cndmask_b32_e32 v103, v120, v165, vcc
	v_add_u32_e32 v102, v103, v102
	v_ashrrev_i32_e32 v103, 31, v102
	v_mul_lo_u32 v104, s20, v103
	v_mul_lo_u32 v105, s21, v102
	v_mad_u64_u32 v[102:103], s[2:3], s20, v102, 0
	v_cndmask_b32_e32 v100, v123, v124, vcc
	v_add3_u32 v103, v103, v104, v105
	v_lshl_add_u64 v[100:101], v[102:103], 1, v[100:101]
	v_lshl_add_u64 v[100:101], v[100:101], 0, s[0:1]
	v_lshl_add_u64 v[100:101], v[100:101], 0, v[138:139]
	s_nop 1
	v_cvt_pk_bf16_f32 v97, v107, v109
	s_nop 1
	v_cvt_pk_bf16_f32 v98, v111, v113
	s_nop 1
	v_cvt_pk_bf16_f32 v99, v115, v117
	global_store_dwordx4 v[100:101], v[96:99], off nt
	s_waitcnt lgkmcnt(0)

.LBB0_309:
	s_abs_i32 s0, s60
	s_mul_hi_u32 s1, s0, s56
	s_mul_i32 s1, s1, s4
	s_sub_i32 s0, s0, s1
	s_sub_i32 s1, s0, s4
	s_cmp_ge_u32 s0, s4
	s_cselect_b32 s0, s1, s0
	s_sub_i32 s1, s0, s4
	s_cmp_ge_u32 s0, s4
	s_cselect_b32 s0, s1, s0
	s_xor_b32 s0, s0, s59
	v_add_u32_e32 v100, 0x420, v154
	s_sub_i32 s0, s0, s59
	ds_write2_b32 v100, v96, v97 offset1:1
	v_add_u32_e32 v96, 0x428, v154
	s_lshl_b32 s2, s0, 5
	s_lshl_b64 s[0:1], s[28:29], 1
	ds_write2_b32 v96, v98, v99 offset1:1
	s_add_u32 s3, s18, s0
	s_waitcnt lgkmcnt(0)
	s_addc_u32 s38, s19, s1
	s_lshl_b64 s[0:1], s[36:37], 1
	s_add_u32 s0, s3, s0
	ds_read2_b32 v[100:101], v155 offset0:33 offset1:41
	ds_read2_b32 v[102:103], v155 offset1:8
	ds_read2_b32 v[104:105], v155 offset0:66 offset1:74
	ds_read2_b32 v[106:107], v155 offset0:99 offset1:107
	ds_read2_b32 v[108:109], v155 offset0:132 offset1:140
	ds_read2_b32 v[110:111], v155 offset0:165 offset1:173
	ds_read2_b32 v[112:113], v155 offset0:198 offset1:206
	ds_read2_b32 v[114:115], v155 offset0:231 offset1:239
	s_addc_u32 s1, s38, s1
	v_lshlrev_b32_e32 v138, 1, v140
	s_waitcnt lgkmcnt(6)
	s_nop 1
	v_cvt_pk_bf16_f32 v96, v102, v100
	v_or_b32_e32 v100, s2, v136
	v_lshl_add_u64 v[116:117], s[0:1], 0, v[138:139]
	v_mad_u64_u32 v[118:119], s[0:1], s26, v100, 0
	s_ashr_i32 s0, s2, 31
	v_mul_lo_u32 v102, s27, v100
	s_mul_i32 s3, s26, s0
	v_add3_u32 v119, v119, s3, v102
	v_lshl_add_u64 v[118:119], v[118:119], 1, v[116:117]
	v_or_b32_e32 v100, s2, v146
	s_waitcnt lgkmcnt(4)
	s_nop 1
	v_cvt_pk_bf16_f32 v97, v104, v106
	s_waitcnt lgkmcnt(2)
	s_nop 1
	v_cvt_pk_bf16_f32 v98, v108, v110
	s_waitcnt lgkmcnt(0)
	s_nop 1
	v_cvt_pk_bf16_f32 v99, v112, v114
	global_store_dwordx4 v[118:119], v[96:99], off nt
	v_mul_lo_u32 v102, s27, v100
	s_nop 0
	s_nop 1
	v_cvt_pk_bf16_f32 v96, v103, v101
	v_mad_u64_u32 v[100:101], s[0:1], s26, v100, 0
	v_add3_u32 v101, v101, s3, v102
	s_nop 1
	v_cvt_pk_bf16_f32 v97, v105, v107
	s_nop 1
	v_cvt_pk_bf16_f32 v98, v109, v111
	s_nop 1
	v_cvt_pk_bf16_f32 v99, v113, v115
	v_lshl_add_u64 v[100:101], v[100:101], 1, v[116:117]
	ds_read2_b32 v[102:103], v155 offset0:16 offset1:24
	ds_read2_b32 v[104:105], v155 offset0:49 offset1:57
	ds_read2_b32 v[106:107], v155 offset0:82 offset1:90
	ds_read2_b32 v[108:109], v155 offset0:115 offset1:123
	ds_read2_b32 v[110:111], v155 offset0:148 offset1:156
	ds_read2_b32 v[112:113], v155 offset0:181 offset1:189
	ds_read2_b32 v[114:115], v155 offset0:214 offset1:222
	ds_read2_b32 v[118:119], v155 offset0:247 offset1:255
	global_store_dwordx4 v[100:101], v[96:99], off nt
	v_or_b32_e32 v100, s2, v148
	s_waitcnt lgkmcnt(6)
	s_nop 1
	v_cvt_pk_bf16_f32 v96, v102, v104
	v_mul_lo_u32 v102, s27, v100
	v_mad_u64_u32 v[100:101], s[0:1], s26, v100, 0
	v_add3_u32 v101, v101, s3, v102
	v_lshl_add_u64 v[100:101], v[100:101], 1, v[116:117]
	s_waitcnt lgkmcnt(4)
	s_nop 1
	v_cvt_pk_bf16_f32 v97, v106, v108
	s_waitcnt lgkmcnt(2)
	s_nop 1
	v_cvt_pk_bf16_f32 v98, v110, v112
	s_waitcnt lgkmcnt(0)
	s_nop 1
	v_cvt_pk_bf16_f32 v99, v114, v118
	global_store_dwordx4 v[100:101], v[96:99], off nt
	v_or_b32_e32 v100, s2, v150
	v_mul_lo_u32 v102, s27, v100
	v_mad_u64_u32 v[100:101], s[0:1], s26, v100, 0
	v_add3_u32 v101, v101, s3, v102
	v_lshl_add_u64 v[100:101], v[100:101], 1, v[116:117]
	s_nop 1
	v_cvt_pk_bf16_f32 v96, v103, v105
	s_nop 1
	v_cvt_pk_bf16_f32 v97, v107, v109
	s_nop 1
	v_cvt_pk_bf16_f32 v98, v111, v113
	s_nop 1
	v_cvt_pk_bf16_f32 v99, v115, v119
	global_store_dwordx4 v[100:101], v[96:99], off nt
	s_waitcnt lgkmcnt(0)

.LBB0_332:
	s_abs_i32 s0, s60
	s_mul_hi_u32 s1, s0, s56
	s_mul_i32 s1, s1, s4
	s_sub_i32 s0, s0, s1
	v_add_u32_e32 v96, 0x420, v154
	s_sub_i32 s1, s0, s4
	ds_write2_b32 v96, v100, v101 offset1:1
	v_add_u32_e32 v96, 0x428, v154
	s_cmp_ge_u32 s0, s4
	ds_write2_b32 v96, v102, v103 offset1:1
	s_cselect_b32 s0, s1, s0
	s_sub_i32 s1, s0, s4
	s_waitcnt lgkmcnt(0)
	s_cmp_ge_u32 s0, s4
	ds_read2_b32 v[96:97], v155 offset0:33 offset1:41
	ds_read2_b32 v[98:99], v155 offset1:8
	s_cselect_b32 s0, s1, s0
	s_xor_b32 s0, s0, s59
	s_sub_i32 s0, s0, s59
	ds_read2_b32 v[102:103], v155 offset0:66 offset1:74
	ds_read2_b32 v[104:105], v155 offset0:132 offset1:140
	ds_read2_b32 v[106:107], v155 offset0:165 offset1:173
	ds_read2_b32 v[108:109], v155 offset0:99 offset1:107
	s_lshl_b32 s2, s0, 5
	v_mov_b32_e32 v100, v139
	s_waitcnt lgkmcnt(4)
	v_cvt_pk_fp8_f32 v100, v98, v96
	v_or_b32_e32 v96, s2, v136
	v_mov_b32_e32 v101, v139
	ds_read2_b32 v[110:111], v155 offset0:198 offset1:206
	ds_read2_b32 v[112:113], v155 offset0:231 offset1:239
	v_cmp_gt_i32_e32 vcc, s53, v96
	s_add_u32 s0, s18, s36
	s_waitcnt lgkmcnt(3)
	v_cvt_pk_fp8_f32 v101, v104, v106
	v_cndmask_b32_e32 v98, v166, v167, vcc
	s_addc_u32 s1, s19, s37
	v_add_u32_e32 v96, v98, v96
	v_lshl_add_u64 v[114:115], s[0:1], 0, v[140:141]
	v_ashrrev_i32_e32 v98, 31, v96
	s_waitcnt lgkmcnt(2)
	v_cvt_pk_fp8_f32 v100, v102, v108 op_sel:[0,0,1]
	v_mul_lo_u32 v98, s20, v98
	v_mul_lo_u32 v102, s21, v96
	v_mad_u64_u32 v[116:117], s[0:1], s20, v96, v[114:115]
	s_waitcnt lgkmcnt(0)
	v_cvt_pk_fp8_f32 v101, v110, v112 op_sel:[0,0,1]
	v_mov_b32_e32 v96, v139
	v_add3_u32 v117, v102, v117, v98
	v_or_b32_e32 v98, s2, v146
	v_cvt_pk_fp8_f32 v96, v99, v97
	v_mov_b32_e32 v97, v139
	v_cmp_gt_i32_e32 vcc, s53, v98
	v_cvt_pk_fp8_f32 v97, v105, v107
	global_store_dwordx2 v[116:117], v[100:101], off nt
	v_cndmask_b32_e32 v99, v166, v167, vcc
	v_add_u32_e32 v102, v99, v98
	v_ashrrev_i32_e32 v98, 31, v102
	v_mul_lo_u32 v120, s20, v98
	ds_read2_b32 v[98:99], v155 offset0:16 offset1:24
	ds_read2_b32 v[100:101], v155 offset0:49 offset1:57
	v_cvt_pk_fp8_f32 v96, v103, v109 op_sel:[0,0,1]
	v_cvt_pk_fp8_f32 v97, v111, v113 op_sel:[0,0,1]
	ds_read2_b32 v[106:107], v155 offset0:82 offset1:90
	ds_read2_b32 v[108:109], v155 offset0:148 offset1:156
	ds_read2_b32 v[110:111], v155 offset0:181 offset1:189
	ds_read2_b32 v[112:113], v155 offset0:115 offset1:123
	v_mul_lo_u32 v121, s21, v102
	v_mad_u64_u32 v[102:103], s[0:1], s20, v102, v[114:115]
	v_mov_b32_e32 v104, v139
	v_mov_b32_e32 v105, v139
	ds_read2_b32 v[116:117], v155 offset0:214 offset1:222
	ds_read2_b32 v[118:119], v155 offset0:247 offset1:255
	s_waitcnt lgkmcnt(6)
	v_cvt_pk_fp8_f32 v104, v98, v100
	s_waitcnt lgkmcnt(3)
	v_cvt_pk_fp8_f32 v105, v108, v110
	v_add3_u32 v103, v121, v103, v120
	global_store_dwordx2 v[102:103], v[96:97], off nt
	v_or_b32_e32 v96, s2, v148
	v_cmp_gt_i32_e32 vcc, s53, v96
	s_waitcnt lgkmcnt(2)
	v_cvt_pk_fp8_f32 v104, v106, v112 op_sel:[0,0,1]
	s_waitcnt lgkmcnt(0)
	v_cvt_pk_fp8_f32 v105, v116, v118 op_sel:[0,0,1]
	v_cndmask_b32_e32 v97, v166, v167, vcc
	v_add_u32_e32 v96, v97, v96
	v_ashrrev_i32_e32 v97, 31, v96
	v_mov_b32_e32 v98, v139
	v_mul_lo_u32 v100, s20, v97
	v_mul_lo_u32 v102, s21, v96
	v_mad_u64_u32 v[96:97], s[0:1], s20, v96, v[114:115]
	v_cvt_pk_fp8_f32 v98, v99, v101
	v_mov_b32_e32 v99, v139
	v_cvt_pk_fp8_f32 v99, v109, v111
	v_add3_u32 v97, v102, v97, v100
	global_store_dwordx2 v[96:97], v[104:105], off nt
	v_or_b32_e32 v96, s2, v150
	v_cmp_gt_i32_e32 vcc, s53, v96
	v_cvt_pk_fp8_f32 v98, v107, v113 op_sel:[0,0,1]
	v_cvt_pk_fp8_f32 v99, v117, v119 op_sel:[0,0,1]
	v_cndmask_b32_e32 v97, v166, v167, vcc
	v_add_u32_e32 v96, v97, v96
	v_ashrrev_i32_e32 v97, 31, v96
	v_mul_lo_u32 v100, s20, v97
	v_mul_lo_u32 v101, s21, v96
	v_mad_u64_u32 v[96:97], s[0:1], s20, v96, v[114:115]
	v_add3_u32 v97, v101, v97, v100
	global_store_dwordx2 v[96:97], v[98:99], off nt
	s_waitcnt lgkmcnt(0)
	s_mov_b64 s[0:1], 0

.LBB0_351:
	s_abs_i32 s0, s60
	s_mul_hi_u32 s1, s0, s56
	s_mul_i32 s1, s1, s4
	s_sub_i32 s0, s0, s1
	v_add_u32_e32 v96, 0x420, v154
	s_sub_i32 s1, s0, s4
	ds_write2_b32 v96, v100, v101 offset1:1
	v_add_u32_e32 v96, 0x428, v154
	s_cmp_ge_u32 s0, s4
	ds_write2_b32 v96, v102, v103 offset1:1
	s_cselect_b32 s0, s1, s0
	s_sub_i32 s1, s0, s4
	s_waitcnt lgkmcnt(0)
	s_cmp_ge_u32 s0, s4
	ds_read2_b32 v[96:97], v155 offset0:33 offset1:41
	ds_read2_b32 v[98:99], v155 offset1:8
	s_cselect_b32 s0, s1, s0
	ds_read2_b32 v[102:103], v155 offset0:66 offset1:74
	ds_read2_b32 v[104:105], v155 offset0:132 offset1:140
	ds_read2_b32 v[106:107], v155 offset0:165 offset1:173
	ds_read2_b32 v[108:109], v155 offset0:99 offset1:107
	s_xor_b32 s0, s0, s59
	s_sub_i32 s0, s0, s59
	s_lshl_b32 s0, s0, 5
	v_mov_b32_e32 v100, v139
	v_mov_b32_e32 v101, v139
	ds_read2_b32 v[110:111], v155 offset0:198 offset1:206
	ds_read2_b32 v[112:113], v155 offset0:231 offset1:239
	s_add_i32 s2, s0, 0xfffff600
	s_waitcnt lgkmcnt(6)
	v_cvt_pk_fp8_f32 v100, v98, v96
	s_waitcnt lgkmcnt(3)
	v_cvt_pk_fp8_f32 v101, v104, v106
	s_add_u32 s0, s18, s36
	s_addc_u32 s1, s19, s37
	v_lshl_add_u64 v[114:115], s[0:1], 0, v[140:141]
	v_or_b32_e32 v96, s2, v136
	s_waitcnt lgkmcnt(2)
	v_cvt_pk_fp8_f32 v100, v102, v108 op_sel:[0,0,1]
	s_waitcnt lgkmcnt(0)
	v_cvt_pk_fp8_f32 v101, v110, v112 op_sel:[0,0,1]
	v_mul_lo_u32 v98, s21, v96
	v_mad_u64_u32 v[116:117], s[0:1], s20, v96, v[114:115]
	v_mov_b32_e32 v96, v139
	s_ashr_i32 s0, s2, 31
	v_cvt_pk_fp8_f32 v96, v99, v97
	v_mov_b32_e32 v97, v139
	s_mul_i32 s3, s20, s0
	v_cvt_pk_fp8_f32 v97, v105, v107
	v_add3_u32 v117, v98, v117, s3
	global_store_dwordx2 v[116:117], v[100:101], off nt
	ds_read2_b32 v[98:99], v155 offset0:16 offset1:24
	ds_read2_b32 v[100:101], v155 offset0:49 offset1:57
	v_cvt_pk_fp8_f32 v96, v103, v109 op_sel:[0,0,1]
	v_cvt_pk_fp8_f32 v97, v111, v113 op_sel:[0,0,1]
	ds_read2_b32 v[106:107], v155 offset0:82 offset1:90
	ds_read2_b32 v[108:109], v155 offset0:148 offset1:156
	ds_read2_b32 v[110:111], v155 offset0:181 offset1:189
	ds_read2_b32 v[112:113], v155 offset0:115 offset1:123
	v_mov_b32_e32 v104, v139
	v_mov_b32_e32 v105, v139
	ds_read2_b32 v[116:117], v155 offset0:214 offset1:222
	ds_read2_b32 v[118:119], v155 offset0:247 offset1:255
	s_waitcnt lgkmcnt(6)
	v_cvt_pk_fp8_f32 v104, v98, v100
	s_waitcnt lgkmcnt(3)
	v_cvt_pk_fp8_f32 v105, v108, v110
	v_mov_b32_e32 v98, v139
	v_or_b32_e32 v102, s2, v146
	v_cvt_pk_fp8_f32 v98, v99, v101
	v_mov_b32_e32 v99, v139
	v_mul_lo_u32 v120, s21, v102
	v_mad_u64_u32 v[102:103], s[0:1], s20, v102, v[114:115]
	v_cvt_pk_fp8_f32 v99, v109, v111
	v_add3_u32 v103, v120, v103, s3
	s_waitcnt lgkmcnt(2)
	v_cvt_pk_fp8_f32 v104, v106, v112 op_sel:[0,0,1]
	s_waitcnt lgkmcnt(0)
	v_cvt_pk_fp8_f32 v105, v116, v118 op_sel:[0,0,1]
	global_store_dwordx2 v[102:103], v[96:97], off nt
	v_or_b32_e32 v96, s2, v148
	v_mul_lo_u32 v100, s21, v96
	v_mad_u64_u32 v[96:97], s[0:1], s20, v96, v[114:115]
	v_add3_u32 v97, v100, v97, s3
	v_cvt_pk_fp8_f32 v98, v107, v113 op_sel:[0,0,1]
	v_cvt_pk_fp8_f32 v99, v117, v119 op_sel:[0,0,1]
	global_store_dwordx2 v[96:97], v[104:105], off nt
	v_or_b32_e32 v96, s2, v150
	v_mul_lo_u32 v100, s21, v96
	v_mad_u64_u32 v[96:97], s[0:1], s20, v96, v[114:115]
	v_add3_u32 v97, v100, v97, s3
	global_store_dwordx2 v[96:97], v[98:99], off nt
	s_waitcnt lgkmcnt(0)

.LBB0_371:
	s_abs_i32 s0, s60
	s_mul_hi_u32 s1, s0, s56
	s_mul_i32 s1, s1, s4
	s_sub_i32 s0, s0, s1
	v_add_u32_e32 v96, 0x420, v154
	s_sub_i32 s1, s0, s4
	ds_write2_b32 v96, v100, v101 offset1:1
	v_add_u32_e32 v96, 0x428, v154
	s_cmp_ge_u32 s0, s4
	ds_write2_b32 v96, v102, v103 offset1:1
	s_cselect_b32 s0, s1, s0
	s_sub_i32 s1, s0, s4
	s_waitcnt lgkmcnt(0)
	s_cmp_ge_u32 s0, s4
	ds_read2_b32 v[96:97], v155 offset0:33 offset1:41
	ds_read2_b32 v[98:99], v155 offset1:8
	s_cselect_b32 s0, s1, s0
	ds_read2_b32 v[102:103], v155 offset0:66 offset1:74
	ds_read2_b32 v[104:105], v155 offset0:132 offset1:140
	ds_read2_b32 v[106:107], v155 offset0:165 offset1:173
	ds_read2_b32 v[108:109], v155 offset0:99 offset1:107
	s_xor_b32 s0, s0, s59
	s_sub_i32 s0, s0, s59
	s_lshl_b32 s0, s0, 5
	v_mov_b32_e32 v100, v139
	v_mov_b32_e32 v101, v139
	ds_read2_b32 v[110:111], v155 offset0:198 offset1:206
	ds_read2_b32 v[112:113], v155 offset0:231 offset1:239
	s_add_i32 s2, s0, 0xfffff000
	s_waitcnt lgkmcnt(6)
	v_cvt_pk_fp8_f32 v100, v98, v96
	s_waitcnt lgkmcnt(3)
	v_cvt_pk_fp8_f32 v101, v104, v106
	s_add_u32 s0, s18, s36
	s_addc_u32 s1, s19, s37
	v_lshl_add_u64 v[114:115], s[0:1], 0, v[140:141]
	v_or_b32_e32 v96, s2, v136
	s_waitcnt lgkmcnt(2)
	v_cvt_pk_fp8_f32 v100, v102, v108 op_sel:[0,0,1]
	s_waitcnt lgkmcnt(0)
	v_cvt_pk_fp8_f32 v101, v110, v112 op_sel:[0,0,1]
	v_mul_lo_u32 v98, s21, v96
	v_mad_u64_u32 v[116:117], s[0:1], s20, v96, v[114:115]
	v_mov_b32_e32 v96, v139
	s_ashr_i32 s0, s2, 31
	v_cvt_pk_fp8_f32 v96, v99, v97
	v_mov_b32_e32 v97, v139
	s_mul_i32 s3, s20, s0
	v_cvt_pk_fp8_f32 v97, v105, v107
	v_add3_u32 v117, v98, v117, s3
	global_store_dwordx2 v[116:117], v[100:101], off nt
	ds_read2_b32 v[98:99], v155 offset0:16 offset1:24
	ds_read2_b32 v[100:101], v155 offset0:49 offset1:57
	v_cvt_pk_fp8_f32 v96, v103, v109 op_sel:[0,0,1]
	v_cvt_pk_fp8_f32 v97, v111, v113 op_sel:[0,0,1]
	ds_read2_b32 v[106:107], v155 offset0:82 offset1:90
	ds_read2_b32 v[108:109], v155 offset0:148 offset1:156
	ds_read2_b32 v[110:111], v155 offset0:181 offset1:189
	ds_read2_b32 v[112:113], v155 offset0:115 offset1:123
	v_mov_b32_e32 v104, v139
	v_mov_b32_e32 v105, v139
	ds_read2_b32 v[116:117], v155 offset0:214 offset1:222
	ds_read2_b32 v[118:119], v155 offset0:247 offset1:255
	s_waitcnt lgkmcnt(6)
	v_cvt_pk_fp8_f32 v104, v98, v100
	s_waitcnt lgkmcnt(3)
	v_cvt_pk_fp8_f32 v105, v108, v110
	v_mov_b32_e32 v98, v139
	v_or_b32_e32 v102, s2, v146
	v_cvt_pk_fp8_f32 v98, v99, v101
	v_mov_b32_e32 v99, v139
	v_mul_lo_u32 v120, s21, v102
	v_mad_u64_u32 v[102:103], s[0:1], s20, v102, v[114:115]
	v_cvt_pk_fp8_f32 v99, v109, v111
	v_add3_u32 v103, v120, v103, s3
	s_waitcnt lgkmcnt(2)
	v_cvt_pk_fp8_f32 v104, v106, v112 op_sel:[0,0,1]
	s_waitcnt lgkmcnt(0)
	v_cvt_pk_fp8_f32 v105, v116, v118 op_sel:[0,0,1]
	global_store_dwordx2 v[102:103], v[96:97], off nt
	v_or_b32_e32 v96, s2, v148
	v_mul_lo_u32 v100, s21, v96
	v_mad_u64_u32 v[96:97], s[0:1], s20, v96, v[114:115]
	v_add3_u32 v97, v100, v97, s3
	v_cvt_pk_fp8_f32 v98, v107, v113 op_sel:[0,0,1]
	v_cvt_pk_fp8_f32 v99, v117, v119 op_sel:[0,0,1]
	global_store_dwordx2 v[96:97], v[104:105], off nt
	v_or_b32_e32 v96, s2, v150
	v_mul_lo_u32 v100, s21, v96
	v_mad_u64_u32 v[96:97], s[0:1], s20, v96, v[114:115]
	v_add3_u32 v97, v100, v97, s3
	global_store_dwordx2 v[96:97], v[98:99], off nt
	s_waitcnt lgkmcnt(0)

.LBB0_396:
	s_abs_i32 s2, s60
	s_mul_hi_u32 s3, s2, s56
	s_mul_i32 s3, s3, s4
	v_add_u32_e32 v96, 0x420, v154
	s_sub_i32 s2, s2, s3
	ds_write2_b32 v96, v100, v101 offset1:1
	v_add_u32_e32 v96, 0x428, v154
	s_sub_i32 s3, s2, s4
	ds_write2_b32 v96, v102, v103 offset1:1
	s_cmp_ge_u32 s2, s4
	s_cselect_b32 s2, s3, s2
	s_waitcnt lgkmcnt(0)
	s_sub_i32 s3, s2, s4
	ds_read2_b32 v[96:97], v155 offset0:33 offset1:41
	ds_read2_b32 v[98:99], v155 offset1:8
	s_cmp_ge_u32 s2, s4
	ds_read2_b32 v[102:103], v155 offset0:66 offset1:74
	ds_read2_b32 v[104:105], v155 offset0:132 offset1:140
	ds_read2_b32 v[106:107], v155 offset0:165 offset1:173
	ds_read2_b32 v[108:109], v155 offset0:99 offset1:107
	s_cselect_b32 s2, s3, s2
	s_xor_b32 s2, s2, s59
	s_sub_i32 s2, s2, s59
	v_mov_b32_e32 v100, v139
	v_mov_b32_e32 v101, v139
	ds_read2_b32 v[110:111], v155 offset0:198 offset1:206
	ds_read2_b32 v[112:113], v155 offset0:231 offset1:239
	s_lshl_b32 s38, s2, 6
	s_waitcnt lgkmcnt(6)
	v_cvt_pk_fp8_f32 v100, v98, v96
	s_waitcnt lgkmcnt(3)
	v_cvt_pk_fp8_f32 v101, v104, v106
	s_add_u32 s2, s18, s36
	s_addc_u32 s3, s19, s37
	v_lshl_add_u64 v[114:115], s[2:3], 0, v[140:141]
	v_or_b32_e32 v96, s38, v156
	s_waitcnt lgkmcnt(2)
	v_cvt_pk_fp8_f32 v100, v102, v108 op_sel:[0,0,1]
	s_waitcnt lgkmcnt(0)
	v_cvt_pk_fp8_f32 v101, v110, v112 op_sel:[0,0,1]
	v_mul_lo_u32 v98, s21, v96
	v_mad_u64_u32 v[116:117], s[2:3], s20, v96, v[114:115]
	v_mov_b32_e32 v96, v139
	s_ashr_i32 s2, s38, 31
	v_cvt_pk_fp8_f32 v96, v99, v97
	v_mov_b32_e32 v97, v139
	s_mul_i32 s37, s20, s2
	v_cvt_pk_fp8_f32 v97, v105, v107
	v_add3_u32 v117, v98, v117, s37
	global_store_dwordx2 v[116:117], v[100:101], off nt
	ds_read2_b32 v[98:99], v155 offset0:16 offset1:24
	ds_read2_b32 v[100:101], v155 offset0:49 offset1:57
	v_cvt_pk_fp8_f32 v96, v103, v109 op_sel:[0,0,1]
	v_cvt_pk_fp8_f32 v97, v111, v113 op_sel:[0,0,1]
	ds_read2_b32 v[106:107], v155 offset0:82 offset1:90
	ds_read2_b32 v[108:109], v155 offset0:148 offset1:156
	ds_read2_b32 v[110:111], v155 offset0:181 offset1:189
	ds_read2_b32 v[112:113], v155 offset0:115 offset1:123
	v_mov_b32_e32 v104, v139
	v_mov_b32_e32 v105, v139
	ds_read2_b32 v[116:117], v155 offset0:214 offset1:222
	ds_read2_b32 v[118:119], v155 offset0:247 offset1:255
	s_waitcnt lgkmcnt(6)
	v_cvt_pk_fp8_f32 v104, v98, v100
	s_waitcnt lgkmcnt(3)
	v_cvt_pk_fp8_f32 v105, v108, v110
	v_mov_b32_e32 v98, v139
	v_or_b32_e32 v102, s38, v157
	v_cvt_pk_fp8_f32 v98, v99, v101
	v_mov_b32_e32 v99, v139
	v_mul_lo_u32 v120, s21, v102
	v_mad_u64_u32 v[102:103], s[2:3], s20, v102, v[114:115]
	v_cvt_pk_fp8_f32 v99, v109, v111
	v_add3_u32 v103, v120, v103, s37
	s_waitcnt lgkmcnt(2)
	v_cvt_pk_fp8_f32 v104, v106, v112 op_sel:[0,0,1]
	s_waitcnt lgkmcnt(0)
	v_cvt_pk_fp8_f32 v105, v116, v118 op_sel:[0,0,1]
	global_store_dwordx2 v[102:103], v[96:97], off nt
	v_or_b32_e32 v96, s38, v158
	v_mul_lo_u32 v100, s21, v96
	v_mad_u64_u32 v[96:97], s[2:3], s20, v96, v[114:115]
	v_add3_u32 v97, v100, v97, s37
	v_cvt_pk_fp8_f32 v98, v107, v113 op_sel:[0,0,1]
	v_cvt_pk_fp8_f32 v99, v117, v119 op_sel:[0,0,1]
	global_store_dwordx2 v[96:97], v[104:105], off nt
	v_or_b32_e32 v96, s38, v159
	v_mul_lo_u32 v100, s21, v96
	v_mad_u64_u32 v[96:97], s[2:3], s20, v96, v[114:115]
	v_add3_u32 v97, v100, v97, s37
	global_store_dwordx2 v[96:97], v[98:99], off nt
	s_waitcnt lgkmcnt(0)
	s_mov_b64 s[2:3], 0

.LBB0_416:
	s_abs_i32 s0, s60
	s_mul_hi_u32 s1, s0, s56
	s_mul_i32 s1, s1, s4
	v_add_u32_e32 v96, 0x420, v154
	s_sub_i32 s0, s0, s1
	ds_write2_b32 v96, v100, v101 offset1:1
	v_add_u32_e32 v96, 0x428, v154
	s_sub_i32 s1, s0, s4
	ds_write2_b32 v96, v102, v103 offset1:1
	s_cmp_ge_u32 s0, s4
	s_cselect_b32 s0, s1, s0
	s_waitcnt lgkmcnt(0)
	s_sub_i32 s1, s0, s4
	ds_read2_b32 v[96:97], v155 offset0:33 offset1:41
	ds_read2_b32 v[98:99], v155 offset1:8
	s_cmp_ge_u32 s0, s4
	ds_read2_b32 v[102:103], v155 offset0:66 offset1:74
	ds_read2_b32 v[104:105], v155 offset0:132 offset1:140
	ds_read2_b32 v[106:107], v155 offset0:165 offset1:173
	ds_read2_b32 v[108:109], v155 offset0:99 offset1:107
	s_cselect_b32 s0, s1, s0
	s_xor_b32 s0, s0, s59
	s_sub_i32 s0, s0, s59
	v_mov_b32_e32 v100, v139
	v_mov_b32_e32 v101, v139
	ds_read2_b32 v[110:111], v155 offset0:198 offset1:206
	ds_read2_b32 v[112:113], v155 offset0:231 offset1:239
	s_lshl_b32 s2, s0, 6
	s_waitcnt lgkmcnt(6)
	v_cvt_pk_fp8_f32 v100, v98, v96
	s_waitcnt lgkmcnt(3)
	v_cvt_pk_fp8_f32 v101, v104, v106
	s_add_u32 s0, s18, s36
	s_addc_u32 s1, s19, s37
	v_lshl_add_u64 v[114:115], s[0:1], 0, v[140:141]
	v_or_b32_e32 v96, s2, v160
	s_waitcnt lgkmcnt(2)
	v_cvt_pk_fp8_f32 v100, v102, v108 op_sel:[0,0,1]
	s_waitcnt lgkmcnt(0)
	v_cvt_pk_fp8_f32 v101, v110, v112 op_sel:[0,0,1]
	v_mul_lo_u32 v98, s21, v96
	v_mad_u64_u32 v[116:117], s[0:1], s20, v96, v[114:115]
	v_mov_b32_e32 v96, v139
	s_ashr_i32 s0, s2, 31
	v_cvt_pk_fp8_f32 v96, v99, v97
	v_mov_b32_e32 v97, v139
	s_mul_i32 s3, s20, s0
	v_cvt_pk_fp8_f32 v97, v105, v107
	v_add3_u32 v117, v98, v117, s3
	global_store_dwordx2 v[116:117], v[100:101], off nt
	ds_read2_b32 v[98:99], v155 offset0:16 offset1:24
	ds_read2_b32 v[100:101], v155 offset0:49 offset1:57
	v_cvt_pk_fp8_f32 v96, v103, v109 op_sel:[0,0,1]
	v_cvt_pk_fp8_f32 v97, v111, v113 op_sel:[0,0,1]
	ds_read2_b32 v[106:107], v155 offset0:82 offset1:90
	ds_read2_b32 v[108:109], v155 offset0:148 offset1:156
	ds_read2_b32 v[110:111], v155 offset0:181 offset1:189
	ds_read2_b32 v[112:113], v155 offset0:115 offset1:123
	v_mov_b32_e32 v104, v139
	v_mov_b32_e32 v105, v139
	ds_read2_b32 v[116:117], v155 offset0:214 offset1:222
	ds_read2_b32 v[118:119], v155 offset0:247 offset1:255
	s_waitcnt lgkmcnt(6)
	v_cvt_pk_fp8_f32 v104, v98, v100
	s_waitcnt lgkmcnt(3)
	v_cvt_pk_fp8_f32 v105, v108, v110
	v_mov_b32_e32 v98, v139
	v_or_b32_e32 v102, s2, v161
	v_cvt_pk_fp8_f32 v98, v99, v101
	v_mov_b32_e32 v99, v139
	v_mul_lo_u32 v120, s21, v102
	v_mad_u64_u32 v[102:103], s[0:1], s20, v102, v[114:115]
	v_cvt_pk_fp8_f32 v99, v109, v111
	v_add3_u32 v103, v120, v103, s3
	s_waitcnt lgkmcnt(2)
	v_cvt_pk_fp8_f32 v104, v106, v112 op_sel:[0,0,1]
	s_waitcnt lgkmcnt(0)
	v_cvt_pk_fp8_f32 v105, v116, v118 op_sel:[0,0,1]
	global_store_dwordx2 v[102:103], v[96:97], off nt
	v_or_b32_e32 v96, s2, v162
	v_mul_lo_u32 v100, s21, v96
	v_mad_u64_u32 v[96:97], s[0:1], s20, v96, v[114:115]
	v_add3_u32 v97, v100, v97, s3
	v_cvt_pk_fp8_f32 v98, v107, v113 op_sel:[0,0,1]
	v_cvt_pk_fp8_f32 v99, v117, v119 op_sel:[0,0,1]
	global_store_dwordx2 v[96:97], v[104:105], off nt
	v_or_b32_e32 v96, s2, v163
	v_mul_lo_u32 v100, s21, v96
	v_mad_u64_u32 v[96:97], s[0:1], s20, v96, v[114:115]
	v_add3_u32 v97, v100, v97, s3
	global_store_dwordx2 v[96:97], v[98:99], off nt
	s_waitcnt lgkmcnt(0)
	s_branch .LBB0_435

.LBB0_434:
	s_abs_i32 s0, s60
	s_mul_hi_u32 s1, s0, s56
	s_mul_i32 s1, s1, s4
	v_add_u32_e32 v64, 0x420, v154
	s_sub_i32 s0, s0, s1
	ds_write2_b32 v64, v68, v69 offset1:1
	v_add_u32_e32 v64, 0x428, v154
	s_sub_i32 s1, s0, s4
	ds_write2_b32 v64, v70, v71 offset1:1
	s_cmp_ge_u32 s0, s4
	s_cselect_b32 s0, s1, s0
	s_waitcnt lgkmcnt(0)
	s_sub_i32 s1, s0, s4
	ds_read2_b32 v[64:65], v155 offset0:33 offset1:41
	ds_read2_b32 v[66:67], v155 offset1:8
	s_cmp_ge_u32 s0, s4
	ds_read2_b32 v[70:71], v155 offset0:66 offset1:74
	ds_read2_b32 v[72:73], v155 offset0:132 offset1:140
	ds_read2_b32 v[74:75], v155 offset0:165 offset1:173
	ds_read2_b32 v[76:77], v155 offset0:99 offset1:107
	s_cselect_b32 s0, s1, s0
	s_xor_b32 s0, s0, s59
	s_sub_i32 s0, s0, s59
	v_mov_b32_e32 v68, v139
	v_mov_b32_e32 v69, v139
	ds_read2_b32 v[78:79], v155 offset0:198 offset1:206
	ds_read2_b32 v[80:81], v155 offset0:231 offset1:239
	s_lshl_b32 s2, s0, 5
	s_waitcnt lgkmcnt(6)
	v_cvt_pk_fp8_f32 v68, v66, v64
	s_waitcnt lgkmcnt(3)
	v_cvt_pk_fp8_f32 v69, v72, v74
	s_add_u32 s0, s18, s36
	s_addc_u32 s1, s19, s37
	v_lshl_add_u64 v[82:83], s[0:1], 0, v[140:141]
	v_or_b32_e32 v64, s2, v136
	s_waitcnt lgkmcnt(2)
	v_cvt_pk_fp8_f32 v68, v70, v76 op_sel:[0,0,1]
	s_waitcnt lgkmcnt(0)
	v_cvt_pk_fp8_f32 v69, v78, v80 op_sel:[0,0,1]
	v_mul_lo_u32 v66, s21, v64
	v_mad_u64_u32 v[84:85], s[0:1], s20, v64, v[82:83]
	v_mov_b32_e32 v64, v139
	s_ashr_i32 s0, s2, 31
	v_cvt_pk_fp8_f32 v64, v67, v65
	v_mov_b32_e32 v65, v139
	s_mul_i32 s3, s20, s0
	v_cvt_pk_fp8_f32 v65, v73, v75
	v_add3_u32 v85, v66, v85, s3
	global_store_dwordx2 v[84:85], v[68:69], off nt
	ds_read2_b32 v[66:67], v155 offset0:16 offset1:24
	ds_read2_b32 v[68:69], v155 offset0:49 offset1:57
	v_cvt_pk_fp8_f32 v64, v71, v77 op_sel:[0,0,1]
	v_cvt_pk_fp8_f32 v65, v79, v81 op_sel:[0,0,1]
	ds_read2_b32 v[74:75], v155 offset0:82 offset1:90
	ds_read2_b32 v[76:77], v155 offset0:148 offset1:156
	ds_read2_b32 v[78:79], v155 offset0:181 offset1:189
	ds_read2_b32 v[80:81], v155 offset0:115 offset1:123
	v_mov_b32_e32 v72, v139
	v_mov_b32_e32 v73, v139
	ds_read2_b32 v[84:85], v155 offset0:214 offset1:222
	ds_read2_b32 v[86:87], v155 offset0:247 offset1:255
	s_waitcnt lgkmcnt(6)
	v_cvt_pk_fp8_f32 v72, v66, v68
	s_waitcnt lgkmcnt(3)
	v_cvt_pk_fp8_f32 v73, v76, v78
	v_mov_b32_e32 v66, v139
	v_or_b32_e32 v70, s2, v146
	v_cvt_pk_fp8_f32 v66, v67, v69
	v_mov_b32_e32 v67, v139
	v_mul_lo_u32 v88, s21, v70
	v_mad_u64_u32 v[70:71], s[0:1], s20, v70, v[82:83]
	v_cvt_pk_fp8_f32 v67, v77, v79
	v_add3_u32 v71, v88, v71, s3
	s_waitcnt lgkmcnt(2)
	v_cvt_pk_fp8_f32 v72, v74, v80 op_sel:[0,0,1]
	s_waitcnt lgkmcnt(0)
	v_cvt_pk_fp8_f32 v73, v84, v86 op_sel:[0,0,1]
	global_store_dwordx2 v[70:71], v[64:65], off nt
	v_or_b32_e32 v64, s2, v148
	v_mul_lo_u32 v68, s21, v64
	v_mad_u64_u32 v[64:65], s[0:1], s20, v64, v[82:83]
	v_add3_u32 v65, v68, v65, s3
	v_cvt_pk_fp8_f32 v66, v75, v81 op_sel:[0,0,1]
	v_cvt_pk_fp8_f32 v67, v85, v87 op_sel:[0,0,1]
	global_store_dwordx2 v[64:65], v[72:73], off nt
	v_or_b32_e32 v64, s2, v150
	v_mul_lo_u32 v68, s21, v64
	v_mad_u64_u32 v[64:65], s[0:1], s20, v64, v[82:83]
	v_add3_u32 v65, v68, v65, s3
	global_store_dwordx2 v[64:65], v[66:67], off nt
	s_waitcnt lgkmcnt(0)

.LBB0_451:
	v_add_u32_e32 v68, 0x420, v154
	ds_write2_b32 v68, v64, v65 offset1:1
	v_add_u32_e32 v64, 0x428, v154
	s_mul_i32 s38, s38, s4
	ds_write2_b32 v64, v66, v67 offset1:1
	s_sub_i32 s0, s60, s38
	s_waitcnt lgkmcnt(0)
	s_lshl_b32 s2, s0, 6
	s_lshl_b64 s[0:1], s[36:37], 1
	s_add_u32 s0, s18, s0
	ds_read2_b32 v[68:69], v155 offset0:33 offset1:41
	ds_read2_b32 v[70:71], v155 offset1:8
	ds_read2_b32 v[72:73], v155 offset0:66 offset1:74
	ds_read2_b32 v[74:75], v155 offset0:99 offset1:107
	ds_read2_b32 v[76:77], v155 offset0:132 offset1:140
	ds_read2_b32 v[78:79], v155 offset0:165 offset1:173
	ds_read2_b32 v[80:81], v155 offset0:198 offset1:206
	ds_read2_b32 v[82:83], v155 offset0:231 offset1:239
	s_addc_u32 s1, s19, s1
	v_lshlrev_b32_e32 v138, 1, v140
	s_waitcnt lgkmcnt(6)
	s_nop 1
	v_cvt_pk_bf16_f32 v64, v70, v68
	v_or_b32_e32 v68, s2, v160
	v_lshl_add_u64 v[84:85], s[0:1], 0, v[138:139]
	v_mad_u64_u32 v[86:87], s[0:1], s20, v68, 0
	s_ashr_i32 s0, s2, 31
	v_mul_lo_u32 v70, s21, v68
	s_mul_i32 s3, s20, s0
	v_add3_u32 v87, v87, s3, v70
	v_lshl_add_u64 v[86:87], v[86:87], 1, v[84:85]
	v_or_b32_e32 v68, s2, v161
	s_waitcnt lgkmcnt(4)
	s_nop 1
	v_cvt_pk_bf16_f32 v65, v72, v74
	s_waitcnt lgkmcnt(2)
	s_nop 1
	v_cvt_pk_bf16_f32 v66, v76, v78
	s_waitcnt lgkmcnt(0)
	s_nop 1
	v_cvt_pk_bf16_f32 v67, v80, v82
	global_store_dwordx4 v[86:87], v[64:67], off nt
	v_mul_lo_u32 v70, s21, v68
	s_nop 0
	s_nop 1
	v_cvt_pk_bf16_f32 v64, v71, v69
	v_mad_u64_u32 v[68:69], s[0:1], s20, v68, 0
	v_add3_u32 v69, v69, s3, v70
	s_nop 1
	v_cvt_pk_bf16_f32 v65, v73, v75
	s_nop 1
	v_cvt_pk_bf16_f32 v66, v77, v79
	s_nop 1
	v_cvt_pk_bf16_f32 v67, v81, v83
	v_lshl_add_u64 v[68:69], v[68:69], 1, v[84:85]
	ds_read2_b32 v[70:71], v155 offset0:16 offset1:24
	ds_read2_b32 v[72:73], v155 offset0:49 offset1:57
	ds_read2_b32 v[74:75], v155 offset0:82 offset1:90
	ds_read2_b32 v[76:77], v155 offset0:115 offset1:123
	ds_read2_b32 v[78:79], v155 offset0:148 offset1:156
	ds_read2_b32 v[80:81], v155 offset0:181 offset1:189
	ds_read2_b32 v[82:83], v155 offset0:214 offset1:222
	ds_read2_b32 v[86:87], v155 offset0:247 offset1:255
	global_store_dwordx4 v[68:69], v[64:67], off nt
	v_or_b32_e32 v68, s2, v162
	s_waitcnt lgkmcnt(6)
	s_nop 1
	v_cvt_pk_bf16_f32 v64, v70, v72
	v_mul_lo_u32 v70, s21, v68
	v_mad_u64_u32 v[68:69], s[0:1], s20, v68, 0
	v_add3_u32 v69, v69, s3, v70
	v_lshl_add_u64 v[68:69], v[68:69], 1, v[84:85]
	s_waitcnt lgkmcnt(4)
	s_nop 1
	v_cvt_pk_bf16_f32 v65, v74, v76
	s_waitcnt lgkmcnt(2)
	s_nop 1
	v_cvt_pk_bf16_f32 v66, v78, v80
	s_waitcnt lgkmcnt(0)
	s_nop 1
	v_cvt_pk_bf16_f32 v67, v82, v86
	global_store_dwordx4 v[68:69], v[64:67], off nt
	v_or_b32_e32 v68, s2, v163
	v_mul_lo_u32 v70, s21, v68
	v_mad_u64_u32 v[68:69], s[0:1], s20, v68, 0
	v_add3_u32 v69, v69, s3, v70
	v_lshl_add_u64 v[68:69], v[68:69], 1, v[84:85]
	s_nop 1
	v_cvt_pk_bf16_f32 v64, v71, v73
	s_nop 1
	v_cvt_pk_bf16_f32 v65, v75, v77
	s_nop 1
	v_cvt_pk_bf16_f32 v66, v79, v81
	s_nop 1
	v_cvt_pk_bf16_f32 v67, v83, v87
	global_store_dwordx4 v[68:69], v[64:67], off nt
	s_waitcnt lgkmcnt(0)
	s_mov_b64 s[0:1], 0

.LBB0_465:
	s_abs_i32 s0, s60
	s_mul_hi_u32 s1, s0, s56
	s_mul_i32 s1, s1, s4
	s_sub_i32 s0, s0, s1
	s_sub_i32 s1, s0, s4
	s_cmp_ge_u32 s0, s4
	s_cselect_b32 s0, s1, s0
	s_sub_i32 s1, s0, s4
	s_cmp_ge_u32 s0, s4
	v_add_u32_e32 v68, 0x420, v154
	s_cselect_b32 s0, s1, s0
	ds_write2_b32 v68, v64, v65 offset1:1
	v_add_u32_e32 v64, 0x428, v154
	s_xor_b32 s0, s0, s59
	ds_write2_b32 v64, v66, v67 offset1:1
	s_sub_i32 s0, s0, s59
	s_waitcnt lgkmcnt(0)
	s_lshl_b32 s2, s0, 6
	s_lshl_b64 s[0:1], s[36:37], 1
	s_add_u32 s0, s18, s0
	ds_read2_b32 v[68:69], v155 offset0:33 offset1:41
	ds_read2_b32 v[70:71], v155 offset1:8
	ds_read2_b32 v[72:73], v155 offset0:66 offset1:74
	ds_read2_b32 v[74:75], v155 offset0:99 offset1:107
	ds_read2_b32 v[76:77], v155 offset0:132 offset1:140
	ds_read2_b32 v[78:79], v155 offset0:165 offset1:173
	ds_read2_b32 v[80:81], v155 offset0:198 offset1:206
	ds_read2_b32 v[82:83], v155 offset0:231 offset1:239
	s_addc_u32 s1, s19, s1
	v_lshlrev_b32_e32 v138, 1, v140
	s_waitcnt lgkmcnt(6)
	s_nop 1
	v_cvt_pk_bf16_f32 v64, v70, v68
	v_or_b32_e32 v68, s2, v156
	v_lshl_add_u64 v[84:85], s[0:1], 0, v[138:139]
	v_mad_u64_u32 v[86:87], s[0:1], s20, v68, 0
	s_ashr_i32 s0, s2, 31
	v_mul_lo_u32 v70, s21, v68
	s_mul_i32 s3, s20, s0
	v_add3_u32 v87, v87, s3, v70
	v_lshl_add_u64 v[86:87], v[86:87], 1, v[84:85]
	v_or_b32_e32 v68, s2, v157
	s_waitcnt lgkmcnt(4)
	s_nop 1
	v_cvt_pk_bf16_f32 v65, v72, v74
	s_waitcnt lgkmcnt(2)
	s_nop 1
	v_cvt_pk_bf16_f32 v66, v76, v78
	s_waitcnt lgkmcnt(0)
	s_nop 1
	v_cvt_pk_bf16_f32 v67, v80, v82
	global_store_dwordx4 v[86:87], v[64:67], off nt
	v_mul_lo_u32 v70, s21, v68
	s_nop 0
	s_nop 1
	v_cvt_pk_bf16_f32 v64, v71, v69
	v_mad_u64_u32 v[68:69], s[0:1], s20, v68, 0
	v_add3_u32 v69, v69, s3, v70
	s_nop 1
	v_cvt_pk_bf16_f32 v65, v73, v75
	s_nop 1
	v_cvt_pk_bf16_f32 v66, v77, v79
	s_nop 1
	v_cvt_pk_bf16_f32 v67, v81, v83
	v_lshl_add_u64 v[68:69], v[68:69], 1, v[84:85]
	ds_read2_b32 v[70:71], v155 offset0:16 offset1:24
	ds_read2_b32 v[72:73], v155 offset0:49 offset1:57
	ds_read2_b32 v[74:75], v155 offset0:82 offset1:90
	ds_read2_b32 v[76:77], v155 offset0:115 offset1:123
	ds_read2_b32 v[78:79], v155 offset0:148 offset1:156
	ds_read2_b32 v[80:81], v155 offset0:181 offset1:189
	ds_read2_b32 v[82:83], v155 offset0:214 offset1:222
	ds_read2_b32 v[86:87], v155 offset0:247 offset1:255
	global_store_dwordx4 v[68:69], v[64:67], off nt
	v_or_b32_e32 v68, s2, v158
	s_waitcnt lgkmcnt(6)
	s_nop 1
	v_cvt_pk_bf16_f32 v64, v70, v72
	v_mul_lo_u32 v70, s21, v68
	v_mad_u64_u32 v[68:69], s[0:1], s20, v68, 0
	v_add3_u32 v69, v69, s3, v70
	v_lshl_add_u64 v[68:69], v[68:69], 1, v[84:85]
	s_waitcnt lgkmcnt(4)
	s_nop 1
	v_cvt_pk_bf16_f32 v65, v74, v76
	s_waitcnt lgkmcnt(2)
	s_nop 1
	v_cvt_pk_bf16_f32 v66, v78, v80
	s_waitcnt lgkmcnt(0)
	s_nop 1
	v_cvt_pk_bf16_f32 v67, v82, v86
	global_store_dwordx4 v[68:69], v[64:67], off nt
	v_or_b32_e32 v68, s2, v159
	v_mul_lo_u32 v70, s21, v68
	v_mad_u64_u32 v[68:69], s[0:1], s20, v68, 0
	v_add3_u32 v69, v69, s3, v70
	v_lshl_add_u64 v[68:69], v[68:69], 1, v[84:85]
	s_nop 1
	v_cvt_pk_bf16_f32 v64, v71, v73
	s_nop 1
	v_cvt_pk_bf16_f32 v65, v75, v77
	s_nop 1
	v_cvt_pk_bf16_f32 v66, v79, v81
	s_nop 1
	v_cvt_pk_bf16_f32 v67, v83, v87
	global_store_dwordx4 v[68:69], v[64:67], off nt
	s_waitcnt lgkmcnt(0)
	s_mov_b64 s[0:1], 0

.LBB0_479:
	s_abs_i32 s0, s60
	s_mul_hi_u32 s1, s0, s56
	s_mul_i32 s1, s1, s4
	s_sub_i32 s0, s0, s1
	s_sub_i32 s1, s0, s4
	s_cmp_ge_u32 s0, s4
	s_cselect_b32 s0, s1, s0
	s_sub_i32 s1, s0, s4
	s_cmp_ge_u32 s0, s4
	s_cselect_b32 s0, s1, s0
	s_xor_b32 s0, s0, s59
	s_sub_i32 s0, s0, s59
	s_lshl_b32 s38, s0, 5
	v_add_u32_e32 v68, 0x420, v154
	s_cmpk_lt_u32 s38, 0xa00
	ds_write2_b32 v68, v64, v65 offset1:1
	v_add_u32_e32 v64, 0x428, v154
	s_cselect_b64 s[0:1], -1, 0
	s_cmpk_lt_u32 s38, 0xe00
	ds_write2_b32 v64, v66, v67 offset1:1
	s_cselect_b64 s[2:3], -1, 0
	s_waitcnt lgkmcnt(0)
	s_and_b64 s[2:3], s[2:3], exec
	ds_read2_b32 v[68:69], v155 offset0:33 offset1:41
	ds_read2_b32 v[70:71], v155 offset1:8
	ds_read2_b32 v[72:73], v155 offset0:66 offset1:74
	ds_read2_b32 v[74:75], v155 offset0:99 offset1:107
	ds_read2_b32 v[76:77], v155 offset0:132 offset1:140
	ds_read2_b32 v[78:79], v155 offset0:165 offset1:173
	ds_read2_b32 v[80:81], v155 offset0:198 offset1:206
	ds_read2_b32 v[82:83], v155 offset0:231 offset1:239
	s_cselect_b32 s2, s54, 0xfffffa00
	s_cselect_b32 s3, s31, s19
	s_cselect_b32 s39, s30, s18
	s_and_b64 s[0:1], s[0:1], exec
	s_waitcnt lgkmcnt(6)
	s_nop 1
	v_cvt_pk_bf16_f32 v64, v70, v68
	v_or_b32_e32 v68, s38, v136
	s_cselect_b32 s0, 0xfffffe00, s2
	v_mov_b32_e32 v88, s0
	v_cmp_gt_i32_e32 vcc, s52, v68
	s_cselect_b32 s1, s18, s39
	s_cselect_b32 s2, s19, s3
	v_cndmask_b32_e32 v70, v88, v165, vcc
	v_add_u32_e32 v68, v70, v68
	v_ashrrev_i32_e32 v70, 31, v68
	s_waitcnt lgkmcnt(4)
	s_nop 1
	v_cvt_pk_bf16_f32 v65, v72, v74
	v_mov_b32_e32 v89, s2
	v_mov_b32_e32 v90, s31
	v_mov_b32_e32 v91, s1
	s_waitcnt vmcnt(9)
	v_mov_b32_e32 v92, s30
	v_mul_lo_u32 v70, s20, v70
	v_mul_lo_u32 v72, s21, v68
	v_mad_u64_u32 v[86:87], s[0:1], s20, v68, 0
	v_cndmask_b32_e32 v85, v89, v90, vcc
	v_cndmask_b32_e32 v84, v91, v92, vcc
	v_add3_u32 v87, v87, v70, v72
	v_lshl_add_u64 v[84:85], v[86:87], 1, v[84:85]
	s_lshl_b64 s[0:1], s[36:37], 1
	v_lshl_add_u64 v[84:85], v[84:85], 0, s[0:1]
	v_lshlrev_b32_e32 v138, 1, v140
	v_or_b32_e32 v70, s38, v146
	v_lshl_add_u64 v[84:85], v[84:85], 0, v[138:139]
	v_cmp_gt_i32_e32 vcc, s52, v70
	s_waitcnt lgkmcnt(2)
	s_nop 1
	v_cvt_pk_bf16_f32 v66, v76, v78
	s_waitcnt lgkmcnt(0)
	s_nop 1
	v_cvt_pk_bf16_f32 v67, v80, v82
	global_store_dwordx4 v[84:85], v[64:67], off nt
	v_cndmask_b32_e32 v68, v91, v92, vcc
	s_nop 0
	s_nop 1
	v_cvt_pk_bf16_f32 v64, v71, v69
	v_cndmask_b32_e32 v71, v88, v165, vcc
	v_add_u32_e32 v70, v71, v70
	v_ashrrev_i32_e32 v71, 31, v70
	s_nop 1
	v_cvt_pk_bf16_f32 v65, v73, v75
	v_mul_lo_u32 v72, s20, v71
	v_mul_lo_u32 v73, s21, v70
	v_mad_u64_u32 v[70:71], s[2:3], s20, v70, 0
	v_cndmask_b32_e32 v69, v89, v90, vcc
	v_add3_u32 v71, v71, v72, v73
	v_lshl_add_u64 v[68:69], v[70:71], 1, v[68:69]
	v_lshl_add_u64 v[68:69], v[68:69], 0, s[0:1]
	s_nop 1
	v_cvt_pk_bf16_f32 v66, v77, v79
	s_nop 1
	v_cvt_pk_bf16_f32 v67, v81, v83
	v_lshl_add_u64 v[68:69], v[68:69], 0, v[138:139]
	ds_read2_b32 v[70:71], v155 offset0:16 offset1:24
	ds_read2_b32 v[72:73], v155 offset0:49 offset1:57
	ds_read2_b32 v[74:75], v155 offset0:82 offset1:90
	ds_read2_b32 v[76:77], v155 offset0:115 offset1:123
	ds_read2_b32 v[78:79], v155 offset0:148 offset1:156
	ds_read2_b32 v[80:81], v155 offset0:181 offset1:189
	ds_read2_b32 v[82:83], v155 offset0:214 offset1:222
	ds_read2_b32 v[84:85], v155 offset0:247 offset1:255
	global_store_dwordx4 v[68:69], v[64:67], off nt
	s_waitcnt lgkmcnt(6)
	s_nop 0
	s_nop 1
	v_cvt_pk_bf16_f32 v64, v70, v72
	v_or_b32_e32 v70, s38, v148
	v_cmp_gt_i32_e32 vcc, s52, v70
	s_waitcnt lgkmcnt(4)
	s_nop 1
	v_cvt_pk_bf16_f32 v65, v74, v76
	s_waitcnt lgkmcnt(2)
	s_nop 1
	v_cvt_pk_bf16_f32 v66, v78, v80
	s_waitcnt lgkmcnt(0)
	s_nop 1
	v_cvt_pk_bf16_f32 v67, v82, v84
	v_cndmask_b32_e32 v72, v88, v165, vcc
	v_add_u32_e32 v70, v72, v70
	v_ashrrev_i32_e32 v72, 31, v70
	v_mul_lo_u32 v72, s20, v72
	v_mul_lo_u32 v74, s21, v70
	v_mad_u64_u32 v[86:87], s[2:3], s20, v70, 0
	v_cndmask_b32_e32 v69, v89, v90, vcc
	v_cndmask_b32_e32 v68, v91, v92, vcc
	v_add3_u32 v87, v87, v72, v74
	v_lshl_add_u64 v[68:69], v[86:87], 1, v[68:69]
	v_lshl_add_u64 v[68:69], v[68:69], 0, s[0:1]
	v_or_b32_e32 v70, s38, v150
	v_lshl_add_u64 v[68:69], v[68:69], 0, v[138:139]
	v_cmp_gt_i32_e32 vcc, s52, v70
	global_store_dwordx4 v[68:69], v[64:67], off nt
	s_nop 0
	v_cndmask_b32_e32 v69, v89, v90, vcc
	s_nop 1
	v_cvt_pk_bf16_f32 v64, v71, v73
	v_cndmask_b32_e32 v71, v88, v165, vcc
	v_add_u32_e32 v70, v71, v70
	v_ashrrev_i32_e32 v71, 31, v70
	v_mul_lo_u32 v72, s20, v71
	v_mul_lo_u32 v73, s21, v70
	v_mad_u64_u32 v[70:71], s[2:3], s20, v70, 0
	v_cndmask_b32_e32 v68, v91, v92, vcc
	v_add3_u32 v71, v71, v72, v73
	v_lshl_add_u64 v[68:69], v[70:71], 1, v[68:69]
	v_lshl_add_u64 v[68:69], v[68:69], 0, s[0:1]
	v_lshl_add_u64 v[68:69], v[68:69], 0, v[138:139]
	s_nop 1
	v_cvt_pk_bf16_f32 v65, v75, v77
	s_nop 1
	v_cvt_pk_bf16_f32 v66, v79, v81
	s_nop 1
	v_cvt_pk_bf16_f32 v67, v83, v85
	global_store_dwordx4 v[68:69], v[64:67], off nt
	s_waitcnt lgkmcnt(0)

.LBB0_494:
	s_abs_i32 s0, s60
	s_mul_hi_u32 s1, s0, s56
	s_mul_i32 s1, s1, s4
	s_sub_i32 s0, s0, s1
	s_sub_i32 s1, s0, s4
	s_cmp_ge_u32 s0, s4
	s_cselect_b32 s0, s1, s0
	s_sub_i32 s1, s0, s4
	s_cmp_ge_u32 s0, s4
	s_cselect_b32 s0, s1, s0
	s_xor_b32 s0, s0, s59
	v_add_u32_e32 v68, 0x420, v154
	s_sub_i32 s0, s0, s59
	ds_write2_b32 v68, v64, v65 offset1:1
	v_add_u32_e32 v64, 0x428, v154
	s_lshl_b32 s2, s0, 5
	s_lshl_b64 s[0:1], s[28:29], 1
	ds_write2_b32 v64, v66, v67 offset1:1
	s_add_u32 s3, s18, s0
	s_waitcnt lgkmcnt(0)
	s_addc_u32 s38, s19, s1
	s_lshl_b64 s[0:1], s[36:37], 1
	s_add_u32 s0, s3, s0
	ds_read2_b32 v[68:69], v155 offset0:33 offset1:41
	ds_read2_b32 v[70:71], v155 offset1:8
	ds_read2_b32 v[72:73], v155 offset0:66 offset1:74
	ds_read2_b32 v[74:75], v155 offset0:99 offset1:107
	ds_read2_b32 v[76:77], v155 offset0:132 offset1:140
	ds_read2_b32 v[78:79], v155 offset0:165 offset1:173
	ds_read2_b32 v[80:81], v155 offset0:198 offset1:206
	ds_read2_b32 v[82:83], v155 offset0:231 offset1:239
	s_addc_u32 s1, s38, s1
	v_lshlrev_b32_e32 v138, 1, v140
	s_waitcnt lgkmcnt(6)
	s_nop 1
	v_cvt_pk_bf16_f32 v64, v70, v68
	v_or_b32_e32 v68, s2, v136
	v_lshl_add_u64 v[84:85], s[0:1], 0, v[138:139]
	v_mad_u64_u32 v[86:87], s[0:1], s26, v68, 0
	s_ashr_i32 s0, s2, 31
	v_mul_lo_u32 v70, s27, v68
	s_mul_i32 s3, s26, s0
	v_add3_u32 v87, v87, s3, v70
	v_lshl_add_u64 v[86:87], v[86:87], 1, v[84:85]
	v_or_b32_e32 v68, s2, v146
	s_waitcnt lgkmcnt(4)
	s_nop 1
	v_cvt_pk_bf16_f32 v65, v72, v74
	s_waitcnt lgkmcnt(2)
	s_nop 1
	v_cvt_pk_bf16_f32 v66, v76, v78
	s_waitcnt lgkmcnt(0)
	s_nop 1
	v_cvt_pk_bf16_f32 v67, v80, v82
	global_store_dwordx4 v[86:87], v[64:67], off nt
	v_mul_lo_u32 v70, s27, v68
	s_nop 0
	s_nop 1
	v_cvt_pk_bf16_f32 v64, v71, v69
	v_mad_u64_u32 v[68:69], s[0:1], s26, v68, 0
	v_add3_u32 v69, v69, s3, v70
	s_nop 1
	v_cvt_pk_bf16_f32 v65, v73, v75
	s_nop 1
	v_cvt_pk_bf16_f32 v66, v77, v79
	s_nop 1
	v_cvt_pk_bf16_f32 v67, v81, v83
	v_lshl_add_u64 v[68:69], v[68:69], 1, v[84:85]
	ds_read2_b32 v[70:71], v155 offset0:16 offset1:24
	ds_read2_b32 v[72:73], v155 offset0:49 offset1:57
	ds_read2_b32 v[74:75], v155 offset0:82 offset1:90
	ds_read2_b32 v[76:77], v155 offset0:115 offset1:123
	ds_read2_b32 v[78:79], v155 offset0:148 offset1:156
	ds_read2_b32 v[80:81], v155 offset0:181 offset1:189
	ds_read2_b32 v[82:83], v155 offset0:214 offset1:222
	ds_read2_b32 v[86:87], v155 offset0:247 offset1:255
	global_store_dwordx4 v[68:69], v[64:67], off nt
	v_or_b32_e32 v68, s2, v148
	s_waitcnt lgkmcnt(6)
	s_nop 1
	v_cvt_pk_bf16_f32 v64, v70, v72
	v_mul_lo_u32 v70, s27, v68
	v_mad_u64_u32 v[68:69], s[0:1], s26, v68, 0
	v_add3_u32 v69, v69, s3, v70
	v_lshl_add_u64 v[68:69], v[68:69], 1, v[84:85]
	s_waitcnt lgkmcnt(4)
	s_nop 1
	v_cvt_pk_bf16_f32 v65, v74, v76
	s_waitcnt lgkmcnt(2)
	s_nop 1
	v_cvt_pk_bf16_f32 v66, v78, v80
	s_waitcnt lgkmcnt(0)
	s_nop 1
	v_cvt_pk_bf16_f32 v67, v82, v86
	global_store_dwordx4 v[68:69], v[64:67], off nt
	v_or_b32_e32 v68, s2, v150
	v_mul_lo_u32 v70, s27, v68
	v_mad_u64_u32 v[68:69], s[0:1], s26, v68, 0
	v_add3_u32 v69, v69, s3, v70
	v_lshl_add_u64 v[68:69], v[68:69], 1, v[84:85]
	s_nop 1
	v_cvt_pk_bf16_f32 v64, v71, v73
	s_nop 1
	v_cvt_pk_bf16_f32 v65, v75, v77
	s_nop 1
	v_cvt_pk_bf16_f32 v66, v79, v81
	s_nop 1
	v_cvt_pk_bf16_f32 v67, v83, v87
	global_store_dwordx4 v[68:69], v[64:67], off nt
	s_waitcnt lgkmcnt(0)

.LBB0_517:
	s_abs_i32 s0, s60
	s_mul_hi_u32 s1, s0, s56
	s_mul_i32 s1, s1, s4
	s_sub_i32 s0, s0, s1
	v_add_u32_e32 v64, 0x420, v154
	s_sub_i32 s1, s0, s4
	ds_write2_b32 v64, v68, v69 offset1:1
	v_add_u32_e32 v64, 0x428, v154
	s_cmp_ge_u32 s0, s4
	ds_write2_b32 v64, v70, v71 offset1:1
	s_cselect_b32 s0, s1, s0
	s_sub_i32 s1, s0, s4
	s_waitcnt lgkmcnt(0)
	s_cmp_ge_u32 s0, s4
	ds_read2_b32 v[64:65], v155 offset0:33 offset1:41
	ds_read2_b32 v[66:67], v155 offset1:8
	s_cselect_b32 s0, s1, s0
	s_xor_b32 s0, s0, s59
	s_sub_i32 s0, s0, s59
	ds_read2_b32 v[70:71], v155 offset0:66 offset1:74
	ds_read2_b32 v[72:73], v155 offset0:132 offset1:140
	ds_read2_b32 v[74:75], v155 offset0:165 offset1:173
	ds_read2_b32 v[76:77], v155 offset0:99 offset1:107
	s_lshl_b32 s2, s0, 5
	v_mov_b32_e32 v68, v139
	s_waitcnt lgkmcnt(4)
	v_cvt_pk_fp8_f32 v68, v66, v64
	v_or_b32_e32 v64, s2, v136
	v_mov_b32_e32 v69, v139
	ds_read2_b32 v[78:79], v155 offset0:198 offset1:206
	ds_read2_b32 v[80:81], v155 offset0:231 offset1:239
	v_cmp_gt_i32_e32 vcc, s53, v64
	s_add_u32 s0, s18, s36
	s_waitcnt lgkmcnt(3)
	v_cvt_pk_fp8_f32 v69, v72, v74
	v_cndmask_b32_e32 v66, v166, v167, vcc
	s_addc_u32 s1, s19, s37
	v_add_u32_e32 v64, v66, v64
	v_lshl_add_u64 v[82:83], s[0:1], 0, v[140:141]
	v_ashrrev_i32_e32 v66, 31, v64
	s_waitcnt lgkmcnt(2)
	v_cvt_pk_fp8_f32 v68, v70, v76 op_sel:[0,0,1]
	v_mul_lo_u32 v66, s20, v66
	v_mul_lo_u32 v70, s21, v64
	v_mad_u64_u32 v[84:85], s[0:1], s20, v64, v[82:83]
	s_waitcnt lgkmcnt(0)
	v_cvt_pk_fp8_f32 v69, v78, v80 op_sel:[0,0,1]
	v_mov_b32_e32 v64, v139
	v_add3_u32 v85, v70, v85, v66
	v_or_b32_e32 v66, s2, v146
	v_cvt_pk_fp8_f32 v64, v67, v65
	v_mov_b32_e32 v65, v139
	v_cmp_gt_i32_e32 vcc, s53, v66
	v_cvt_pk_fp8_f32 v65, v73, v75
	global_store_dwordx2 v[84:85], v[68:69], off nt
	v_cndmask_b32_e32 v67, v166, v167, vcc
	v_add_u32_e32 v70, v67, v66
	v_ashrrev_i32_e32 v66, 31, v70
	v_mul_lo_u32 v88, s20, v66
	ds_read2_b32 v[66:67], v155 offset0:16 offset1:24
	ds_read2_b32 v[68:69], v155 offset0:49 offset1:57
	v_cvt_pk_fp8_f32 v64, v71, v77 op_sel:[0,0,1]
	v_cvt_pk_fp8_f32 v65, v79, v81 op_sel:[0,0,1]
	ds_read2_b32 v[74:75], v155 offset0:82 offset1:90
	ds_read2_b32 v[76:77], v155 offset0:148 offset1:156
	ds_read2_b32 v[78:79], v155 offset0:181 offset1:189
	ds_read2_b32 v[80:81], v155 offset0:115 offset1:123
	v_mul_lo_u32 v89, s21, v70
	v_mad_u64_u32 v[70:71], s[0:1], s20, v70, v[82:83]
	v_mov_b32_e32 v72, v139
	v_mov_b32_e32 v73, v139
	ds_read2_b32 v[84:85], v155 offset0:214 offset1:222
	ds_read2_b32 v[86:87], v155 offset0:247 offset1:255
	s_waitcnt lgkmcnt(6)
	v_cvt_pk_fp8_f32 v72, v66, v68
	s_waitcnt lgkmcnt(3)
	v_cvt_pk_fp8_f32 v73, v76, v78
	v_add3_u32 v71, v89, v71, v88
	global_store_dwordx2 v[70:71], v[64:65], off nt
	v_or_b32_e32 v64, s2, v148
	v_cmp_gt_i32_e32 vcc, s53, v64
	s_waitcnt lgkmcnt(2)
	v_cvt_pk_fp8_f32 v72, v74, v80 op_sel:[0,0,1]
	s_waitcnt lgkmcnt(0)
	v_cvt_pk_fp8_f32 v73, v84, v86 op_sel:[0,0,1]
	v_cndmask_b32_e32 v65, v166, v167, vcc
	v_add_u32_e32 v64, v65, v64
	v_ashrrev_i32_e32 v65, 31, v64
	v_mov_b32_e32 v66, v139
	v_mul_lo_u32 v68, s20, v65
	v_mul_lo_u32 v70, s21, v64
	v_mad_u64_u32 v[64:65], s[0:1], s20, v64, v[82:83]
	v_cvt_pk_fp8_f32 v66, v67, v69
	v_mov_b32_e32 v67, v139
	v_cvt_pk_fp8_f32 v67, v77, v79
	v_add3_u32 v65, v70, v65, v68
	global_store_dwordx2 v[64:65], v[72:73], off nt
	v_or_b32_e32 v64, s2, v150
	v_cmp_gt_i32_e32 vcc, s53, v64
	v_cvt_pk_fp8_f32 v66, v75, v81 op_sel:[0,0,1]
	v_cvt_pk_fp8_f32 v67, v85, v87 op_sel:[0,0,1]
	v_cndmask_b32_e32 v65, v166, v167, vcc
	v_add_u32_e32 v64, v65, v64
	v_ashrrev_i32_e32 v65, 31, v64
	v_mul_lo_u32 v68, s20, v65
	v_mul_lo_u32 v69, s21, v64
	v_mad_u64_u32 v[64:65], s[0:1], s20, v64, v[82:83]
	v_add3_u32 v65, v69, v65, v68
	global_store_dwordx2 v[64:65], v[66:67], off nt
	s_waitcnt lgkmcnt(0)
	s_mov_b64 s[0:1], 0

.LBB0_536:
	s_abs_i32 s0, s60
	s_mul_hi_u32 s1, s0, s56
	s_mul_i32 s1, s1, s4
	s_sub_i32 s0, s0, s1
	v_add_u32_e32 v64, 0x420, v154
	s_sub_i32 s1, s0, s4
	ds_write2_b32 v64, v68, v69 offset1:1
	v_add_u32_e32 v64, 0x428, v154
	s_cmp_ge_u32 s0, s4
	ds_write2_b32 v64, v70, v71 offset1:1
	s_cselect_b32 s0, s1, s0
	s_sub_i32 s1, s0, s4
	s_waitcnt lgkmcnt(0)
	s_cmp_ge_u32 s0, s4
	ds_read2_b32 v[64:65], v155 offset0:33 offset1:41
	ds_read2_b32 v[66:67], v155 offset1:8
	s_cselect_b32 s0, s1, s0
	ds_read2_b32 v[70:71], v155 offset0:66 offset1:74
	ds_read2_b32 v[72:73], v155 offset0:132 offset1:140
	ds_read2_b32 v[74:75], v155 offset0:165 offset1:173
	ds_read2_b32 v[76:77], v155 offset0:99 offset1:107
	s_xor_b32 s0, s0, s59
	s_sub_i32 s0, s0, s59
	s_lshl_b32 s0, s0, 5
	v_mov_b32_e32 v68, v139
	v_mov_b32_e32 v69, v139
	ds_read2_b32 v[78:79], v155 offset0:198 offset1:206
	ds_read2_b32 v[80:81], v155 offset0:231 offset1:239
	s_add_i32 s2, s0, 0xfffff600
	s_waitcnt lgkmcnt(6)
	v_cvt_pk_fp8_f32 v68, v66, v64
	s_waitcnt lgkmcnt(3)
	v_cvt_pk_fp8_f32 v69, v72, v74
	s_add_u32 s0, s18, s36
	s_addc_u32 s1, s19, s37
	v_lshl_add_u64 v[82:83], s[0:1], 0, v[140:141]
	v_or_b32_e32 v64, s2, v136
	s_waitcnt lgkmcnt(2)
	v_cvt_pk_fp8_f32 v68, v70, v76 op_sel:[0,0,1]
	s_waitcnt lgkmcnt(0)
	v_cvt_pk_fp8_f32 v69, v78, v80 op_sel:[0,0,1]
	v_mul_lo_u32 v66, s21, v64
	v_mad_u64_u32 v[84:85], s[0:1], s20, v64, v[82:83]
	v_mov_b32_e32 v64, v139
	s_ashr_i32 s0, s2, 31
	v_cvt_pk_fp8_f32 v64, v67, v65
	v_mov_b32_e32 v65, v139
	s_mul_i32 s3, s20, s0
	v_cvt_pk_fp8_f32 v65, v73, v75
	v_add3_u32 v85, v66, v85, s3
	global_store_dwordx2 v[84:85], v[68:69], off nt
	ds_read2_b32 v[66:67], v155 offset0:16 offset1:24
	ds_read2_b32 v[68:69], v155 offset0:49 offset1:57
	v_cvt_pk_fp8_f32 v64, v71, v77 op_sel:[0,0,1]
	v_cvt_pk_fp8_f32 v65, v79, v81 op_sel:[0,0,1]
	ds_read2_b32 v[74:75], v155 offset0:82 offset1:90
	ds_read2_b32 v[76:77], v155 offset0:148 offset1:156
	ds_read2_b32 v[78:79], v155 offset0:181 offset1:189
	ds_read2_b32 v[80:81], v155 offset0:115 offset1:123
	v_mov_b32_e32 v72, v139
	v_mov_b32_e32 v73, v139
	ds_read2_b32 v[84:85], v155 offset0:214 offset1:222
	ds_read2_b32 v[86:87], v155 offset0:247 offset1:255
	s_waitcnt lgkmcnt(6)
	v_cvt_pk_fp8_f32 v72, v66, v68
	s_waitcnt lgkmcnt(3)
	v_cvt_pk_fp8_f32 v73, v76, v78
	v_mov_b32_e32 v66, v139
	v_or_b32_e32 v70, s2, v146
	v_cvt_pk_fp8_f32 v66, v67, v69
	v_mov_b32_e32 v67, v139
	v_mul_lo_u32 v88, s21, v70
	v_mad_u64_u32 v[70:71], s[0:1], s20, v70, v[82:83]
	v_cvt_pk_fp8_f32 v67, v77, v79
	v_add3_u32 v71, v88, v71, s3
	s_waitcnt lgkmcnt(2)
	v_cvt_pk_fp8_f32 v72, v74, v80 op_sel:[0,0,1]
	s_waitcnt lgkmcnt(0)
	v_cvt_pk_fp8_f32 v73, v84, v86 op_sel:[0,0,1]
	global_store_dwordx2 v[70:71], v[64:65], off nt
	v_or_b32_e32 v64, s2, v148
	v_mul_lo_u32 v68, s21, v64
	v_mad_u64_u32 v[64:65], s[0:1], s20, v64, v[82:83]
	v_add3_u32 v65, v68, v65, s3
	v_cvt_pk_fp8_f32 v66, v75, v81 op_sel:[0,0,1]
	v_cvt_pk_fp8_f32 v67, v85, v87 op_sel:[0,0,1]
	global_store_dwordx2 v[64:65], v[72:73], off nt
	v_or_b32_e32 v64, s2, v150
	v_mul_lo_u32 v68, s21, v64
	v_mad_u64_u32 v[64:65], s[0:1], s20, v64, v[82:83]
	v_add3_u32 v65, v68, v65, s3
	global_store_dwordx2 v[64:65], v[66:67], off nt
	s_waitcnt lgkmcnt(0)

.LBB0_556:
	s_abs_i32 s0, s60
	s_mul_hi_u32 s1, s0, s56
	s_mul_i32 s1, s1, s4
	s_sub_i32 s0, s0, s1
	v_add_u32_e32 v64, 0x420, v154
	s_sub_i32 s1, s0, s4
	ds_write2_b32 v64, v68, v69 offset1:1
	v_add_u32_e32 v64, 0x428, v154
	s_cmp_ge_u32 s0, s4
	ds_write2_b32 v64, v70, v71 offset1:1
	s_cselect_b32 s0, s1, s0
	s_sub_i32 s1, s0, s4
	s_waitcnt lgkmcnt(0)
	s_cmp_ge_u32 s0, s4
	ds_read2_b32 v[64:65], v155 offset0:33 offset1:41
	ds_read2_b32 v[66:67], v155 offset1:8
	s_cselect_b32 s0, s1, s0
	ds_read2_b32 v[70:71], v155 offset0:66 offset1:74
	ds_read2_b32 v[72:73], v155 offset0:132 offset1:140
	ds_read2_b32 v[74:75], v155 offset0:165 offset1:173
	ds_read2_b32 v[76:77], v155 offset0:99 offset1:107
	s_xor_b32 s0, s0, s59
	s_sub_i32 s0, s0, s59
	s_lshl_b32 s0, s0, 5
	v_mov_b32_e32 v68, v139
	v_mov_b32_e32 v69, v139
	ds_read2_b32 v[78:79], v155 offset0:198 offset1:206
	ds_read2_b32 v[80:81], v155 offset0:231 offset1:239
	s_add_i32 s2, s0, 0xfffff000
	s_waitcnt lgkmcnt(6)
	v_cvt_pk_fp8_f32 v68, v66, v64
	s_waitcnt lgkmcnt(3)
	v_cvt_pk_fp8_f32 v69, v72, v74
	s_add_u32 s0, s18, s36
	s_addc_u32 s1, s19, s37
	v_lshl_add_u64 v[82:83], s[0:1], 0, v[140:141]
	v_or_b32_e32 v64, s2, v136
	s_waitcnt lgkmcnt(2)
	v_cvt_pk_fp8_f32 v68, v70, v76 op_sel:[0,0,1]
	s_waitcnt lgkmcnt(0)
	v_cvt_pk_fp8_f32 v69, v78, v80 op_sel:[0,0,1]
	v_mul_lo_u32 v66, s21, v64
	v_mad_u64_u32 v[84:85], s[0:1], s20, v64, v[82:83]
	v_mov_b32_e32 v64, v139
	s_ashr_i32 s0, s2, 31
	v_cvt_pk_fp8_f32 v64, v67, v65
	v_mov_b32_e32 v65, v139
	s_mul_i32 s3, s20, s0
	v_cvt_pk_fp8_f32 v65, v73, v75
	v_add3_u32 v85, v66, v85, s3
	global_store_dwordx2 v[84:85], v[68:69], off nt
	ds_read2_b32 v[66:67], v155 offset0:16 offset1:24
	ds_read2_b32 v[68:69], v155 offset0:49 offset1:57
	v_cvt_pk_fp8_f32 v64, v71, v77 op_sel:[0,0,1]
	v_cvt_pk_fp8_f32 v65, v79, v81 op_sel:[0,0,1]
	ds_read2_b32 v[74:75], v155 offset0:82 offset1:90
	ds_read2_b32 v[76:77], v155 offset0:148 offset1:156
	ds_read2_b32 v[78:79], v155 offset0:181 offset1:189
	ds_read2_b32 v[80:81], v155 offset0:115 offset1:123
	v_mov_b32_e32 v72, v139
	v_mov_b32_e32 v73, v139
	ds_read2_b32 v[84:85], v155 offset0:214 offset1:222
	ds_read2_b32 v[86:87], v155 offset0:247 offset1:255
	s_waitcnt lgkmcnt(6)
	v_cvt_pk_fp8_f32 v72, v66, v68
	s_waitcnt lgkmcnt(3)
	v_cvt_pk_fp8_f32 v73, v76, v78
	v_mov_b32_e32 v66, v139
	v_or_b32_e32 v70, s2, v146
	v_cvt_pk_fp8_f32 v66, v67, v69
	v_mov_b32_e32 v67, v139
	v_mul_lo_u32 v88, s21, v70
	v_mad_u64_u32 v[70:71], s[0:1], s20, v70, v[82:83]
	v_cvt_pk_fp8_f32 v67, v77, v79
	v_add3_u32 v71, v88, v71, s3
	s_waitcnt lgkmcnt(2)
	v_cvt_pk_fp8_f32 v72, v74, v80 op_sel:[0,0,1]
	s_waitcnt lgkmcnt(0)
	v_cvt_pk_fp8_f32 v73, v84, v86 op_sel:[0,0,1]
	global_store_dwordx2 v[70:71], v[64:65], off nt
	v_or_b32_e32 v64, s2, v148
	v_mul_lo_u32 v68, s21, v64
	v_mad_u64_u32 v[64:65], s[0:1], s20, v64, v[82:83]
	v_add3_u32 v65, v68, v65, s3
	v_cvt_pk_fp8_f32 v66, v75, v81 op_sel:[0,0,1]
	v_cvt_pk_fp8_f32 v67, v85, v87 op_sel:[0,0,1]
	global_store_dwordx2 v[64:65], v[72:73], off nt
	v_or_b32_e32 v64, s2, v150
	v_mul_lo_u32 v68, s21, v64
	v_mad_u64_u32 v[64:65], s[0:1], s20, v64, v[82:83]
	v_add3_u32 v65, v68, v65, s3
	global_store_dwordx2 v[64:65], v[66:67], off nt
	s_waitcnt lgkmcnt(0)

.LBB0_581:
	s_abs_i32 s2, s60
	s_mul_hi_u32 s3, s2, s56
	s_mul_i32 s3, s3, s4
	v_add_u32_e32 v64, 0x420, v154
	s_sub_i32 s2, s2, s3
	ds_write2_b32 v64, v68, v69 offset1:1
	v_add_u32_e32 v64, 0x428, v154
	s_sub_i32 s3, s2, s4
	ds_write2_b32 v64, v70, v71 offset1:1
	s_cmp_ge_u32 s2, s4
	s_cselect_b32 s2, s3, s2
	s_waitcnt lgkmcnt(0)
	s_sub_i32 s3, s2, s4
	ds_read2_b32 v[64:65], v155 offset0:33 offset1:41
	ds_read2_b32 v[66:67], v155 offset1:8
	s_cmp_ge_u32 s2, s4
	ds_read2_b32 v[70:71], v155 offset0:66 offset1:74
	ds_read2_b32 v[72:73], v155 offset0:132 offset1:140
	ds_read2_b32 v[74:75], v155 offset0:165 offset1:173
	ds_read2_b32 v[76:77], v155 offset0:99 offset1:107
	s_cselect_b32 s2, s3, s2
	s_xor_b32 s2, s2, s59
	s_sub_i32 s2, s2, s59
	v_mov_b32_e32 v68, v139
	v_mov_b32_e32 v69, v139
	ds_read2_b32 v[78:79], v155 offset0:198 offset1:206
	ds_read2_b32 v[80:81], v155 offset0:231 offset1:239
	s_lshl_b32 s38, s2, 6
	s_waitcnt lgkmcnt(6)
	v_cvt_pk_fp8_f32 v68, v66, v64
	s_waitcnt lgkmcnt(3)
	v_cvt_pk_fp8_f32 v69, v72, v74
	s_add_u32 s2, s18, s36
	s_addc_u32 s3, s19, s37
	v_lshl_add_u64 v[82:83], s[2:3], 0, v[140:141]
	v_or_b32_e32 v64, s38, v156
	s_waitcnt lgkmcnt(2)
	v_cvt_pk_fp8_f32 v68, v70, v76 op_sel:[0,0,1]
	s_waitcnt lgkmcnt(0)
	v_cvt_pk_fp8_f32 v69, v78, v80 op_sel:[0,0,1]
	v_mul_lo_u32 v66, s21, v64
	v_mad_u64_u32 v[84:85], s[2:3], s20, v64, v[82:83]
	v_mov_b32_e32 v64, v139
	s_ashr_i32 s2, s38, 31
	v_cvt_pk_fp8_f32 v64, v67, v65
	v_mov_b32_e32 v65, v139
	s_mul_i32 s37, s20, s2
	v_cvt_pk_fp8_f32 v65, v73, v75
	v_add3_u32 v85, v66, v85, s37
	global_store_dwordx2 v[84:85], v[68:69], off nt
	ds_read2_b32 v[66:67], v155 offset0:16 offset1:24
	ds_read2_b32 v[68:69], v155 offset0:49 offset1:57
	v_cvt_pk_fp8_f32 v64, v71, v77 op_sel:[0,0,1]
	v_cvt_pk_fp8_f32 v65, v79, v81 op_sel:[0,0,1]
	ds_read2_b32 v[74:75], v155 offset0:82 offset1:90
	ds_read2_b32 v[76:77], v155 offset0:148 offset1:156
	ds_read2_b32 v[78:79], v155 offset0:181 offset1:189
	ds_read2_b32 v[80:81], v155 offset0:115 offset1:123
	v_mov_b32_e32 v72, v139
	v_mov_b32_e32 v73, v139
	ds_read2_b32 v[84:85], v155 offset0:214 offset1:222
	ds_read2_b32 v[86:87], v155 offset0:247 offset1:255
	s_waitcnt lgkmcnt(6)
	v_cvt_pk_fp8_f32 v72, v66, v68
	s_waitcnt lgkmcnt(3)
	v_cvt_pk_fp8_f32 v73, v76, v78
	v_mov_b32_e32 v66, v139
	v_or_b32_e32 v70, s38, v157
	v_cvt_pk_fp8_f32 v66, v67, v69
	v_mov_b32_e32 v67, v139
	v_mul_lo_u32 v88, s21, v70
	v_mad_u64_u32 v[70:71], s[2:3], s20, v70, v[82:83]
	v_cvt_pk_fp8_f32 v67, v77, v79
	v_add3_u32 v71, v88, v71, s37
	s_waitcnt lgkmcnt(2)
	v_cvt_pk_fp8_f32 v72, v74, v80 op_sel:[0,0,1]
	s_waitcnt lgkmcnt(0)
	v_cvt_pk_fp8_f32 v73, v84, v86 op_sel:[0,0,1]
	global_store_dwordx2 v[70:71], v[64:65], off nt
	v_or_b32_e32 v64, s38, v158
	v_mul_lo_u32 v68, s21, v64
	v_mad_u64_u32 v[64:65], s[2:3], s20, v64, v[82:83]
	v_add3_u32 v65, v68, v65, s37
	v_cvt_pk_fp8_f32 v66, v75, v81 op_sel:[0,0,1]
	v_cvt_pk_fp8_f32 v67, v85, v87 op_sel:[0,0,1]
	global_store_dwordx2 v[64:65], v[72:73], off nt
	v_or_b32_e32 v64, s38, v159
	v_mul_lo_u32 v68, s21, v64
	v_mad_u64_u32 v[64:65], s[2:3], s20, v64, v[82:83]
	v_add3_u32 v65, v68, v65, s37
	global_store_dwordx2 v[64:65], v[66:67], off nt
	s_waitcnt lgkmcnt(0)
	s_mov_b64 s[2:3], 0

.LBB0_601:
	s_abs_i32 s0, s60
	s_mul_hi_u32 s1, s0, s56
	s_mul_i32 s1, s1, s4
	v_add_u32_e32 v64, 0x420, v154
	s_sub_i32 s0, s0, s1
	ds_write2_b32 v64, v68, v69 offset1:1
	v_add_u32_e32 v64, 0x428, v154
	s_sub_i32 s1, s0, s4
	ds_write2_b32 v64, v70, v71 offset1:1
	s_cmp_ge_u32 s0, s4
	s_cselect_b32 s0, s1, s0
	s_waitcnt lgkmcnt(0)
	s_sub_i32 s1, s0, s4
	ds_read2_b32 v[64:65], v155 offset0:33 offset1:41
	ds_read2_b32 v[66:67], v155 offset1:8
	s_cmp_ge_u32 s0, s4
	ds_read2_b32 v[70:71], v155 offset0:66 offset1:74
	ds_read2_b32 v[72:73], v155 offset0:132 offset1:140
	ds_read2_b32 v[74:75], v155 offset0:165 offset1:173
	ds_read2_b32 v[76:77], v155 offset0:99 offset1:107
	s_cselect_b32 s0, s1, s0
	s_xor_b32 s0, s0, s59
	s_sub_i32 s0, s0, s59
	v_mov_b32_e32 v68, v139
	v_mov_b32_e32 v69, v139
	ds_read2_b32 v[78:79], v155 offset0:198 offset1:206
	ds_read2_b32 v[80:81], v155 offset0:231 offset1:239
	s_lshl_b32 s2, s0, 6
	s_waitcnt lgkmcnt(6)
	v_cvt_pk_fp8_f32 v68, v66, v64
	s_waitcnt lgkmcnt(3)
	v_cvt_pk_fp8_f32 v69, v72, v74
	s_add_u32 s0, s18, s36
	s_addc_u32 s1, s19, s37
	v_lshl_add_u64 v[82:83], s[0:1], 0, v[140:141]
	v_or_b32_e32 v64, s2, v160
	s_waitcnt lgkmcnt(2)
	v_cvt_pk_fp8_f32 v68, v70, v76 op_sel:[0,0,1]
	s_waitcnt lgkmcnt(0)
	v_cvt_pk_fp8_f32 v69, v78, v80 op_sel:[0,0,1]
	v_mul_lo_u32 v66, s21, v64
	v_mad_u64_u32 v[84:85], s[0:1], s20, v64, v[82:83]
	v_mov_b32_e32 v64, v139
	s_ashr_i32 s0, s2, 31
	v_cvt_pk_fp8_f32 v64, v67, v65
	v_mov_b32_e32 v65, v139
	s_mul_i32 s3, s20, s0
	v_cvt_pk_fp8_f32 v65, v73, v75
	v_add3_u32 v85, v66, v85, s3
	global_store_dwordx2 v[84:85], v[68:69], off nt
	ds_read2_b32 v[66:67], v155 offset0:16 offset1:24
	ds_read2_b32 v[68:69], v155 offset0:49 offset1:57
	v_cvt_pk_fp8_f32 v64, v71, v77 op_sel:[0,0,1]
	v_cvt_pk_fp8_f32 v65, v79, v81 op_sel:[0,0,1]
	ds_read2_b32 v[74:75], v155 offset0:82 offset1:90
	ds_read2_b32 v[76:77], v155 offset0:148 offset1:156
	ds_read2_b32 v[78:79], v155 offset0:181 offset1:189
	ds_read2_b32 v[80:81], v155 offset0:115 offset1:123
	v_mov_b32_e32 v72, v139
	v_mov_b32_e32 v73, v139
	ds_read2_b32 v[84:85], v155 offset0:214 offset1:222
	ds_read2_b32 v[86:87], v155 offset0:247 offset1:255
	s_waitcnt lgkmcnt(6)
	v_cvt_pk_fp8_f32 v72, v66, v68
	s_waitcnt lgkmcnt(3)
	v_cvt_pk_fp8_f32 v73, v76, v78
	v_mov_b32_e32 v66, v139
	v_or_b32_e32 v70, s2, v161
	v_cvt_pk_fp8_f32 v66, v67, v69
	v_mov_b32_e32 v67, v139
	v_mul_lo_u32 v88, s21, v70
	v_mad_u64_u32 v[70:71], s[0:1], s20, v70, v[82:83]
	v_cvt_pk_fp8_f32 v67, v77, v79
	v_add3_u32 v71, v88, v71, s3
	s_waitcnt lgkmcnt(2)
	v_cvt_pk_fp8_f32 v72, v74, v80 op_sel:[0,0,1]
	s_waitcnt lgkmcnt(0)
	v_cvt_pk_fp8_f32 v73, v84, v86 op_sel:[0,0,1]
	global_store_dwordx2 v[70:71], v[64:65], off nt
	v_or_b32_e32 v64, s2, v162
	v_mul_lo_u32 v68, s21, v64
	v_mad_u64_u32 v[64:65], s[0:1], s20, v64, v[82:83]
	v_add3_u32 v65, v68, v65, s3
	v_cvt_pk_fp8_f32 v66, v75, v81 op_sel:[0,0,1]
	v_cvt_pk_fp8_f32 v67, v85, v87 op_sel:[0,0,1]
	global_store_dwordx2 v[64:65], v[72:73], off nt
	v_or_b32_e32 v64, s2, v163
	v_mul_lo_u32 v68, s21, v64
	v_mad_u64_u32 v[64:65], s[0:1], s20, v64, v[82:83]
	v_add3_u32 v65, v68, v65, s3
	global_store_dwordx2 v[64:65], v[66:67], off nt
	s_waitcnt lgkmcnt(0)
	s_branch .LBB0_620

.LBB0_619:
	s_abs_i32 s0, s60
	s_mul_hi_u32 s1, s0, s56
	s_mul_i32 s1, s1, s4
	v_add_u32_e32 v32, 0x420, v154
	s_sub_i32 s0, s0, s1
	ds_write2_b32 v32, v36, v37 offset1:1
	v_add_u32_e32 v32, 0x428, v154
	s_sub_i32 s1, s0, s4
	ds_write2_b32 v32, v38, v39 offset1:1
	s_cmp_ge_u32 s0, s4
	s_cselect_b32 s0, s1, s0
	s_waitcnt lgkmcnt(0)
	s_sub_i32 s1, s0, s4
	ds_read2_b32 v[32:33], v155 offset0:33 offset1:41
	ds_read2_b32 v[34:35], v155 offset1:8
	s_cmp_ge_u32 s0, s4
	ds_read2_b32 v[38:39], v155 offset0:66 offset1:74
	ds_read2_b32 v[40:41], v155 offset0:132 offset1:140
	ds_read2_b32 v[42:43], v155 offset0:165 offset1:173
	ds_read2_b32 v[44:45], v155 offset0:99 offset1:107
	s_cselect_b32 s0, s1, s0
	s_xor_b32 s0, s0, s59
	s_sub_i32 s0, s0, s59
	v_mov_b32_e32 v36, v139
	v_mov_b32_e32 v37, v139
	ds_read2_b32 v[46:47], v155 offset0:198 offset1:206
	ds_read2_b32 v[48:49], v155 offset0:231 offset1:239
	s_lshl_b32 s2, s0, 5
	s_waitcnt lgkmcnt(6)
	v_cvt_pk_fp8_f32 v36, v34, v32
	s_waitcnt lgkmcnt(3)
	v_cvt_pk_fp8_f32 v37, v40, v42
	s_add_u32 s0, s18, s36
	s_addc_u32 s1, s19, s37
	v_lshl_add_u64 v[50:51], s[0:1], 0, v[140:141]
	v_or_b32_e32 v32, s2, v136
	s_waitcnt lgkmcnt(2)
	v_cvt_pk_fp8_f32 v36, v38, v44 op_sel:[0,0,1]
	s_waitcnt lgkmcnt(0)
	v_cvt_pk_fp8_f32 v37, v46, v48 op_sel:[0,0,1]
	v_mul_lo_u32 v34, s21, v32
	v_mad_u64_u32 v[52:53], s[0:1], s20, v32, v[50:51]
	v_mov_b32_e32 v32, v139
	s_ashr_i32 s0, s2, 31
	v_cvt_pk_fp8_f32 v32, v35, v33
	v_mov_b32_e32 v33, v139
	s_mul_i32 s3, s20, s0
	v_cvt_pk_fp8_f32 v33, v41, v43
	v_add3_u32 v53, v34, v53, s3
	global_store_dwordx2 v[52:53], v[36:37], off nt
	ds_read2_b32 v[34:35], v155 offset0:16 offset1:24
	ds_read2_b32 v[36:37], v155 offset0:49 offset1:57
	v_cvt_pk_fp8_f32 v32, v39, v45 op_sel:[0,0,1]
	v_cvt_pk_fp8_f32 v33, v47, v49 op_sel:[0,0,1]
	ds_read2_b32 v[42:43], v155 offset0:82 offset1:90
	ds_read2_b32 v[44:45], v155 offset0:148 offset1:156
	ds_read2_b32 v[46:47], v155 offset0:181 offset1:189
	ds_read2_b32 v[48:49], v155 offset0:115 offset1:123
	v_mov_b32_e32 v40, v139
	v_mov_b32_e32 v41, v139
	ds_read2_b32 v[52:53], v155 offset0:214 offset1:222
	ds_read2_b32 v[54:55], v155 offset0:247 offset1:255
	s_waitcnt lgkmcnt(6)
	v_cvt_pk_fp8_f32 v40, v34, v36
	s_waitcnt lgkmcnt(3)
	v_cvt_pk_fp8_f32 v41, v44, v46
	v_mov_b32_e32 v34, v139
	v_or_b32_e32 v38, s2, v146
	v_cvt_pk_fp8_f32 v34, v35, v37
	v_mov_b32_e32 v35, v139
	v_mul_lo_u32 v56, s21, v38
	v_mad_u64_u32 v[38:39], s[0:1], s20, v38, v[50:51]
	v_cvt_pk_fp8_f32 v35, v45, v47
	v_add3_u32 v39, v56, v39, s3
	s_waitcnt lgkmcnt(2)
	v_cvt_pk_fp8_f32 v40, v42, v48 op_sel:[0,0,1]
	s_waitcnt lgkmcnt(0)
	v_cvt_pk_fp8_f32 v41, v52, v54 op_sel:[0,0,1]
	global_store_dwordx2 v[38:39], v[32:33], off nt
	v_or_b32_e32 v32, s2, v148
	v_mul_lo_u32 v36, s21, v32
	v_mad_u64_u32 v[32:33], s[0:1], s20, v32, v[50:51]
	v_add3_u32 v33, v36, v33, s3
	v_cvt_pk_fp8_f32 v34, v43, v49 op_sel:[0,0,1]
	v_cvt_pk_fp8_f32 v35, v53, v55 op_sel:[0,0,1]
	global_store_dwordx2 v[32:33], v[40:41], off nt
	v_or_b32_e32 v32, s2, v150
	v_mul_lo_u32 v36, s21, v32
	v_mad_u64_u32 v[32:33], s[0:1], s20, v32, v[50:51]
	v_add3_u32 v33, v36, v33, s3
	global_store_dwordx2 v[32:33], v[34:35], off nt
	s_waitcnt lgkmcnt(0)

.LBB0_636:
	v_add_u32_e32 v36, 0x420, v154
	ds_write2_b32 v36, v32, v33 offset1:1
	v_add_u32_e32 v32, 0x428, v154
	s_mul_i32 s58, s58, s4
	ds_write2_b32 v32, v34, v35 offset1:1
	s_sub_i32 s0, s39, s58
	s_waitcnt lgkmcnt(0)
	s_lshl_b32 s2, s0, 6
	s_lshl_b64 s[0:1], s[36:37], 1
	s_add_u32 s0, s18, s0
	ds_read2_b32 v[36:37], v155 offset0:33 offset1:41
	ds_read2_b32 v[38:39], v155 offset1:8
	ds_read2_b32 v[40:41], v155 offset0:66 offset1:74
	ds_read2_b32 v[42:43], v155 offset0:99 offset1:107
	ds_read2_b32 v[44:45], v155 offset0:132 offset1:140
	ds_read2_b32 v[46:47], v155 offset0:165 offset1:173
	ds_read2_b32 v[48:49], v155 offset0:198 offset1:206
	ds_read2_b32 v[50:51], v155 offset0:231 offset1:239
	s_addc_u32 s1, s19, s1
	v_lshlrev_b32_e32 v138, 1, v140
	s_waitcnt lgkmcnt(6)
	s_nop 1
	v_cvt_pk_bf16_f32 v32, v38, v36
	v_or_b32_e32 v36, s2, v160
	v_lshl_add_u64 v[52:53], s[0:1], 0, v[138:139]
	v_mad_u64_u32 v[54:55], s[0:1], s20, v36, 0
	s_ashr_i32 s0, s2, 31
	v_mul_lo_u32 v38, s21, v36
	s_mul_i32 s3, s20, s0
	v_add3_u32 v55, v55, s3, v38
	v_lshl_add_u64 v[54:55], v[54:55], 1, v[52:53]
	v_or_b32_e32 v36, s2, v161
	s_waitcnt lgkmcnt(4)
	s_nop 1
	v_cvt_pk_bf16_f32 v33, v40, v42
	s_waitcnt lgkmcnt(2)
	s_nop 1
	v_cvt_pk_bf16_f32 v34, v44, v46
	s_waitcnt lgkmcnt(0)
	s_nop 1
	v_cvt_pk_bf16_f32 v35, v48, v50
	global_store_dwordx4 v[54:55], v[32:35], off nt
	v_mul_lo_u32 v38, s21, v36
	s_nop 0
	s_nop 1
	v_cvt_pk_bf16_f32 v32, v39, v37
	v_mad_u64_u32 v[36:37], s[0:1], s20, v36, 0
	v_add3_u32 v37, v37, s3, v38
	s_nop 1
	v_cvt_pk_bf16_f32 v33, v41, v43
	s_nop 1
	v_cvt_pk_bf16_f32 v34, v45, v47
	s_nop 1
	v_cvt_pk_bf16_f32 v35, v49, v51
	v_lshl_add_u64 v[36:37], v[36:37], 1, v[52:53]
	ds_read2_b32 v[38:39], v155 offset0:16 offset1:24
	ds_read2_b32 v[40:41], v155 offset0:49 offset1:57
	ds_read2_b32 v[42:43], v155 offset0:82 offset1:90
	ds_read2_b32 v[44:45], v155 offset0:115 offset1:123
	ds_read2_b32 v[46:47], v155 offset0:148 offset1:156
	ds_read2_b32 v[48:49], v155 offset0:181 offset1:189
	ds_read2_b32 v[50:51], v155 offset0:214 offset1:222
	ds_read2_b32 v[54:55], v155 offset0:247 offset1:255
	global_store_dwordx4 v[36:37], v[32:35], off nt
	v_or_b32_e32 v36, s2, v162
	s_waitcnt lgkmcnt(6)
	s_nop 1
	v_cvt_pk_bf16_f32 v32, v38, v40
	v_mul_lo_u32 v38, s21, v36
	v_mad_u64_u32 v[36:37], s[0:1], s20, v36, 0
	v_add3_u32 v37, v37, s3, v38
	v_lshl_add_u64 v[36:37], v[36:37], 1, v[52:53]
	s_waitcnt lgkmcnt(4)
	s_nop 1
	v_cvt_pk_bf16_f32 v33, v42, v44
	s_waitcnt lgkmcnt(2)
	s_nop 1
	v_cvt_pk_bf16_f32 v34, v46, v48
	s_waitcnt lgkmcnt(0)
	s_nop 1
	v_cvt_pk_bf16_f32 v35, v50, v54
	global_store_dwordx4 v[36:37], v[32:35], off nt
	v_or_b32_e32 v36, s2, v163
	v_mul_lo_u32 v38, s21, v36
	v_mad_u64_u32 v[36:37], s[0:1], s20, v36, 0
	v_add3_u32 v37, v37, s3, v38
	v_lshl_add_u64 v[36:37], v[36:37], 1, v[52:53]
	s_nop 1
	v_cvt_pk_bf16_f32 v32, v39, v41
	s_nop 1
	v_cvt_pk_bf16_f32 v33, v43, v45
	s_nop 1
	v_cvt_pk_bf16_f32 v34, v47, v49
	s_nop 1
	v_cvt_pk_bf16_f32 v35, v51, v55
	global_store_dwordx4 v[36:37], v[32:35], off nt
	s_waitcnt lgkmcnt(0)
	s_mov_b64 s[0:1], 0

.LBB0_650:
	s_abs_i32 s0, s39
	s_mul_hi_u32 s1, s0, s56
	s_mul_i32 s1, s1, s4
	s_sub_i32 s0, s0, s1
	s_sub_i32 s1, s0, s4
	s_cmp_ge_u32 s0, s4
	s_cselect_b32 s0, s1, s0
	s_sub_i32 s1, s0, s4
	s_cmp_ge_u32 s0, s4
	v_add_u32_e32 v36, 0x420, v154
	s_cselect_b32 s0, s1, s0
	ds_write2_b32 v36, v32, v33 offset1:1
	v_add_u32_e32 v32, 0x428, v154
	s_xor_b32 s0, s0, s38
	ds_write2_b32 v32, v34, v35 offset1:1
	s_sub_i32 s0, s0, s38
	s_waitcnt lgkmcnt(0)
	s_lshl_b32 s2, s0, 6
	s_lshl_b64 s[0:1], s[36:37], 1
	s_add_u32 s0, s18, s0
	ds_read2_b32 v[36:37], v155 offset0:33 offset1:41
	ds_read2_b32 v[38:39], v155 offset1:8
	ds_read2_b32 v[40:41], v155 offset0:66 offset1:74
	ds_read2_b32 v[42:43], v155 offset0:99 offset1:107
	ds_read2_b32 v[44:45], v155 offset0:132 offset1:140
	ds_read2_b32 v[46:47], v155 offset0:165 offset1:173
	ds_read2_b32 v[48:49], v155 offset0:198 offset1:206
	ds_read2_b32 v[50:51], v155 offset0:231 offset1:239
	s_addc_u32 s1, s19, s1
	v_lshlrev_b32_e32 v138, 1, v140
	s_waitcnt lgkmcnt(6)
	s_nop 1
	v_cvt_pk_bf16_f32 v32, v38, v36
	v_or_b32_e32 v36, s2, v156
	v_lshl_add_u64 v[52:53], s[0:1], 0, v[138:139]
	v_mad_u64_u32 v[54:55], s[0:1], s20, v36, 0
	s_ashr_i32 s0, s2, 31
	v_mul_lo_u32 v38, s21, v36
	s_mul_i32 s3, s20, s0
	v_add3_u32 v55, v55, s3, v38
	v_lshl_add_u64 v[54:55], v[54:55], 1, v[52:53]
	v_or_b32_e32 v36, s2, v157
	s_waitcnt lgkmcnt(4)
	s_nop 1
	v_cvt_pk_bf16_f32 v33, v40, v42
	s_waitcnt lgkmcnt(2)
	s_nop 1
	v_cvt_pk_bf16_f32 v34, v44, v46
	s_waitcnt lgkmcnt(0)
	s_nop 1
	v_cvt_pk_bf16_f32 v35, v48, v50
	global_store_dwordx4 v[54:55], v[32:35], off nt
	v_mul_lo_u32 v38, s21, v36
	s_nop 0
	s_nop 1
	v_cvt_pk_bf16_f32 v32, v39, v37
	v_mad_u64_u32 v[36:37], s[0:1], s20, v36, 0
	v_add3_u32 v37, v37, s3, v38
	s_nop 1
	v_cvt_pk_bf16_f32 v33, v41, v43
	s_nop 1
	v_cvt_pk_bf16_f32 v34, v45, v47
	s_nop 1
	v_cvt_pk_bf16_f32 v35, v49, v51
	v_lshl_add_u64 v[36:37], v[36:37], 1, v[52:53]
	ds_read2_b32 v[38:39], v155 offset0:16 offset1:24
	ds_read2_b32 v[40:41], v155 offset0:49 offset1:57
	ds_read2_b32 v[42:43], v155 offset0:82 offset1:90
	ds_read2_b32 v[44:45], v155 offset0:115 offset1:123
	ds_read2_b32 v[46:47], v155 offset0:148 offset1:156
	ds_read2_b32 v[48:49], v155 offset0:181 offset1:189
	ds_read2_b32 v[50:51], v155 offset0:214 offset1:222
	ds_read2_b32 v[54:55], v155 offset0:247 offset1:255
	global_store_dwordx4 v[36:37], v[32:35], off nt
	v_or_b32_e32 v36, s2, v158
	s_waitcnt lgkmcnt(6)
	s_nop 1
	v_cvt_pk_bf16_f32 v32, v38, v40
	v_mul_lo_u32 v38, s21, v36
	v_mad_u64_u32 v[36:37], s[0:1], s20, v36, 0
	v_add3_u32 v37, v37, s3, v38
	v_lshl_add_u64 v[36:37], v[36:37], 1, v[52:53]
	s_waitcnt lgkmcnt(4)
	s_nop 1
	v_cvt_pk_bf16_f32 v33, v42, v44
	s_waitcnt lgkmcnt(2)
	s_nop 1
	v_cvt_pk_bf16_f32 v34, v46, v48
	s_waitcnt lgkmcnt(0)
	s_nop 1
	v_cvt_pk_bf16_f32 v35, v50, v54
	global_store_dwordx4 v[36:37], v[32:35], off nt
	v_or_b32_e32 v36, s2, v159
	v_mul_lo_u32 v38, s21, v36
	v_mad_u64_u32 v[36:37], s[0:1], s20, v36, 0
	v_add3_u32 v37, v37, s3, v38
	v_lshl_add_u64 v[36:37], v[36:37], 1, v[52:53]
	s_nop 1
	v_cvt_pk_bf16_f32 v32, v39, v41
	s_nop 1
	v_cvt_pk_bf16_f32 v33, v43, v45
	s_nop 1
	v_cvt_pk_bf16_f32 v34, v47, v49
	s_nop 1
	v_cvt_pk_bf16_f32 v35, v51, v55
	global_store_dwordx4 v[36:37], v[32:35], off nt
	s_waitcnt lgkmcnt(0)
	s_mov_b64 s[0:1], 0

.LBB0_664:
	s_abs_i32 s0, s39
	s_mul_hi_u32 s1, s0, s56
	s_mul_i32 s1, s1, s4
	s_sub_i32 s0, s0, s1
	s_sub_i32 s1, s0, s4
	s_cmp_ge_u32 s0, s4
	s_cselect_b32 s0, s1, s0
	s_sub_i32 s1, s0, s4
	s_cmp_ge_u32 s0, s4
	s_cselect_b32 s0, s1, s0
	s_xor_b32 s0, s0, s38
	s_sub_i32 s0, s0, s38
	s_lshl_b32 s34, s0, 5
	v_add_u32_e32 v36, 0x420, v154
	s_cmpk_lt_u32 s34, 0xa00
	ds_write2_b32 v36, v32, v33 offset1:1
	v_add_u32_e32 v32, 0x428, v154
	s_cselect_b64 s[0:1], -1, 0
	s_cmpk_lt_u32 s34, 0xe00
	ds_write2_b32 v32, v34, v35 offset1:1
	s_cselect_b64 s[2:3], -1, 0
	s_waitcnt lgkmcnt(0)
	s_and_b64 s[2:3], s[2:3], exec
	ds_read2_b32 v[36:37], v155 offset0:33 offset1:41
	ds_read2_b32 v[38:39], v155 offset1:8
	ds_read2_b32 v[40:41], v155 offset0:66 offset1:74
	ds_read2_b32 v[42:43], v155 offset0:99 offset1:107
	ds_read2_b32 v[44:45], v155 offset0:132 offset1:140
	ds_read2_b32 v[46:47], v155 offset0:165 offset1:173
	ds_read2_b32 v[48:49], v155 offset0:198 offset1:206
	ds_read2_b32 v[50:51], v155 offset0:231 offset1:239
	s_cselect_b32 s2, s54, 0xfffffa00
	s_cselect_b32 s3, s31, s19
	s_cselect_b32 s35, s30, s18
	s_and_b64 s[0:1], s[0:1], exec
	s_waitcnt lgkmcnt(6)
	s_nop 1
	v_cvt_pk_bf16_f32 v32, v38, v36
	v_or_b32_e32 v36, s34, v136
	s_cselect_b32 s0, 0xfffffe00, s2
	v_mov_b32_e32 v56, s0
	v_cmp_gt_i32_e32 vcc, s52, v36
	s_cselect_b32 s1, s18, s35
	s_cselect_b32 s2, s19, s3
	v_cndmask_b32_e32 v38, v56, v165, vcc
	v_add_u32_e32 v36, v38, v36
	v_ashrrev_i32_e32 v38, 31, v36
	s_waitcnt lgkmcnt(4)
	s_nop 1
	v_cvt_pk_bf16_f32 v33, v40, v42
	v_mov_b32_e32 v57, s2
	v_mov_b32_e32 v58, s31
	v_mov_b32_e32 v59, s1
	s_waitcnt vmcnt(8)
	v_mov_b32_e32 v60, s30
	v_mul_lo_u32 v38, s20, v38
	v_mul_lo_u32 v40, s21, v36
	v_mad_u64_u32 v[54:55], s[0:1], s20, v36, 0
	v_cndmask_b32_e32 v53, v57, v58, vcc
	v_cndmask_b32_e32 v52, v59, v60, vcc
	v_add3_u32 v55, v55, v38, v40
	v_lshl_add_u64 v[52:53], v[54:55], 1, v[52:53]
	s_lshl_b64 s[0:1], s[36:37], 1
	v_lshl_add_u64 v[52:53], v[52:53], 0, s[0:1]
	v_lshlrev_b32_e32 v138, 1, v140
	v_or_b32_e32 v38, s34, v146
	v_lshl_add_u64 v[52:53], v[52:53], 0, v[138:139]
	v_cmp_gt_i32_e32 vcc, s52, v38
	s_waitcnt lgkmcnt(2)
	s_nop 1
	v_cvt_pk_bf16_f32 v34, v44, v46
	s_waitcnt lgkmcnt(0)
	s_nop 1
	v_cvt_pk_bf16_f32 v35, v48, v50
	global_store_dwordx4 v[52:53], v[32:35], off nt
	v_cndmask_b32_e32 v36, v59, v60, vcc
	s_nop 0
	s_nop 1
	v_cvt_pk_bf16_f32 v32, v39, v37
	v_cndmask_b32_e32 v39, v56, v165, vcc
	v_add_u32_e32 v38, v39, v38
	v_ashrrev_i32_e32 v39, 31, v38
	s_nop 1
	v_cvt_pk_bf16_f32 v33, v41, v43
	v_mul_lo_u32 v40, s20, v39
	v_mul_lo_u32 v41, s21, v38
	v_mad_u64_u32 v[38:39], s[2:3], s20, v38, 0
	v_cndmask_b32_e32 v37, v57, v58, vcc
	v_add3_u32 v39, v39, v40, v41
	v_lshl_add_u64 v[36:37], v[38:39], 1, v[36:37]
	v_lshl_add_u64 v[36:37], v[36:37], 0, s[0:1]
	s_nop 1
	v_cvt_pk_bf16_f32 v34, v45, v47
	s_nop 1
	v_cvt_pk_bf16_f32 v35, v49, v51
	v_lshl_add_u64 v[36:37], v[36:37], 0, v[138:139]
	ds_read2_b32 v[38:39], v155 offset0:16 offset1:24
	ds_read2_b32 v[40:41], v155 offset0:49 offset1:57
	ds_read2_b32 v[42:43], v155 offset0:82 offset1:90
	ds_read2_b32 v[44:45], v155 offset0:115 offset1:123
	ds_read2_b32 v[46:47], v155 offset0:148 offset1:156
	ds_read2_b32 v[48:49], v155 offset0:181 offset1:189
	ds_read2_b32 v[50:51], v155 offset0:214 offset1:222
	ds_read2_b32 v[52:53], v155 offset0:247 offset1:255
	global_store_dwordx4 v[36:37], v[32:35], off nt
	s_waitcnt lgkmcnt(6)
	s_nop 0
	s_nop 1
	v_cvt_pk_bf16_f32 v32, v38, v40
	v_or_b32_e32 v38, s34, v148
	v_cmp_gt_i32_e32 vcc, s52, v38
	s_waitcnt lgkmcnt(4)
	s_nop 1
	v_cvt_pk_bf16_f32 v33, v42, v44
	s_waitcnt lgkmcnt(2)
	s_nop 1
	v_cvt_pk_bf16_f32 v34, v46, v48
	s_waitcnt lgkmcnt(0)
	s_nop 1
	v_cvt_pk_bf16_f32 v35, v50, v52
	v_cndmask_b32_e32 v40, v56, v165, vcc
	v_add_u32_e32 v38, v40, v38
	v_ashrrev_i32_e32 v40, 31, v38
	v_mul_lo_u32 v40, s20, v40
	v_mul_lo_u32 v42, s21, v38
	v_mad_u64_u32 v[54:55], s[2:3], s20, v38, 0
	v_cndmask_b32_e32 v37, v57, v58, vcc
	v_cndmask_b32_e32 v36, v59, v60, vcc
	v_add3_u32 v55, v55, v40, v42
	v_lshl_add_u64 v[36:37], v[54:55], 1, v[36:37]
	v_lshl_add_u64 v[36:37], v[36:37], 0, s[0:1]
	v_or_b32_e32 v38, s34, v150
	v_lshl_add_u64 v[36:37], v[36:37], 0, v[138:139]
	v_cmp_gt_i32_e32 vcc, s52, v38
	global_store_dwordx4 v[36:37], v[32:35], off nt
	s_nop 0
	v_cndmask_b32_e32 v37, v57, v58, vcc
	s_nop 1
	v_cvt_pk_bf16_f32 v32, v39, v41
	v_cndmask_b32_e32 v39, v56, v165, vcc
	v_add_u32_e32 v38, v39, v38
	v_ashrrev_i32_e32 v39, 31, v38
	v_mul_lo_u32 v40, s20, v39
	v_mul_lo_u32 v41, s21, v38
	v_mad_u64_u32 v[38:39], s[2:3], s20, v38, 0
	v_cndmask_b32_e32 v36, v59, v60, vcc
	v_add3_u32 v39, v39, v40, v41
	v_lshl_add_u64 v[36:37], v[38:39], 1, v[36:37]
	v_lshl_add_u64 v[36:37], v[36:37], 0, s[0:1]
	v_lshl_add_u64 v[36:37], v[36:37], 0, v[138:139]
	s_nop 1
	v_cvt_pk_bf16_f32 v33, v43, v45
	s_nop 1
	v_cvt_pk_bf16_f32 v34, v47, v49
	s_nop 1
	v_cvt_pk_bf16_f32 v35, v51, v53
	global_store_dwordx4 v[36:37], v[32:35], off nt
	s_waitcnt lgkmcnt(0)

.LBB0_679:
	s_abs_i32 s0, s39
	s_mul_hi_u32 s1, s0, s56
	s_mul_i32 s1, s1, s4
	s_sub_i32 s0, s0, s1
	s_sub_i32 s1, s0, s4
	s_cmp_ge_u32 s0, s4
	s_cselect_b32 s0, s1, s0
	s_sub_i32 s1, s0, s4
	s_cmp_ge_u32 s0, s4
	s_cselect_b32 s0, s1, s0
	s_xor_b32 s0, s0, s38
	v_add_u32_e32 v36, 0x420, v154
	s_sub_i32 s0, s0, s38
	ds_write2_b32 v36, v32, v33 offset1:1
	v_add_u32_e32 v32, 0x428, v154
	s_lshl_b32 s2, s0, 5
	s_lshl_b64 s[0:1], s[28:29], 1
	ds_write2_b32 v32, v34, v35 offset1:1
	s_add_u32 s3, s18, s0
	s_waitcnt lgkmcnt(0)
	s_addc_u32 s28, s19, s1
	s_lshl_b64 s[0:1], s[36:37], 1
	s_add_u32 s0, s3, s0
	ds_read2_b32 v[36:37], v155 offset0:33 offset1:41
	ds_read2_b32 v[38:39], v155 offset1:8
	ds_read2_b32 v[40:41], v155 offset0:66 offset1:74
	ds_read2_b32 v[42:43], v155 offset0:99 offset1:107
	ds_read2_b32 v[44:45], v155 offset0:132 offset1:140
	ds_read2_b32 v[46:47], v155 offset0:165 offset1:173
	ds_read2_b32 v[48:49], v155 offset0:198 offset1:206
	ds_read2_b32 v[50:51], v155 offset0:231 offset1:239
	s_addc_u32 s1, s28, s1
	v_lshlrev_b32_e32 v138, 1, v140
	s_waitcnt lgkmcnt(6)
	s_nop 1
	v_cvt_pk_bf16_f32 v32, v38, v36
	v_or_b32_e32 v36, s2, v136
	v_lshl_add_u64 v[52:53], s[0:1], 0, v[138:139]
	v_mad_u64_u32 v[54:55], s[0:1], s26, v36, 0
	s_ashr_i32 s0, s2, 31
	v_mul_lo_u32 v38, s27, v36
	s_mul_i32 s3, s26, s0
	v_add3_u32 v55, v55, s3, v38
	v_lshl_add_u64 v[54:55], v[54:55], 1, v[52:53]
	v_or_b32_e32 v36, s2, v146
	s_waitcnt lgkmcnt(4)
	s_nop 1
	v_cvt_pk_bf16_f32 v33, v40, v42
	s_waitcnt lgkmcnt(2)
	s_nop 1
	v_cvt_pk_bf16_f32 v34, v44, v46
	s_waitcnt lgkmcnt(0)
	s_nop 1
	v_cvt_pk_bf16_f32 v35, v48, v50
	global_store_dwordx4 v[54:55], v[32:35], off nt
	v_mul_lo_u32 v38, s27, v36
	s_nop 0
	s_nop 1
	v_cvt_pk_bf16_f32 v32, v39, v37
	v_mad_u64_u32 v[36:37], s[0:1], s26, v36, 0
	v_add3_u32 v37, v37, s3, v38
	s_nop 1
	v_cvt_pk_bf16_f32 v33, v41, v43
	s_nop 1
	v_cvt_pk_bf16_f32 v34, v45, v47
	s_nop 1
	v_cvt_pk_bf16_f32 v35, v49, v51
	v_lshl_add_u64 v[36:37], v[36:37], 1, v[52:53]
	ds_read2_b32 v[38:39], v155 offset0:16 offset1:24
	ds_read2_b32 v[40:41], v155 offset0:49 offset1:57
	ds_read2_b32 v[42:43], v155 offset0:82 offset1:90
	ds_read2_b32 v[44:45], v155 offset0:115 offset1:123
	ds_read2_b32 v[46:47], v155 offset0:148 offset1:156
	ds_read2_b32 v[48:49], v155 offset0:181 offset1:189
	ds_read2_b32 v[50:51], v155 offset0:214 offset1:222
	ds_read2_b32 v[54:55], v155 offset0:247 offset1:255
	global_store_dwordx4 v[36:37], v[32:35], off nt
	v_or_b32_e32 v36, s2, v148
	s_waitcnt lgkmcnt(6)
	s_nop 1
	v_cvt_pk_bf16_f32 v32, v38, v40
	v_mul_lo_u32 v38, s27, v36
	v_mad_u64_u32 v[36:37], s[0:1], s26, v36, 0
	v_add3_u32 v37, v37, s3, v38
	v_lshl_add_u64 v[36:37], v[36:37], 1, v[52:53]
	s_waitcnt lgkmcnt(4)
	s_nop 1
	v_cvt_pk_bf16_f32 v33, v42, v44
	s_waitcnt lgkmcnt(2)
	s_nop 1
	v_cvt_pk_bf16_f32 v34, v46, v48
	s_waitcnt lgkmcnt(0)
	s_nop 1
	v_cvt_pk_bf16_f32 v35, v50, v54
	global_store_dwordx4 v[36:37], v[32:35], off nt
	v_or_b32_e32 v36, s2, v150
	v_mul_lo_u32 v38, s27, v36
	v_mad_u64_u32 v[36:37], s[0:1], s26, v36, 0
	v_add3_u32 v37, v37, s3, v38
	v_lshl_add_u64 v[36:37], v[36:37], 1, v[52:53]
	s_nop 1
	v_cvt_pk_bf16_f32 v32, v39, v41
	s_nop 1
	v_cvt_pk_bf16_f32 v33, v43, v45
	s_nop 1
	v_cvt_pk_bf16_f32 v34, v47, v49
	s_nop 1
	v_cvt_pk_bf16_f32 v35, v51, v55
	global_store_dwordx4 v[36:37], v[32:35], off nt
	s_waitcnt lgkmcnt(0)

.LBB0_702:
	s_abs_i32 s0, s39
	s_mul_hi_u32 s1, s0, s56
	s_mul_i32 s1, s1, s4
	s_sub_i32 s0, s0, s1
	v_add_u32_e32 v32, 0x420, v154
	s_sub_i32 s1, s0, s4
	ds_write2_b32 v32, v36, v37 offset1:1
	v_add_u32_e32 v32, 0x428, v154
	s_cmp_ge_u32 s0, s4
	ds_write2_b32 v32, v38, v39 offset1:1
	s_cselect_b32 s0, s1, s0
	s_sub_i32 s1, s0, s4
	s_waitcnt lgkmcnt(0)
	s_cmp_ge_u32 s0, s4
	ds_read2_b32 v[32:33], v155 offset0:33 offset1:41
	ds_read2_b32 v[34:35], v155 offset1:8
	s_cselect_b32 s0, s1, s0
	s_xor_b32 s0, s0, s38
	s_sub_i32 s0, s0, s38
	ds_read2_b32 v[38:39], v155 offset0:66 offset1:74
	ds_read2_b32 v[40:41], v155 offset0:132 offset1:140
	ds_read2_b32 v[42:43], v155 offset0:165 offset1:173
	ds_read2_b32 v[44:45], v155 offset0:99 offset1:107
	s_lshl_b32 s2, s0, 5
	v_mov_b32_e32 v36, v139
	s_waitcnt lgkmcnt(4)
	v_cvt_pk_fp8_f32 v36, v34, v32
	v_or_b32_e32 v32, s2, v136
	v_mov_b32_e32 v37, v139
	ds_read2_b32 v[46:47], v155 offset0:198 offset1:206
	ds_read2_b32 v[48:49], v155 offset0:231 offset1:239
	v_cmp_gt_i32_e32 vcc, s53, v32
	s_add_u32 s0, s18, s36
	s_waitcnt lgkmcnt(3)
	v_cvt_pk_fp8_f32 v37, v40, v42
	v_cndmask_b32_e32 v34, v166, v167, vcc
	s_addc_u32 s1, s19, s37
	v_add_u32_e32 v32, v34, v32
	v_lshl_add_u64 v[50:51], s[0:1], 0, v[140:141]
	v_ashrrev_i32_e32 v34, 31, v32
	s_waitcnt lgkmcnt(2)
	v_cvt_pk_fp8_f32 v36, v38, v44 op_sel:[0,0,1]
	v_mul_lo_u32 v34, s20, v34
	v_mul_lo_u32 v38, s21, v32
	v_mad_u64_u32 v[52:53], s[0:1], s20, v32, v[50:51]
	s_waitcnt lgkmcnt(0)
	v_cvt_pk_fp8_f32 v37, v46, v48 op_sel:[0,0,1]
	v_mov_b32_e32 v32, v139
	v_add3_u32 v53, v38, v53, v34
	v_or_b32_e32 v34, s2, v146
	v_cvt_pk_fp8_f32 v32, v35, v33
	v_mov_b32_e32 v33, v139
	v_cmp_gt_i32_e32 vcc, s53, v34
	v_cvt_pk_fp8_f32 v33, v41, v43
	global_store_dwordx2 v[52:53], v[36:37], off nt
	v_cndmask_b32_e32 v35, v166, v167, vcc
	v_add_u32_e32 v38, v35, v34
	v_ashrrev_i32_e32 v34, 31, v38
	v_mul_lo_u32 v56, s20, v34
	ds_read2_b32 v[34:35], v155 offset0:16 offset1:24
	ds_read2_b32 v[36:37], v155 offset0:49 offset1:57
	v_cvt_pk_fp8_f32 v32, v39, v45 op_sel:[0,0,1]
	v_cvt_pk_fp8_f32 v33, v47, v49 op_sel:[0,0,1]
	ds_read2_b32 v[42:43], v155 offset0:82 offset1:90
	ds_read2_b32 v[44:45], v155 offset0:148 offset1:156
	ds_read2_b32 v[46:47], v155 offset0:181 offset1:189
	ds_read2_b32 v[48:49], v155 offset0:115 offset1:123
	v_mul_lo_u32 v57, s21, v38
	v_mad_u64_u32 v[38:39], s[0:1], s20, v38, v[50:51]
	v_mov_b32_e32 v40, v139
	v_mov_b32_e32 v41, v139
	ds_read2_b32 v[52:53], v155 offset0:214 offset1:222
	ds_read2_b32 v[54:55], v155 offset0:247 offset1:255
	s_waitcnt lgkmcnt(6)
	v_cvt_pk_fp8_f32 v40, v34, v36
	s_waitcnt lgkmcnt(3)
	v_cvt_pk_fp8_f32 v41, v44, v46
	v_add3_u32 v39, v57, v39, v56
	global_store_dwordx2 v[38:39], v[32:33], off nt
	v_or_b32_e32 v32, s2, v148
	v_cmp_gt_i32_e32 vcc, s53, v32
	s_waitcnt lgkmcnt(2)
	v_cvt_pk_fp8_f32 v40, v42, v48 op_sel:[0,0,1]
	s_waitcnt lgkmcnt(0)
	v_cvt_pk_fp8_f32 v41, v52, v54 op_sel:[0,0,1]
	v_cndmask_b32_e32 v33, v166, v167, vcc
	v_add_u32_e32 v32, v33, v32
	v_ashrrev_i32_e32 v33, 31, v32
	v_mov_b32_e32 v34, v139
	v_mul_lo_u32 v36, s20, v33
	v_mul_lo_u32 v38, s21, v32
	v_mad_u64_u32 v[32:33], s[0:1], s20, v32, v[50:51]
	v_cvt_pk_fp8_f32 v34, v35, v37
	v_mov_b32_e32 v35, v139
	v_cvt_pk_fp8_f32 v35, v45, v47
	v_add3_u32 v33, v38, v33, v36
	global_store_dwordx2 v[32:33], v[40:41], off nt
	v_or_b32_e32 v32, s2, v150
	v_cmp_gt_i32_e32 vcc, s53, v32
	v_cvt_pk_fp8_f32 v34, v43, v49 op_sel:[0,0,1]
	v_cvt_pk_fp8_f32 v35, v53, v55 op_sel:[0,0,1]
	v_cndmask_b32_e32 v33, v166, v167, vcc
	v_add_u32_e32 v32, v33, v32
	v_ashrrev_i32_e32 v33, 31, v32
	v_mul_lo_u32 v36, s20, v33
	v_mul_lo_u32 v37, s21, v32
	v_mad_u64_u32 v[32:33], s[0:1], s20, v32, v[50:51]
	v_add3_u32 v33, v37, v33, v36
	global_store_dwordx2 v[32:33], v[34:35], off nt
	s_waitcnt lgkmcnt(0)
	s_mov_b64 s[0:1], 0

.LBB0_721:
	s_abs_i32 s0, s39
	s_mul_hi_u32 s1, s0, s56
	s_mul_i32 s1, s1, s4
	s_sub_i32 s0, s0, s1
	v_add_u32_e32 v32, 0x420, v154
	s_sub_i32 s1, s0, s4
	ds_write2_b32 v32, v36, v37 offset1:1
	v_add_u32_e32 v32, 0x428, v154
	s_cmp_ge_u32 s0, s4
	ds_write2_b32 v32, v38, v39 offset1:1
	s_cselect_b32 s0, s1, s0
	s_sub_i32 s1, s0, s4
	s_waitcnt lgkmcnt(0)
	s_cmp_ge_u32 s0, s4
	ds_read2_b32 v[32:33], v155 offset0:33 offset1:41
	ds_read2_b32 v[34:35], v155 offset1:8
	s_cselect_b32 s0, s1, s0
	ds_read2_b32 v[38:39], v155 offset0:66 offset1:74
	ds_read2_b32 v[40:41], v155 offset0:132 offset1:140
	ds_read2_b32 v[42:43], v155 offset0:165 offset1:173
	ds_read2_b32 v[44:45], v155 offset0:99 offset1:107
	s_xor_b32 s0, s0, s38
	s_sub_i32 s0, s0, s38
	s_lshl_b32 s0, s0, 5
	v_mov_b32_e32 v36, v139
	v_mov_b32_e32 v37, v139
	ds_read2_b32 v[46:47], v155 offset0:198 offset1:206
	ds_read2_b32 v[48:49], v155 offset0:231 offset1:239
	s_add_i32 s2, s0, 0xfffff600
	s_waitcnt lgkmcnt(6)
	v_cvt_pk_fp8_f32 v36, v34, v32
	s_waitcnt lgkmcnt(3)
	v_cvt_pk_fp8_f32 v37, v40, v42
	s_add_u32 s0, s18, s36
	s_addc_u32 s1, s19, s37
	v_lshl_add_u64 v[50:51], s[0:1], 0, v[140:141]
	v_or_b32_e32 v32, s2, v136
	s_waitcnt lgkmcnt(2)
	v_cvt_pk_fp8_f32 v36, v38, v44 op_sel:[0,0,1]
	s_waitcnt lgkmcnt(0)
	v_cvt_pk_fp8_f32 v37, v46, v48 op_sel:[0,0,1]
	v_mul_lo_u32 v34, s21, v32
	v_mad_u64_u32 v[52:53], s[0:1], s20, v32, v[50:51]
	v_mov_b32_e32 v32, v139
	s_ashr_i32 s0, s2, 31
	v_cvt_pk_fp8_f32 v32, v35, v33
	v_mov_b32_e32 v33, v139
	s_mul_i32 s3, s20, s0
	v_cvt_pk_fp8_f32 v33, v41, v43
	v_add3_u32 v53, v34, v53, s3
	global_store_dwordx2 v[52:53], v[36:37], off nt
	ds_read2_b32 v[34:35], v155 offset0:16 offset1:24
	ds_read2_b32 v[36:37], v155 offset0:49 offset1:57
	v_cvt_pk_fp8_f32 v32, v39, v45 op_sel:[0,0,1]
	v_cvt_pk_fp8_f32 v33, v47, v49 op_sel:[0,0,1]
	ds_read2_b32 v[42:43], v155 offset0:82 offset1:90
	ds_read2_b32 v[44:45], v155 offset0:148 offset1:156
	ds_read2_b32 v[46:47], v155 offset0:181 offset1:189
	ds_read2_b32 v[48:49], v155 offset0:115 offset1:123
	v_mov_b32_e32 v40, v139
	v_mov_b32_e32 v41, v139
	ds_read2_b32 v[52:53], v155 offset0:214 offset1:222
	ds_read2_b32 v[54:55], v155 offset0:247 offset1:255
	s_waitcnt lgkmcnt(6)
	v_cvt_pk_fp8_f32 v40, v34, v36
	s_waitcnt lgkmcnt(3)
	v_cvt_pk_fp8_f32 v41, v44, v46
	v_mov_b32_e32 v34, v139
	v_or_b32_e32 v38, s2, v146
	v_cvt_pk_fp8_f32 v34, v35, v37
	v_mov_b32_e32 v35, v139
	v_mul_lo_u32 v56, s21, v38
	v_mad_u64_u32 v[38:39], s[0:1], s20, v38, v[50:51]
	v_cvt_pk_fp8_f32 v35, v45, v47
	v_add3_u32 v39, v56, v39, s3
	s_waitcnt lgkmcnt(2)
	v_cvt_pk_fp8_f32 v40, v42, v48 op_sel:[0,0,1]
	s_waitcnt lgkmcnt(0)
	v_cvt_pk_fp8_f32 v41, v52, v54 op_sel:[0,0,1]
	global_store_dwordx2 v[38:39], v[32:33], off nt
	v_or_b32_e32 v32, s2, v148
	v_mul_lo_u32 v36, s21, v32
	v_mad_u64_u32 v[32:33], s[0:1], s20, v32, v[50:51]
	v_add3_u32 v33, v36, v33, s3
	v_cvt_pk_fp8_f32 v34, v43, v49 op_sel:[0,0,1]
	v_cvt_pk_fp8_f32 v35, v53, v55 op_sel:[0,0,1]
	global_store_dwordx2 v[32:33], v[40:41], off nt
	v_or_b32_e32 v32, s2, v150
	v_mul_lo_u32 v36, s21, v32
	v_mad_u64_u32 v[32:33], s[0:1], s20, v32, v[50:51]
	v_add3_u32 v33, v36, v33, s3
	global_store_dwordx2 v[32:33], v[34:35], off nt
	s_waitcnt lgkmcnt(0)

.LBB0_741:
	s_abs_i32 s0, s39
	s_mul_hi_u32 s1, s0, s56
	s_mul_i32 s1, s1, s4
	s_sub_i32 s0, s0, s1
	v_add_u32_e32 v32, 0x420, v154
	s_sub_i32 s1, s0, s4
	ds_write2_b32 v32, v36, v37 offset1:1
	v_add_u32_e32 v32, 0x428, v154
	s_cmp_ge_u32 s0, s4
	ds_write2_b32 v32, v38, v39 offset1:1
	s_cselect_b32 s0, s1, s0
	s_sub_i32 s1, s0, s4
	s_waitcnt lgkmcnt(0)
	s_cmp_ge_u32 s0, s4
	ds_read2_b32 v[32:33], v155 offset0:33 offset1:41
	ds_read2_b32 v[34:35], v155 offset1:8
	s_cselect_b32 s0, s1, s0
	ds_read2_b32 v[38:39], v155 offset0:66 offset1:74
	ds_read2_b32 v[40:41], v155 offset0:132 offset1:140
	ds_read2_b32 v[42:43], v155 offset0:165 offset1:173
	ds_read2_b32 v[44:45], v155 offset0:99 offset1:107
	s_xor_b32 s0, s0, s38
	s_sub_i32 s0, s0, s38
	s_lshl_b32 s0, s0, 5
	v_mov_b32_e32 v36, v139
	v_mov_b32_e32 v37, v139
	ds_read2_b32 v[46:47], v155 offset0:198 offset1:206
	ds_read2_b32 v[48:49], v155 offset0:231 offset1:239
	s_add_i32 s2, s0, 0xfffff000
	s_waitcnt lgkmcnt(6)
	v_cvt_pk_fp8_f32 v36, v34, v32
	s_waitcnt lgkmcnt(3)
	v_cvt_pk_fp8_f32 v37, v40, v42
	s_add_u32 s0, s18, s36
	s_addc_u32 s1, s19, s37
	v_lshl_add_u64 v[50:51], s[0:1], 0, v[140:141]
	v_or_b32_e32 v32, s2, v136
	s_waitcnt lgkmcnt(2)
	v_cvt_pk_fp8_f32 v36, v38, v44 op_sel:[0,0,1]
	s_waitcnt lgkmcnt(0)
	v_cvt_pk_fp8_f32 v37, v46, v48 op_sel:[0,0,1]
	v_mul_lo_u32 v34, s21, v32
	v_mad_u64_u32 v[52:53], s[0:1], s20, v32, v[50:51]
	v_mov_b32_e32 v32, v139
	s_ashr_i32 s0, s2, 31
	v_cvt_pk_fp8_f32 v32, v35, v33
	v_mov_b32_e32 v33, v139
	s_mul_i32 s3, s20, s0
	v_cvt_pk_fp8_f32 v33, v41, v43
	v_add3_u32 v53, v34, v53, s3
	global_store_dwordx2 v[52:53], v[36:37], off nt
	ds_read2_b32 v[34:35], v155 offset0:16 offset1:24
	ds_read2_b32 v[36:37], v155 offset0:49 offset1:57
	v_cvt_pk_fp8_f32 v32, v39, v45 op_sel:[0,0,1]
	v_cvt_pk_fp8_f32 v33, v47, v49 op_sel:[0,0,1]
	ds_read2_b32 v[42:43], v155 offset0:82 offset1:90
	ds_read2_b32 v[44:45], v155 offset0:148 offset1:156
	ds_read2_b32 v[46:47], v155 offset0:181 offset1:189
	ds_read2_b32 v[48:49], v155 offset0:115 offset1:123
	v_mov_b32_e32 v40, v139
	v_mov_b32_e32 v41, v139
	ds_read2_b32 v[52:53], v155 offset0:214 offset1:222
	ds_read2_b32 v[54:55], v155 offset0:247 offset1:255
	s_waitcnt lgkmcnt(6)
	v_cvt_pk_fp8_f32 v40, v34, v36
	s_waitcnt lgkmcnt(3)
	v_cvt_pk_fp8_f32 v41, v44, v46
	v_mov_b32_e32 v34, v139
	v_or_b32_e32 v38, s2, v146
	v_cvt_pk_fp8_f32 v34, v35, v37
	v_mov_b32_e32 v35, v139
	v_mul_lo_u32 v56, s21, v38
	v_mad_u64_u32 v[38:39], s[0:1], s20, v38, v[50:51]
	v_cvt_pk_fp8_f32 v35, v45, v47
	v_add3_u32 v39, v56, v39, s3
	s_waitcnt lgkmcnt(2)
	v_cvt_pk_fp8_f32 v40, v42, v48 op_sel:[0,0,1]
	s_waitcnt lgkmcnt(0)
	v_cvt_pk_fp8_f32 v41, v52, v54 op_sel:[0,0,1]
	global_store_dwordx2 v[38:39], v[32:33], off nt
	v_or_b32_e32 v32, s2, v148
	v_mul_lo_u32 v36, s21, v32
	v_mad_u64_u32 v[32:33], s[0:1], s20, v32, v[50:51]
	v_add3_u32 v33, v36, v33, s3
	v_cvt_pk_fp8_f32 v34, v43, v49 op_sel:[0,0,1]
	v_cvt_pk_fp8_f32 v35, v53, v55 op_sel:[0,0,1]
	global_store_dwordx2 v[32:33], v[40:41], off nt
	v_or_b32_e32 v32, s2, v150
	v_mul_lo_u32 v36, s21, v32
	v_mad_u64_u32 v[32:33], s[0:1], s20, v32, v[50:51]
	v_add3_u32 v33, v36, v33, s3
	global_store_dwordx2 v[32:33], v[34:35], off nt
	s_waitcnt lgkmcnt(0)

.LBB0_766:
	s_abs_i32 s2, s39
	s_mul_hi_u32 s3, s2, s56
	s_mul_i32 s3, s3, s4
	v_add_u32_e32 v32, 0x420, v154
	s_sub_i32 s2, s2, s3
	ds_write2_b32 v32, v36, v37 offset1:1
	v_add_u32_e32 v32, 0x428, v154
	s_sub_i32 s3, s2, s4
	ds_write2_b32 v32, v38, v39 offset1:1
	s_cmp_ge_u32 s2, s4
	s_cselect_b32 s2, s3, s2
	s_waitcnt lgkmcnt(0)
	s_sub_i32 s3, s2, s4
	ds_read2_b32 v[32:33], v155 offset0:33 offset1:41
	ds_read2_b32 v[34:35], v155 offset1:8
	s_cmp_ge_u32 s2, s4
	ds_read2_b32 v[38:39], v155 offset0:66 offset1:74
	ds_read2_b32 v[40:41], v155 offset0:132 offset1:140
	ds_read2_b32 v[42:43], v155 offset0:165 offset1:173
	ds_read2_b32 v[44:45], v155 offset0:99 offset1:107
	s_cselect_b32 s2, s3, s2
	s_xor_b32 s2, s2, s38
	s_sub_i32 s2, s2, s38
	v_mov_b32_e32 v36, v139
	v_mov_b32_e32 v37, v139
	ds_read2_b32 v[46:47], v155 offset0:198 offset1:206
	ds_read2_b32 v[48:49], v155 offset0:231 offset1:239
	s_lshl_b32 s26, s2, 6
	s_waitcnt lgkmcnt(6)
	v_cvt_pk_fp8_f32 v36, v34, v32
	s_waitcnt lgkmcnt(3)
	v_cvt_pk_fp8_f32 v37, v40, v42
	s_add_u32 s2, s18, s36
	s_addc_u32 s3, s19, s37
	v_lshl_add_u64 v[50:51], s[2:3], 0, v[140:141]
	v_or_b32_e32 v32, s26, v156
	s_waitcnt lgkmcnt(2)
	v_cvt_pk_fp8_f32 v36, v38, v44 op_sel:[0,0,1]
	s_waitcnt lgkmcnt(0)
	v_cvt_pk_fp8_f32 v37, v46, v48 op_sel:[0,0,1]
	v_mul_lo_u32 v34, s21, v32
	v_mad_u64_u32 v[52:53], s[2:3], s20, v32, v[50:51]
	v_mov_b32_e32 v32, v139
	s_ashr_i32 s2, s26, 31
	v_cvt_pk_fp8_f32 v32, v35, v33
	v_mov_b32_e32 v33, v139
	s_mul_i32 s27, s20, s2
	v_cvt_pk_fp8_f32 v33, v41, v43
	v_add3_u32 v53, v34, v53, s27
	global_store_dwordx2 v[52:53], v[36:37], off nt
	ds_read2_b32 v[34:35], v155 offset0:16 offset1:24
	ds_read2_b32 v[36:37], v155 offset0:49 offset1:57
	v_cvt_pk_fp8_f32 v32, v39, v45 op_sel:[0,0,1]
	v_cvt_pk_fp8_f32 v33, v47, v49 op_sel:[0,0,1]
	ds_read2_b32 v[42:43], v155 offset0:82 offset1:90
	ds_read2_b32 v[44:45], v155 offset0:148 offset1:156
	ds_read2_b32 v[46:47], v155 offset0:181 offset1:189
	ds_read2_b32 v[48:49], v155 offset0:115 offset1:123
	v_mov_b32_e32 v40, v139
	v_mov_b32_e32 v41, v139
	ds_read2_b32 v[52:53], v155 offset0:214 offset1:222
	ds_read2_b32 v[54:55], v155 offset0:247 offset1:255
	s_waitcnt lgkmcnt(6)
	v_cvt_pk_fp8_f32 v40, v34, v36
	s_waitcnt lgkmcnt(3)
	v_cvt_pk_fp8_f32 v41, v44, v46
	v_mov_b32_e32 v34, v139
	v_or_b32_e32 v38, s26, v157
	v_cvt_pk_fp8_f32 v34, v35, v37
	v_mov_b32_e32 v35, v139
	v_mul_lo_u32 v56, s21, v38
	v_mad_u64_u32 v[38:39], s[2:3], s20, v38, v[50:51]
	v_cvt_pk_fp8_f32 v35, v45, v47
	v_add3_u32 v39, v56, v39, s27
	s_waitcnt lgkmcnt(2)
	v_cvt_pk_fp8_f32 v40, v42, v48 op_sel:[0,0,1]
	s_waitcnt lgkmcnt(0)
	v_cvt_pk_fp8_f32 v41, v52, v54 op_sel:[0,0,1]
	global_store_dwordx2 v[38:39], v[32:33], off nt
	v_or_b32_e32 v32, s26, v158
	v_mul_lo_u32 v36, s21, v32
	v_mad_u64_u32 v[32:33], s[2:3], s20, v32, v[50:51]
	v_add3_u32 v33, v36, v33, s27
	v_cvt_pk_fp8_f32 v34, v43, v49 op_sel:[0,0,1]
	v_cvt_pk_fp8_f32 v35, v53, v55 op_sel:[0,0,1]
	global_store_dwordx2 v[32:33], v[40:41], off nt
	v_or_b32_e32 v32, s26, v159
	v_mul_lo_u32 v36, s21, v32
	v_mad_u64_u32 v[32:33], s[2:3], s20, v32, v[50:51]
	v_add3_u32 v33, v36, v33, s27
	global_store_dwordx2 v[32:33], v[34:35], off nt
	s_waitcnt lgkmcnt(0)
	s_mov_b64 s[2:3], 0

.LBB0_786:
	s_abs_i32 s0, s39
	s_mul_hi_u32 s1, s0, s56
	s_mul_i32 s1, s1, s4
	v_add_u32_e32 v32, 0x420, v154
	s_sub_i32 s0, s0, s1
	ds_write2_b32 v32, v36, v37 offset1:1
	v_add_u32_e32 v32, 0x428, v154
	s_sub_i32 s1, s0, s4
	ds_write2_b32 v32, v38, v39 offset1:1
	s_cmp_ge_u32 s0, s4
	s_cselect_b32 s0, s1, s0
	s_waitcnt lgkmcnt(0)
	s_sub_i32 s1, s0, s4
	ds_read2_b32 v[32:33], v155 offset0:33 offset1:41
	ds_read2_b32 v[34:35], v155 offset1:8
	s_cmp_ge_u32 s0, s4
	ds_read2_b32 v[38:39], v155 offset0:66 offset1:74
	ds_read2_b32 v[40:41], v155 offset0:132 offset1:140
	ds_read2_b32 v[42:43], v155 offset0:165 offset1:173
	ds_read2_b32 v[44:45], v155 offset0:99 offset1:107
	s_cselect_b32 s0, s1, s0
	s_xor_b32 s0, s0, s38
	s_sub_i32 s0, s0, s38
	v_mov_b32_e32 v36, v139
	v_mov_b32_e32 v37, v139
	ds_read2_b32 v[46:47], v155 offset0:198 offset1:206
	ds_read2_b32 v[48:49], v155 offset0:231 offset1:239
	s_lshl_b32 s26, s0, 6
	s_waitcnt lgkmcnt(6)
	v_cvt_pk_fp8_f32 v36, v34, v32
	s_waitcnt lgkmcnt(3)
	v_cvt_pk_fp8_f32 v37, v40, v42
	s_add_u32 s0, s18, s36
	s_addc_u32 s1, s19, s37
	v_lshl_add_u64 v[50:51], s[0:1], 0, v[140:141]
	v_or_b32_e32 v32, s26, v160
	s_waitcnt lgkmcnt(2)
	v_cvt_pk_fp8_f32 v36, v38, v44 op_sel:[0,0,1]
	s_waitcnt lgkmcnt(0)
	v_cvt_pk_fp8_f32 v37, v46, v48 op_sel:[0,0,1]
	v_mul_lo_u32 v34, s21, v32
	v_mad_u64_u32 v[52:53], s[0:1], s20, v32, v[50:51]
	v_mov_b32_e32 v32, v139
	s_ashr_i32 s0, s26, 31
	v_cvt_pk_fp8_f32 v32, v35, v33
	v_mov_b32_e32 v33, v139
	s_mul_i32 s27, s20, s0
	v_cvt_pk_fp8_f32 v33, v41, v43
	v_add3_u32 v53, v34, v53, s27
	global_store_dwordx2 v[52:53], v[36:37], off nt
	ds_read2_b32 v[34:35], v155 offset0:16 offset1:24
	ds_read2_b32 v[36:37], v155 offset0:49 offset1:57
	v_cvt_pk_fp8_f32 v32, v39, v45 op_sel:[0,0,1]
	v_cvt_pk_fp8_f32 v33, v47, v49 op_sel:[0,0,1]
	ds_read2_b32 v[42:43], v155 offset0:82 offset1:90
	ds_read2_b32 v[44:45], v155 offset0:148 offset1:156
	ds_read2_b32 v[46:47], v155 offset0:181 offset1:189
	ds_read2_b32 v[48:49], v155 offset0:115 offset1:123
	v_mov_b32_e32 v40, v139
	v_mov_b32_e32 v41, v139
	ds_read2_b32 v[52:53], v155 offset0:214 offset1:222
	ds_read2_b32 v[54:55], v155 offset0:247 offset1:255
	s_waitcnt lgkmcnt(6)
	v_cvt_pk_fp8_f32 v40, v34, v36
	s_waitcnt lgkmcnt(3)
	v_cvt_pk_fp8_f32 v41, v44, v46
	v_mov_b32_e32 v34, v139
	v_or_b32_e32 v38, s26, v161
	v_cvt_pk_fp8_f32 v34, v35, v37
	v_mov_b32_e32 v35, v139
	v_mul_lo_u32 v56, s21, v38
	v_mad_u64_u32 v[38:39], s[0:1], s20, v38, v[50:51]
	v_cvt_pk_fp8_f32 v35, v45, v47
	v_add3_u32 v39, v56, v39, s27
	s_waitcnt lgkmcnt(2)
	v_cvt_pk_fp8_f32 v40, v42, v48 op_sel:[0,0,1]
	s_waitcnt lgkmcnt(0)
	v_cvt_pk_fp8_f32 v41, v52, v54 op_sel:[0,0,1]
	global_store_dwordx2 v[38:39], v[32:33], off nt
	v_or_b32_e32 v32, s26, v162
	v_mul_lo_u32 v36, s21, v32
	v_mad_u64_u32 v[32:33], s[0:1], s20, v32, v[50:51]
	v_add3_u32 v33, v36, v33, s27
	v_cvt_pk_fp8_f32 v34, v43, v49 op_sel:[0,0,1]
	v_cvt_pk_fp8_f32 v35, v53, v55 op_sel:[0,0,1]
	global_store_dwordx2 v[32:33], v[40:41], off nt
	v_or_b32_e32 v32, s26, v163
	v_mul_lo_u32 v36, s21, v32
	v_mad_u64_u32 v[32:33], s[0:1], s20, v32, v[50:51]
	v_add3_u32 v33, v36, v33, s27
	global_store_dwordx2 v[32:33], v[34:35], off nt
	s_waitcnt lgkmcnt(0)
	s_branch .LBB0_17
